# gemm_accumulators_no_zeroing_first_k_iteration_uses_srcC_0
# speedup vs baseline: 1.0138x; 1.0138x over previous
.LBB0_251:
	s_mov_b64 s[26:27], 0
	s_add_u32 s0, s0, s26
	s_addc_u32 s1, s1, s27
	s_add_u32 s4, s4, s26
	s_addc_u32 s5, s5, s27
	s_mov_b32 s25, 16
	s_cmp_lt_i32 s25, 1
	s_cbranch_scc1 .LBB0_267
	s_ashr_i32 s23, s22, 31
	s_lshl_b64 s[26:27], s[22:23], 19
	s_add_u32 s23, s30, s26
	s_addc_u32 s59, s31, s27
	s_ashr_i32 s21, s20, 31
	s_lshl_b64 s[26:27], s[20:21], 19
	s_add_u32 s21, s37, s26
	s_addc_u32 s60, s38, s27
	s_mov_b32 s61, 2
	s_mov_b64 s[26:27], 0x40080
	s_mov_b32 s100, 1
.LBB0_253:
	v_add_u32_e32 v133, 0x10000, v131
	ds_read_b128 v[136:139], v133
	ds_read_b128 v[140:143], v133 offset:1024
	ds_read_b128 v[144:147], v133 offset:2048
	ds_read_b128 v[148:151], v133 offset:3072
	v_add_u32_e32 v133, 0x14000, v131
	ds_read_b128 v[152:155], v133
	ds_read_b128 v[156:159], v133 offset:1024
	ds_read_b128 v[160:163], v133 offset:2048
	ds_read_b128 v[164:167], v133 offset:3072
	s_cmp_eq_u32 s25, s61
	s_cselect_b64 s[66:67], -1, 0
	v_lshl_add_u64 v[192:193], s[0:1], 0, v[194:195]
	s_mov_b32 m0, s56
	v_lshl_add_u64 v[192:193], v[192:193], 0, s[26:27]
	v_mov_b32_e32 v133, v195
	ds_read_b128 v[168:171], v135
	ds_read_b128 v[172:175], v135 offset:1024
	ds_read_b128 v[176:179], v135 offset:2048
	ds_read_b128 v[180:183], v135 offset:3072
	ds_read_b128 v[184:187], v135 offset:4096
	ds_read_b128 v[188:191], v135 offset:5120
	ds_read_b128 v[196:199], v135 offset:6144
	ds_read_b128 v[200:203], v135 offset:7168
	global_load_lds_dwordx4 v[192:193], off
	v_lshl_add_u64 v[192:193], s[0:1], 0, v[132:133]
	v_lshl_add_u64 v[192:193], v[192:193], 0, s[26:27]
	s_mov_b32 m0, s57
	s_nop 0
	global_load_lds_dwordx4 v[192:193], off
	s_cmp_lg_u32 s100, 0
	s_waitcnt vmcnt(8)
	s_waitcnt lgkmcnt(0)
	s_barrier
	s_setprio 1
	s_waitcnt lgkmcnt(0)
	s_cbranch_scc1 .Lcz1_253
	v_mfma_f32_16x16x32_bf16 v[126:129], v[136:139], v[168:171], v[126:129]
	v_mfma_f32_16x16x32_bf16 v[122:125], v[144:147], v[168:171], v[122:125]
	v_mfma_f32_16x16x32_bf16 v[114:117], v[136:139], v[176:179], v[114:117]
	v_mfma_f32_16x16x32_bf16 v[110:113], v[144:147], v[176:179], v[110:113]
	v_mfma_f32_16x16x32_bf16 v[94:97], v[136:139], v[184:187], v[94:97]
	v_mfma_f32_16x16x32_bf16 v[90:93], v[144:147], v[184:187], v[90:93]
	v_mfma_f32_16x16x32_bf16 v[78:81], v[136:139], v[196:199], v[78:81]
	v_mfma_f32_16x16x32_bf16 v[74:77], v[144:147], v[196:199], v[74:77]
	v_mfma_f32_16x16x32_bf16 v[126:129], v[140:143], v[172:175], v[126:129]
	v_mfma_f32_16x16x32_bf16 v[122:125], v[148:151], v[172:175], v[122:125]
	v_mfma_f32_16x16x32_bf16 v[114:117], v[140:143], v[180:183], v[114:117]
	v_mfma_f32_16x16x32_bf16 v[110:113], v[148:151], v[180:183], v[110:113]
	v_mfma_f32_16x16x32_bf16 v[94:97], v[140:143], v[188:191], v[94:97]
	v_mfma_f32_16x16x32_bf16 v[90:93], v[148:151], v[188:191], v[90:93]
	v_mfma_f32_16x16x32_bf16 v[78:81], v[140:143], v[200:203], v[78:81]
	v_mfma_f32_16x16x32_bf16 v[74:77], v[148:151], v[200:203], v[74:77]
	s_setprio 0
	s_setprio 1
	v_mfma_f32_16x16x32_bf16 v[106:109], v[152:155], v[168:171], v[106:109]
	v_mfma_f32_16x16x32_bf16 v[118:121], v[160:163], v[168:171], v[118:121]
	v_mfma_f32_16x16x32_bf16 v[102:105], v[152:155], v[176:179], v[102:105]
	v_mfma_f32_16x16x32_bf16 v[98:101], v[160:163], v[176:179], v[98:101]
	v_mfma_f32_16x16x32_bf16 v[86:89], v[152:155], v[184:187], v[86:89]
	v_mfma_f32_16x16x32_bf16 v[82:85], v[160:163], v[184:187], v[82:85]
	v_mfma_f32_16x16x32_bf16 v[70:73], v[152:155], v[196:199], v[70:73]
	v_mfma_f32_16x16x32_bf16 v[66:69], v[160:163], v[196:199], v[66:69]
	v_mfma_f32_16x16x32_bf16 v[106:109], v[156:159], v[172:175], v[106:109]
	v_mfma_f32_16x16x32_bf16 v[118:121], v[164:167], v[172:175], v[118:121]
	v_mfma_f32_16x16x32_bf16 v[102:105], v[156:159], v[180:183], v[102:105]
	v_mfma_f32_16x16x32_bf16 v[98:101], v[164:167], v[180:183], v[98:101]
	v_mfma_f32_16x16x32_bf16 v[86:89], v[156:159], v[188:191], v[86:89]
	v_mfma_f32_16x16x32_bf16 v[82:85], v[164:167], v[188:191], v[82:85]
	v_mfma_f32_16x16x32_bf16 v[70:73], v[156:159], v[200:203], v[70:73]
	v_mfma_f32_16x16x32_bf16 v[66:69], v[164:167], v[200:203], v[66:69]
.Lcj1_253:
	s_setprio 0
	s_barrier
	s_and_b64 s[68:69], s[66:67], exec
	s_cselect_b32 s62, 0, s61
	s_and_b64 s[66:67], s[2:3], s[66:67]
	s_and_b64 s[66:67], s[66:67], exec
	s_cselect_b32 s5, s60, s5
	s_cselect_b32 s4, s21, s4
	s_cselect_b32 s1, s59, s1
	s_cselect_b32 s0, s23, s0
	s_lshl_b64 s[66:67], s[62:63], 7
	s_add_u32 s68, s4, s66
	s_addc_u32 s69, s5, s67
	s_mov_b32 m0, s41
	s_add_u32 s72, s4, 0x40000
	ds_read_b128 v[168:171], v135 offset:16384
	ds_read_b128 v[172:175], v135 offset:17408
	ds_read_b128 v[176:179], v135 offset:18432
	ds_read_b128 v[180:183], v135 offset:19456
	ds_read_b128 v[184:187], v135 offset:20480
	ds_read_b128 v[188:191], v135 offset:21504
	ds_read_b128 v[196:199], v135 offset:22528
	ds_read_b128 v[200:203], v135 offset:23552
	global_load_lds_dwordx4 v130, s[68:69]
	s_mov_b32 m0, s42
	s_addc_u32 s73, s5, 0
	global_load_lds_dwordx4 v134, s[68:69]
	s_add_u32 s68, s72, s66
	s_addc_u32 s69, s73, s67
	s_mov_b32 m0, s43
	s_add_u32 s66, s0, s66
	global_load_lds_dwordx4 v130, s[68:69]
	s_mov_b32 m0, s44
	s_addc_u32 s67, s1, s67
	global_load_lds_dwordx4 v134, s[68:69]
	s_mov_b32 m0, s40
	s_nop 0
	global_load_lds_dwordx4 v194, s[66:67]
	s_mov_b32 m0, s45
	s_nop 0
	global_load_lds_dwordx4 v132, s[66:67]
	s_cmp_lg_u32 s100, 0
	s_waitcnt vmcnt(8)
	s_waitcnt lgkmcnt(0)
	s_barrier
	s_setprio 1
	s_waitcnt lgkmcnt(0)
	s_cbranch_scc1 .Lcz2_253
	v_mfma_f32_16x16x32_bf16 v[62:65], v[136:139], v[168:171], v[62:65]
	v_mfma_f32_16x16x32_bf16 v[58:61], v[144:147], v[168:171], v[58:61]
	v_mfma_f32_16x16x32_bf16 v[46:49], v[136:139], v[176:179], v[46:49]
	v_mfma_f32_16x16x32_bf16 v[42:45], v[144:147], v[176:179], v[42:45]
	v_mfma_f32_16x16x32_bf16 v[30:33], v[136:139], v[184:187], v[30:33]
	v_mfma_f32_16x16x32_bf16 v[26:29], v[144:147], v[184:187], v[26:29]
	v_mfma_f32_16x16x32_bf16 v[14:17], v[136:139], v[196:199], v[14:17]
	v_mfma_f32_16x16x32_bf16 v[10:13], v[144:147], v[196:199], v[10:13]
	v_mfma_f32_16x16x32_bf16 v[62:65], v[140:143], v[172:175], v[62:65]
	v_mfma_f32_16x16x32_bf16 v[58:61], v[148:151], v[172:175], v[58:61]
	v_mfma_f32_16x16x32_bf16 v[46:49], v[140:143], v[180:183], v[46:49]
	v_mfma_f32_16x16x32_bf16 v[42:45], v[148:151], v[180:183], v[42:45]
	v_mfma_f32_16x16x32_bf16 v[30:33], v[140:143], v[188:191], v[30:33]
	v_mfma_f32_16x16x32_bf16 v[26:29], v[148:151], v[188:191], v[26:29]
	v_mfma_f32_16x16x32_bf16 v[14:17], v[140:143], v[200:203], v[14:17]
	v_mfma_f32_16x16x32_bf16 v[10:13], v[148:151], v[200:203], v[10:13]
	s_setprio 0
	s_setprio 1
	v_mfma_f32_16x16x32_bf16 v[54:57], v[152:155], v[168:171], v[54:57]
	v_mfma_f32_16x16x32_bf16 v[50:53], v[160:163], v[168:171], v[50:53]
	v_mfma_f32_16x16x32_bf16 v[38:41], v[152:155], v[176:179], v[38:41]
	v_mfma_f32_16x16x32_bf16 v[34:37], v[160:163], v[176:179], v[34:37]
	v_mfma_f32_16x16x32_bf16 v[22:25], v[152:155], v[184:187], v[22:25]
	v_mfma_f32_16x16x32_bf16 v[18:21], v[160:163], v[184:187], v[18:21]
	v_mfma_f32_16x16x32_bf16 v[6:9], v[152:155], v[196:199], v[6:9]
	v_mfma_f32_16x16x32_bf16 v[2:5], v[160:163], v[196:199], v[2:5]
	v_mfma_f32_16x16x32_bf16 v[54:57], v[156:159], v[172:175], v[54:57]
	v_mfma_f32_16x16x32_bf16 v[50:53], v[164:167], v[172:175], v[50:53]
	v_mfma_f32_16x16x32_bf16 v[38:41], v[156:159], v[180:183], v[38:41]
	v_mfma_f32_16x16x32_bf16 v[34:37], v[164:167], v[180:183], v[34:37]
	v_mfma_f32_16x16x32_bf16 v[22:25], v[156:159], v[188:191], v[22:25]
	v_mfma_f32_16x16x32_bf16 v[18:21], v[164:167], v[188:191], v[18:21]
	v_mfma_f32_16x16x32_bf16 v[6:9], v[156:159], v[200:203], v[6:9]
	v_mfma_f32_16x16x32_bf16 v[2:5], v[164:167], v[200:203], v[2:5]
.Lcj2_253:
	s_setprio 0
	s_barrier
	v_add_u32_e32 v133, 0x18000, v131
	ds_read_b128 v[136:139], v133
	ds_read_b128 v[140:143], v133 offset:1024
	ds_read_b128 v[144:147], v133 offset:2048
	ds_read_b128 v[148:151], v133 offset:3072
	v_add_u32_e32 v133, 0x1c000, v131
	ds_read_b128 v[152:155], v133
	ds_read_b128 v[156:159], v133 offset:1024
	ds_read_b128 v[160:163], v133 offset:2048
	ds_read_b128 v[164:167], v133 offset:3072
	s_add_u32 s66, s66, 0x40000
	s_addc_u32 s67, s67, 0
	s_mov_b32 m0, s46
	ds_read_b128 v[168:171], v135 offset:32768
	ds_read_b128 v[172:175], v135 offset:33792
	ds_read_b128 v[176:179], v135 offset:34816
	ds_read_b128 v[180:183], v135 offset:35840
	ds_read_b128 v[184:187], v135 offset:36864
	ds_read_b128 v[188:191], v135 offset:37888
	ds_read_b128 v[196:199], v135 offset:38912
	ds_read_b128 v[200:203], v135 offset:39936
	global_load_lds_dwordx4 v194, s[66:67]
	s_mov_b32 m0, s47
	s_nop 0
	global_load_lds_dwordx4 v132, s[66:67]
	s_waitcnt vmcnt(8)
	s_waitcnt lgkmcnt(0)
	s_barrier
	s_setprio 1
	s_waitcnt lgkmcnt(0)
	v_mfma_f32_16x16x32_bf16 v[126:129], v[136:139], v[168:171], v[126:129]
	v_mfma_f32_16x16x32_bf16 v[122:125], v[144:147], v[168:171], v[122:125]
	v_mfma_f32_16x16x32_bf16 v[114:117], v[136:139], v[176:179], v[114:117]
	v_mfma_f32_16x16x32_bf16 v[110:113], v[144:147], v[176:179], v[110:113]
	v_mfma_f32_16x16x32_bf16 v[94:97], v[136:139], v[184:187], v[94:97]
	v_mfma_f32_16x16x32_bf16 v[90:93], v[144:147], v[184:187], v[90:93]
	v_mfma_f32_16x16x32_bf16 v[78:81], v[136:139], v[196:199], v[78:81]
	v_mfma_f32_16x16x32_bf16 v[74:77], v[144:147], v[196:199], v[74:77]
	v_mfma_f32_16x16x32_bf16 v[126:129], v[140:143], v[172:175], v[126:129]
	v_mfma_f32_16x16x32_bf16 v[122:125], v[148:151], v[172:175], v[122:125]
	v_mfma_f32_16x16x32_bf16 v[114:117], v[140:143], v[180:183], v[114:117]
	v_mfma_f32_16x16x32_bf16 v[110:113], v[148:151], v[180:183], v[110:113]
	v_mfma_f32_16x16x32_bf16 v[94:97], v[140:143], v[188:191], v[94:97]
	v_mfma_f32_16x16x32_bf16 v[90:93], v[148:151], v[188:191], v[90:93]
	v_mfma_f32_16x16x32_bf16 v[78:81], v[140:143], v[200:203], v[78:81]
	v_mfma_f32_16x16x32_bf16 v[74:77], v[148:151], v[200:203], v[74:77]
	s_setprio 0
	s_setprio 1
	v_mfma_f32_16x16x32_bf16 v[106:109], v[152:155], v[168:171], v[106:109]
	v_mfma_f32_16x16x32_bf16 v[118:121], v[160:163], v[168:171], v[118:121]
	v_mfma_f32_16x16x32_bf16 v[102:105], v[152:155], v[176:179], v[102:105]
	v_mfma_f32_16x16x32_bf16 v[98:101], v[160:163], v[176:179], v[98:101]
	v_mfma_f32_16x16x32_bf16 v[86:89], v[152:155], v[184:187], v[86:89]
	v_mfma_f32_16x16x32_bf16 v[82:85], v[160:163], v[184:187], v[82:85]
	v_mfma_f32_16x16x32_bf16 v[70:73], v[152:155], v[196:199], v[70:73]
	v_mfma_f32_16x16x32_bf16 v[66:69], v[160:163], v[196:199], v[66:69]
	v_mfma_f32_16x16x32_bf16 v[106:109], v[156:159], v[172:175], v[106:109]
	v_mfma_f32_16x16x32_bf16 v[118:121], v[164:167], v[172:175], v[118:121]
	v_mfma_f32_16x16x32_bf16 v[102:105], v[156:159], v[180:183], v[102:105]
	v_mfma_f32_16x16x32_bf16 v[98:101], v[164:167], v[180:183], v[98:101]
	v_mfma_f32_16x16x32_bf16 v[86:89], v[156:159], v[188:191], v[86:89]
	v_mfma_f32_16x16x32_bf16 v[82:85], v[164:167], v[188:191], v[82:85]
	v_mfma_f32_16x16x32_bf16 v[70:73], v[156:159], v[200:203], v[70:73]
	v_mfma_f32_16x16x32_bf16 v[66:69], v[164:167], v[200:203], v[66:69]
	s_setprio 0
	s_barrier
	s_or_b32 s62, s62, 1
	s_lshl_b64 s[66:67], s[62:63], 7
	s_add_u32 s68, s4, s66
	s_mov_b32 m0, s48
	s_addc_u32 s69, s5, s67
	ds_read_b128 v[168:171], v135 offset:49152
	ds_read_b128 v[172:175], v135 offset:50176
	ds_read_b128 v[176:179], v135 offset:51200
	ds_read_b128 v[180:183], v135 offset:52224
	ds_read_b128 v[184:187], v135 offset:53248
	ds_read_b128 v[188:191], v135 offset:54272
	ds_read_b128 v[196:199], v135 offset:55296
	ds_read_b128 v[200:203], v135 offset:56320
	global_load_lds_dwordx4 v130, s[68:69]
	s_mov_b32 m0, s49
	s_nop 0
	global_load_lds_dwordx4 v134, s[68:69]
	s_add_u32 s68, s72, s66
	s_addc_u32 s69, s73, s67
	s_mov_b32 m0, s52
	s_add_u32 s66, s0, s66
	global_load_lds_dwordx4 v130, s[68:69]
	s_mov_b32 m0, s53
	s_addc_u32 s67, s1, s67
	global_load_lds_dwordx4 v134, s[68:69]
	s_mov_b32 m0, s50
	s_nop 0
	global_load_lds_dwordx4 v194, s[66:67]
	s_mov_b32 m0, s51
	s_nop 0
	global_load_lds_dwordx4 v132, s[66:67]
	s_waitcnt vmcnt(8)
	s_waitcnt lgkmcnt(0)
	s_barrier
	s_setprio 1
	s_waitcnt lgkmcnt(0)
	v_mfma_f32_16x16x32_bf16 v[62:65], v[136:139], v[168:171], v[62:65]
	v_mfma_f32_16x16x32_bf16 v[58:61], v[144:147], v[168:171], v[58:61]
	v_mfma_f32_16x16x32_bf16 v[46:49], v[136:139], v[176:179], v[46:49]
	v_mfma_f32_16x16x32_bf16 v[42:45], v[144:147], v[176:179], v[42:45]
	v_mfma_f32_16x16x32_bf16 v[30:33], v[136:139], v[184:187], v[30:33]
	v_mfma_f32_16x16x32_bf16 v[26:29], v[144:147], v[184:187], v[26:29]
	v_mfma_f32_16x16x32_bf16 v[14:17], v[136:139], v[196:199], v[14:17]
	v_mfma_f32_16x16x32_bf16 v[10:13], v[144:147], v[196:199], v[10:13]
	v_mfma_f32_16x16x32_bf16 v[62:65], v[140:143], v[172:175], v[62:65]
	v_mfma_f32_16x16x32_bf16 v[58:61], v[148:151], v[172:175], v[58:61]
	v_mfma_f32_16x16x32_bf16 v[46:49], v[140:143], v[180:183], v[46:49]
	v_mfma_f32_16x16x32_bf16 v[42:45], v[148:151], v[180:183], v[42:45]
	v_mfma_f32_16x16x32_bf16 v[30:33], v[140:143], v[188:191], v[30:33]
	v_mfma_f32_16x16x32_bf16 v[26:29], v[148:151], v[188:191], v[26:29]
	v_mfma_f32_16x16x32_bf16 v[14:17], v[140:143], v[200:203], v[14:17]
	v_mfma_f32_16x16x32_bf16 v[10:13], v[148:151], v[200:203], v[10:13]
	s_setprio 0
	s_setprio 1
	v_mfma_f32_16x16x32_bf16 v[54:57], v[152:155], v[168:171], v[54:57]
	v_mfma_f32_16x16x32_bf16 v[50:53], v[160:163], v[168:171], v[50:53]
	v_mfma_f32_16x16x32_bf16 v[38:41], v[152:155], v[176:179], v[38:41]
	v_mfma_f32_16x16x32_bf16 v[34:37], v[160:163], v[176:179], v[34:37]
	v_mfma_f32_16x16x32_bf16 v[22:25], v[152:155], v[184:187], v[22:25]
	v_mfma_f32_16x16x32_bf16 v[18:21], v[160:163], v[184:187], v[18:21]
	v_mfma_f32_16x16x32_bf16 v[6:9], v[152:155], v[196:199], v[6:9]
	v_mfma_f32_16x16x32_bf16 v[2:5], v[160:163], v[196:199], v[2:5]
	v_mfma_f32_16x16x32_bf16 v[54:57], v[156:159], v[172:175], v[54:57]
	v_mfma_f32_16x16x32_bf16 v[50:53], v[164:167], v[172:175], v[50:53]
	v_mfma_f32_16x16x32_bf16 v[38:41], v[156:159], v[180:183], v[38:41]
	v_mfma_f32_16x16x32_bf16 v[34:37], v[164:167], v[180:183], v[34:37]
	v_mfma_f32_16x16x32_bf16 v[22:25], v[156:159], v[188:191], v[22:25]
	v_mfma_f32_16x16x32_bf16 v[18:21], v[164:167], v[188:191], v[18:21]
	v_mfma_f32_16x16x32_bf16 v[6:9], v[156:159], v[200:203], v[6:9]
	v_mfma_f32_16x16x32_bf16 v[2:5], v[164:167], v[200:203], v[2:5]
	s_setprio 0
	s_barrier
	s_add_i32 s62, s61, 2
	s_add_u32 s26, s26, 0x100
	s_addc_u32 s27, s27, 0
	s_cmp_ge_i32 s61, s25
	s_mov_b32 s61, s62
	s_cbranch_scc0 .LBB0_253
	s_branch .Lcsk_253
.Lcz1_253:
	v_mfma_f32_16x16x32_bf16 v[126:129], v[136:139], v[168:171], 0
	v_mfma_f32_16x16x32_bf16 v[122:125], v[144:147], v[168:171], 0
	v_mfma_f32_16x16x32_bf16 v[114:117], v[136:139], v[176:179], 0
	v_mfma_f32_16x16x32_bf16 v[110:113], v[144:147], v[176:179], 0
	v_mfma_f32_16x16x32_bf16 v[94:97], v[136:139], v[184:187], 0
	v_mfma_f32_16x16x32_bf16 v[90:93], v[144:147], v[184:187], 0
	v_mfma_f32_16x16x32_bf16 v[78:81], v[136:139], v[196:199], 0
	v_mfma_f32_16x16x32_bf16 v[74:77], v[144:147], v[196:199], 0
	v_mfma_f32_16x16x32_bf16 v[126:129], v[140:143], v[172:175], v[126:129]
	v_mfma_f32_16x16x32_bf16 v[122:125], v[148:151], v[172:175], v[122:125]
	v_mfma_f32_16x16x32_bf16 v[114:117], v[140:143], v[180:183], v[114:117]
	v_mfma_f32_16x16x32_bf16 v[110:113], v[148:151], v[180:183], v[110:113]
	v_mfma_f32_16x16x32_bf16 v[94:97], v[140:143], v[188:191], v[94:97]
	v_mfma_f32_16x16x32_bf16 v[90:93], v[148:151], v[188:191], v[90:93]
	v_mfma_f32_16x16x32_bf16 v[78:81], v[140:143], v[200:203], v[78:81]
	v_mfma_f32_16x16x32_bf16 v[74:77], v[148:151], v[200:203], v[74:77]
	s_setprio 0
	s_setprio 1
	v_mfma_f32_16x16x32_bf16 v[106:109], v[152:155], v[168:171], 0
	v_mfma_f32_16x16x32_bf16 v[118:121], v[160:163], v[168:171], 0
	v_mfma_f32_16x16x32_bf16 v[102:105], v[152:155], v[176:179], 0
	v_mfma_f32_16x16x32_bf16 v[98:101], v[160:163], v[176:179], 0
	v_mfma_f32_16x16x32_bf16 v[86:89], v[152:155], v[184:187], 0
	v_mfma_f32_16x16x32_bf16 v[82:85], v[160:163], v[184:187], 0
	v_mfma_f32_16x16x32_bf16 v[70:73], v[152:155], v[196:199], 0
	v_mfma_f32_16x16x32_bf16 v[66:69], v[160:163], v[196:199], 0
	v_mfma_f32_16x16x32_bf16 v[106:109], v[156:159], v[172:175], v[106:109]
	v_mfma_f32_16x16x32_bf16 v[118:121], v[164:167], v[172:175], v[118:121]
	v_mfma_f32_16x16x32_bf16 v[102:105], v[156:159], v[180:183], v[102:105]
	v_mfma_f32_16x16x32_bf16 v[98:101], v[164:167], v[180:183], v[98:101]
	v_mfma_f32_16x16x32_bf16 v[86:89], v[156:159], v[188:191], v[86:89]
	v_mfma_f32_16x16x32_bf16 v[82:85], v[164:167], v[188:191], v[82:85]
	v_mfma_f32_16x16x32_bf16 v[70:73], v[156:159], v[200:203], v[70:73]
	v_mfma_f32_16x16x32_bf16 v[66:69], v[164:167], v[200:203], v[66:69]
	s_branch .Lcj1_253
.Lcz2_253:
	v_mfma_f32_16x16x32_bf16 v[62:65], v[136:139], v[168:171], 0
	v_mfma_f32_16x16x32_bf16 v[58:61], v[144:147], v[168:171], 0
	v_mfma_f32_16x16x32_bf16 v[46:49], v[136:139], v[176:179], 0
	v_mfma_f32_16x16x32_bf16 v[42:45], v[144:147], v[176:179], 0
	v_mfma_f32_16x16x32_bf16 v[30:33], v[136:139], v[184:187], 0
	v_mfma_f32_16x16x32_bf16 v[26:29], v[144:147], v[184:187], 0
	v_mfma_f32_16x16x32_bf16 v[14:17], v[136:139], v[196:199], 0
	v_mfma_f32_16x16x32_bf16 v[10:13], v[144:147], v[196:199], 0
	v_mfma_f32_16x16x32_bf16 v[62:65], v[140:143], v[172:175], v[62:65]
	v_mfma_f32_16x16x32_bf16 v[58:61], v[148:151], v[172:175], v[58:61]
	v_mfma_f32_16x16x32_bf16 v[46:49], v[140:143], v[180:183], v[46:49]
	v_mfma_f32_16x16x32_bf16 v[42:45], v[148:151], v[180:183], v[42:45]
	v_mfma_f32_16x16x32_bf16 v[30:33], v[140:143], v[188:191], v[30:33]
	v_mfma_f32_16x16x32_bf16 v[26:29], v[148:151], v[188:191], v[26:29]
	v_mfma_f32_16x16x32_bf16 v[14:17], v[140:143], v[200:203], v[14:17]
	v_mfma_f32_16x16x32_bf16 v[10:13], v[148:151], v[200:203], v[10:13]
	s_setprio 0
	s_setprio 1
	v_mfma_f32_16x16x32_bf16 v[54:57], v[152:155], v[168:171], 0
	v_mfma_f32_16x16x32_bf16 v[50:53], v[160:163], v[168:171], 0
	v_mfma_f32_16x16x32_bf16 v[38:41], v[152:155], v[176:179], 0
	v_mfma_f32_16x16x32_bf16 v[34:37], v[160:163], v[176:179], 0
	v_mfma_f32_16x16x32_bf16 v[22:25], v[152:155], v[184:187], 0
	v_mfma_f32_16x16x32_bf16 v[18:21], v[160:163], v[184:187], 0
	v_mfma_f32_16x16x32_bf16 v[6:9], v[152:155], v[196:199], 0
	v_mfma_f32_16x16x32_bf16 v[2:5], v[160:163], v[196:199], 0
	v_mfma_f32_16x16x32_bf16 v[54:57], v[156:159], v[172:175], v[54:57]
	v_mfma_f32_16x16x32_bf16 v[50:53], v[164:167], v[172:175], v[50:53]
	v_mfma_f32_16x16x32_bf16 v[38:41], v[156:159], v[180:183], v[38:41]
	v_mfma_f32_16x16x32_bf16 v[34:37], v[164:167], v[180:183], v[34:37]
	v_mfma_f32_16x16x32_bf16 v[22:25], v[156:159], v[188:191], v[22:25]
	v_mfma_f32_16x16x32_bf16 v[18:21], v[164:167], v[188:191], v[18:21]
	v_mfma_f32_16x16x32_bf16 v[6:9], v[156:159], v[200:203], v[6:9]
	v_mfma_f32_16x16x32_bf16 v[2:5], v[164:167], v[200:203], v[2:5]
	s_mov_b32 s100, 0
	s_branch .Lcj2_253
.Lcsk_253:
	s_mov_b32 s72, 0xf800000
	s_mov_b32 s73, 0x10000
	s_and_b64 vcc, exec, s[18:19]
	s_cbranch_vccz .LBB0_256

.LBB0_285:
	s_mov_b64 s[20:21], 0
	s_add_u32 s10, s10, s20
	s_addc_u32 s11, s11, s21
	s_add_u32 s18, s18, s20
	s_addc_u32 s19, s19, s21
	s_mov_b32 s55, 16
	s_cmp_lt_i32 s55, 1
	s_cbranch_scc1 .LBB0_291
	s_ashr_i32 s17, s16, 31
	s_lshl_b64 s[20:21], s[16:17], 19
	s_add_u32 s17, s31, s20
	s_addc_u32 s22, s37, s21
	s_and_b64 s[20:21], exec, s[4:5]
	s_cselect_b32 s21, s11, s22
	s_cselect_b32 s20, s10, s17
	s_cselect_b32 s23, s19, s1
	s_cselect_b32 s22, s18, s0
	s_lshl_b32 s17, s54, 8
	s_mov_b32 s56, 2
	s_mov_b64 s[24:25], 0x40080
	s_mov_b32 s100, 1
.LBB0_287:
	v_add_u32_e32 v130, 0x10000, v165
	v_add_u32_e32 v142, 0x14000, v165
	ds_read_b128 v[146:149], v130
	ds_read_b128 v[150:153], v130 offset:1024
	ds_read_b128 v[154:157], v130 offset:2048
	ds_read_b128 v[158:161], v130 offset:3072
	ds_read_b128 v[130:133], v142
	ds_read_b128 v[134:137], v142 offset:1024
	ds_read_b128 v[138:141], v142 offset:2048
	ds_read_b128 v[142:145], v142 offset:3072
	s_add_i32 m0, s13, 0xc000
	s_add_i32 s26, s13, 0xe000
	s_cmp_lg_u32 s55, s56
	s_cselect_b64 s[58:59], -1, 0
	v_lshl_add_u64 v[204:205], s[10:11], 0, v[194:195]
	v_lshl_add_u64 v[204:205], v[204:205], 0, s[24:25]
	v_mov_b32_e32 v163, v195
	ds_read_b128 v[174:177], v167
	ds_read_b128 v[178:181], v167 offset:1024
	ds_read_b128 v[182:185], v167 offset:2048
	ds_read_b128 v[186:189], v167 offset:3072
	ds_read_b128 v[190:193], v167 offset:4096
	ds_read_b128 v[196:199], v167 offset:5120
	ds_read_b128 v[200:203], v167 offset:6144
	ds_read_b128 v[216:219], v167 offset:7168
	global_load_lds_dwordx4 v[204:205], off
	v_lshl_add_u64 v[204:205], s[10:11], 0, v[162:163]
	v_lshl_add_u64 v[204:205], v[204:205], 0, s[24:25]
	s_mov_b32 m0, s26
	s_nop 0
	global_load_lds_dwordx4 v[204:205], off
	s_cmp_lg_u32 s100, 0
	s_waitcnt vmcnt(8)
	s_waitcnt lgkmcnt(0)
	s_barrier
	s_setprio 1
	s_waitcnt lgkmcnt(0)
	s_cbranch_scc1 .Lcz1_287
	v_mfma_f32_16x16x32_bf16 v[126:129], v[146:149], v[174:177], v[126:129]
	v_mfma_f32_16x16x32_bf16 v[122:125], v[154:157], v[174:177], v[122:125]
	v_mfma_f32_16x16x32_bf16 v[110:113], v[146:149], v[182:185], v[110:113]
	v_mfma_f32_16x16x32_bf16 v[106:109], v[154:157], v[182:185], v[106:109]
	v_mfma_f32_16x16x32_bf16 v[94:97], v[146:149], v[190:193], v[94:97]
	v_mfma_f32_16x16x32_bf16 v[90:93], v[154:157], v[190:193], v[90:93]
	v_mfma_f32_16x16x32_bf16 v[78:81], v[146:149], v[200:203], v[78:81]
	v_mfma_f32_16x16x32_bf16 v[74:77], v[154:157], v[200:203], v[74:77]
	v_mfma_f32_16x16x32_bf16 v[126:129], v[150:153], v[178:181], v[126:129]
	v_mfma_f32_16x16x32_bf16 v[122:125], v[158:161], v[178:181], v[122:125]
	v_mfma_f32_16x16x32_bf16 v[110:113], v[150:153], v[186:189], v[110:113]
	v_mfma_f32_16x16x32_bf16 v[106:109], v[158:161], v[186:189], v[106:109]
	v_mfma_f32_16x16x32_bf16 v[94:97], v[150:153], v[196:199], v[94:97]
	v_mfma_f32_16x16x32_bf16 v[90:93], v[158:161], v[196:199], v[90:93]
	v_mfma_f32_16x16x32_bf16 v[78:81], v[150:153], v[216:219], v[78:81]
	v_mfma_f32_16x16x32_bf16 v[74:77], v[158:161], v[216:219], v[74:77]
	s_setprio 0
	s_setprio 1
	v_mfma_f32_16x16x32_bf16 v[118:121], v[130:133], v[174:177], v[118:121]
	v_mfma_f32_16x16x32_bf16 v[114:117], v[138:141], v[174:177], v[114:117]
	v_mfma_f32_16x16x32_bf16 v[102:105], v[130:133], v[182:185], v[102:105]
	v_mfma_f32_16x16x32_bf16 v[98:101], v[138:141], v[182:185], v[98:101]
	v_mfma_f32_16x16x32_bf16 v[86:89], v[130:133], v[190:193], v[86:89]
	v_mfma_f32_16x16x32_bf16 v[82:85], v[138:141], v[190:193], v[82:85]
	v_mfma_f32_16x16x32_bf16 v[70:73], v[130:133], v[200:203], v[70:73]
	v_mfma_f32_16x16x32_bf16 v[66:69], v[138:141], v[200:203], v[66:69]
	v_mfma_f32_16x16x32_bf16 v[118:121], v[134:137], v[178:181], v[118:121]
	v_mfma_f32_16x16x32_bf16 v[114:117], v[142:145], v[178:181], v[114:117]
	v_mfma_f32_16x16x32_bf16 v[102:105], v[134:137], v[186:189], v[102:105]
	v_mfma_f32_16x16x32_bf16 v[98:101], v[142:145], v[186:189], v[98:101]
	v_mfma_f32_16x16x32_bf16 v[86:89], v[134:137], v[196:199], v[86:89]
	v_mfma_f32_16x16x32_bf16 v[82:85], v[142:145], v[196:199], v[82:85]
	v_mfma_f32_16x16x32_bf16 v[70:73], v[134:137], v[216:219], v[70:73]
	v_mfma_f32_16x16x32_bf16 v[66:69], v[142:145], v[216:219], v[66:69]
.Lcj1_287:
	s_setprio 0
	s_barrier
	s_and_b64 s[26:27], s[58:59], exec
	s_cselect_b32 s26, s56, 0
	s_or_b64 s[58:59], s[4:5], s[58:59]
	s_and_b64 vcc, exec, s[58:59]
	s_cbranch_vccnz .LBB0_289
	v_mov_b32_e32 v164, v0
	s_mov_b32 s26, 0
	v_ashrrev_i32_e32 v166, 31, v164
	v_lshrrev_b32_e32 v166, 26, v166
	v_lshlrev_b32_e32 v168, 4, v164
	v_add_u32_e32 v166, v164, v166
	v_bfe_i32 v164, v164, 27, 1
	v_lshrrev_b32_e32 v164, 22, v164
	v_add_u32_e32 v164, v168, v164
	v_and_b32_e32 v164, 0xfffffc00, v164
	v_sub_u32_e32 v164, v168, v164
	v_lshrrev_b32_e32 v169, 4, v164
	v_bitop3_b32 v164, v169, v164, 32 bitop3:0x6c
	v_ashrrev_i32_e32 v170, 31, v164
	v_ashrrev_i32_e32 v166, 6, v166
	v_lshrrev_b32_e32 v170, 26, v170
	v_lshlrev_b32_e32 v169, 3, v166
	v_add_u32_e32 v170, v164, v170
	v_and_b32_e32 v169, -16, v169
	v_ashrrev_i32_e32 v171, 6, v170
	v_add_u32_e32 v169, v171, v169
	v_and_b32_e32 v170, 0xc0, v170
	v_sub_u32_e32 v164, v164, v170
	v_lshlrev_b32_e32 v170, 1, v169
	v_lshrrev_b32_e32 v174, 2, v169
	v_and_b32_e32 v171, 3, v171
	v_and_b32_e32 v170, 24, v170
	v_and_b32_e32 v174, 4, v174
	v_and_or_b32 v169, v169, s71, v171
	v_lshlrev_b32_e32 v166, 5, v166
	v_ashrrev_i16_sdwa v164, v237, sext(v164) dst_sel:DWORD dst_unused:UNUSED_PAD src0_sel:DWORD src1_sel:BYTE_0
	v_or3_b32 v169, v169, v174, v170
	v_and_b32_e32 v166, 32, v166
	v_bfe_i32 v164, v164, 0, 16
	v_add_u32_e32 v170, s17, v169
	v_lshlrev_b32_e32 v169, 7, v169
	v_and_b32_e32 v169, 0x3f80, v169
	v_add_lshl_u32 v166, v166, v164, 1
	v_and_b32_e32 v164, 0x1fc000, v170
	v_bfe_u32 v171, v170, 7, 7
	v_add_u32_e32 v170, 0x80, v170
	v_or3_b32 v164, v164, v171, v169
	v_and_b32_e32 v171, 0x1fc000, v170
	v_bfe_u32 v170, v170, 7, 7
	v_or3_b32 v169, v171, v170, v169
	v_add_u32_e32 v168, 0x2000, v168
	v_lshl_add_u32 v164, v164, 11, v166
	v_lshl_add_u32 v166, v169, 11, v166
	v_ashrrev_i32_e32 v169, 31, v168
	v_lshrrev_b32_e32 v169, 22, v169
	v_add_u32_e32 v169, v168, v169
	v_ashrrev_i32_e32 v169, 10, v169
	v_mul_i32_i24_e32 v170, 0x400, v169
	v_sub_u32_e32 v168, v168, v170
	v_lshrrev_b32_e32 v170, 4, v168
	v_bitop3_b32 v168, v170, v168, 32 bitop3:0x6c
	v_ashrrev_i32_e32 v171, 31, v168
	v_lshrrev_b32_e32 v171, 26, v171
	v_lshlrev_b32_e32 v170, 3, v169
	v_add_u32_e32 v171, v168, v171
	v_and_b32_e32 v170, -16, v170
	v_ashrrev_i32_e32 v174, 6, v171
	v_add_u32_e32 v170, v174, v170
	v_and_b32_e32 v171, 0xc0, v171
	v_sub_u32_e32 v168, v168, v171
	v_lshlrev_b32_e32 v171, 1, v170
	v_lshrrev_b32_e32 v175, 2, v170
	v_and_b32_e32 v174, 3, v174
	v_and_b32_e32 v171, 24, v171
	v_and_b32_e32 v175, 4, v175
	v_and_or_b32 v170, v170, s71, v174
	v_lshlrev_b32_e32 v169, 5, v169
	v_ashrrev_i16_sdwa v168, v237, sext(v168) dst_sel:DWORD dst_unused:UNUSED_PAD src0_sel:DWORD src1_sel:BYTE_0
	v_or3_b32 v170, v170, v175, v171
	v_and_b32_e32 v169, 32, v169
	v_bfe_i32 v168, v168, 0, 16
	v_add_u32_e32 v171, s17, v170
	v_lshlrev_b32_e32 v170, 7, v170
	v_and_b32_e32 v170, 0x3f80, v170
	v_add_lshl_u32 v169, v169, v168, 1
	v_and_b32_e32 v168, 0x1fc000, v171
	v_bfe_u32 v174, v171, 7, 7
	v_add_u32_e32 v171, 0x80, v171
	v_or3_b32 v168, v168, v174, v170
	v_and_b32_e32 v174, 0x1fc000, v171
	v_bfe_u32 v171, v171, 7, 7
	v_or3_b32 v170, v174, v171, v170
	v_lshl_add_u32 v168, v168, 11, v169
	v_lshl_add_u32 v170, v170, 11, v169
	s_mov_b64 s[18:19], s[22:23]
	s_mov_b64 s[10:11], s[20:21]
.LBB0_289:
	s_ashr_i32 s27, s26, 31
	s_lshl_b64 s[26:27], s[26:27], 7
	s_add_u32 s58, s18, s26
	s_mov_b32 m0, s38
	s_addc_u32 s59, s19, s27
	ds_read_b128 v[174:177], v167 offset:16384
	ds_read_b128 v[178:181], v167 offset:17408
	ds_read_b128 v[182:185], v167 offset:18432
	ds_read_b128 v[186:189], v167 offset:19456
	ds_read_b128 v[190:193], v167 offset:20480
	ds_read_b128 v[196:199], v167 offset:21504
	ds_read_b128 v[200:203], v167 offset:22528
	ds_read_b128 v[216:219], v167 offset:23552
	global_load_lds_dwordx4 v164, s[58:59]
	s_mov_b32 m0, s39
	s_nop 0
	global_load_lds_dwordx4 v168, s[58:59]
	s_mov_b32 m0, s40
	s_nop 0
	global_load_lds_dwordx4 v166, s[58:59]
	s_mov_b32 m0, s41
	s_nop 0
	global_load_lds_dwordx4 v170, s[58:59]
	s_add_u32 s58, s10, s26
	s_addc_u32 s59, s11, s27
	v_lshl_add_u64 v[204:205], s[58:59], 0, v[194:195]
	s_mov_b32 m0, s13
	s_nop 0
	global_load_lds_dwordx4 v[204:205], off
	v_lshl_add_u64 v[204:205], s[58:59], 0, v[162:163]
	s_mov_b32 m0, s42
	s_nop 0
	global_load_lds_dwordx4 v[204:205], off
	s_cmp_lg_u32 s100, 0
	s_waitcnt vmcnt(8)
	s_waitcnt lgkmcnt(0)
	s_barrier
	s_setprio 1
	s_waitcnt lgkmcnt(0)
	s_cbranch_scc1 .Lcz2_287
	v_mfma_f32_16x16x32_bf16 v[62:65], v[146:149], v[174:177], v[62:65]
	v_mfma_f32_16x16x32_bf16 v[58:61], v[154:157], v[174:177], v[58:61]
	v_mfma_f32_16x16x32_bf16 v[46:49], v[146:149], v[182:185], v[46:49]
	v_mfma_f32_16x16x32_bf16 v[42:45], v[154:157], v[182:185], v[42:45]
	v_mfma_f32_16x16x32_bf16 v[30:33], v[146:149], v[190:193], v[30:33]
	v_mfma_f32_16x16x32_bf16 v[26:29], v[154:157], v[190:193], v[26:29]
	v_mfma_f32_16x16x32_bf16 v[14:17], v[146:149], v[200:203], v[14:17]
	v_mfma_f32_16x16x32_bf16 v[10:13], v[154:157], v[200:203], v[10:13]
	v_mfma_f32_16x16x32_bf16 v[62:65], v[150:153], v[178:181], v[62:65]
	v_mfma_f32_16x16x32_bf16 v[58:61], v[158:161], v[178:181], v[58:61]
	v_mfma_f32_16x16x32_bf16 v[46:49], v[150:153], v[186:189], v[46:49]
	v_mfma_f32_16x16x32_bf16 v[42:45], v[158:161], v[186:189], v[42:45]
	v_mfma_f32_16x16x32_bf16 v[30:33], v[150:153], v[196:199], v[30:33]
	v_mfma_f32_16x16x32_bf16 v[26:29], v[158:161], v[196:199], v[26:29]
	v_mfma_f32_16x16x32_bf16 v[14:17], v[150:153], v[216:219], v[14:17]
	v_mfma_f32_16x16x32_bf16 v[10:13], v[158:161], v[216:219], v[10:13]
	s_setprio 0
	s_setprio 1
	v_mfma_f32_16x16x32_bf16 v[54:57], v[130:133], v[174:177], v[54:57]
	v_mfma_f32_16x16x32_bf16 v[50:53], v[138:141], v[174:177], v[50:53]
	v_mfma_f32_16x16x32_bf16 v[38:41], v[130:133], v[182:185], v[38:41]
	v_mfma_f32_16x16x32_bf16 v[34:37], v[138:141], v[182:185], v[34:37]
	v_mfma_f32_16x16x32_bf16 v[22:25], v[130:133], v[190:193], v[22:25]
	v_mfma_f32_16x16x32_bf16 v[18:21], v[138:141], v[190:193], v[18:21]
	v_mfma_f32_16x16x32_bf16 v[6:9], v[130:133], v[200:203], v[6:9]
	v_mfma_f32_16x16x32_bf16 v[2:5], v[138:141], v[200:203], v[2:5]
	v_mfma_f32_16x16x32_bf16 v[54:57], v[134:137], v[178:181], v[54:57]
	v_mfma_f32_16x16x32_bf16 v[50:53], v[142:145], v[178:181], v[50:53]
	v_mfma_f32_16x16x32_bf16 v[38:41], v[134:137], v[186:189], v[38:41]
	v_mfma_f32_16x16x32_bf16 v[34:37], v[142:145], v[186:189], v[34:37]
	v_mfma_f32_16x16x32_bf16 v[22:25], v[134:137], v[196:199], v[22:25]
	v_mfma_f32_16x16x32_bf16 v[18:21], v[142:145], v[196:199], v[18:21]
	v_mfma_f32_16x16x32_bf16 v[6:9], v[134:137], v[216:219], v[6:9]
	v_mfma_f32_16x16x32_bf16 v[2:5], v[142:145], v[216:219], v[2:5]
.Lcj2_287:
	s_setprio 0
	s_barrier
	v_add_u32_e32 v142, 0x18000, v165
	v_add_u32_e32 v158, 0x1c000, v165
	ds_read_b128 v[130:133], v142
	ds_read_b128 v[134:137], v142 offset:1024
	ds_read_b128 v[138:141], v142 offset:2048
	ds_read_b128 v[142:145], v142 offset:3072
	ds_read_b128 v[146:149], v158
	ds_read_b128 v[150:153], v158 offset:1024
	ds_read_b128 v[154:157], v158 offset:2048
	ds_read_b128 v[158:161], v158 offset:3072
	s_add_u32 s58, s58, 0x40000
	s_addc_u32 s59, s59, 0
	s_mov_b32 m0, s43
	v_lshl_add_u64 v[204:205], s[58:59], 0, v[194:195]
	ds_read_b128 v[174:177], v167 offset:32768
	ds_read_b128 v[178:181], v167 offset:33792
	ds_read_b128 v[182:185], v167 offset:34816
	ds_read_b128 v[186:189], v167 offset:35840
	ds_read_b128 v[190:193], v167 offset:36864
	ds_read_b128 v[196:199], v167 offset:37888
	ds_read_b128 v[200:203], v167 offset:38912
	ds_read_b128 v[216:219], v167 offset:39936
	global_load_lds_dwordx4 v[204:205], off
	v_lshl_add_u64 v[204:205], s[58:59], 0, v[162:163]
	s_mov_b32 m0, s44
	s_nop 0
	global_load_lds_dwordx4 v[204:205], off
	s_waitcnt vmcnt(8)
	s_waitcnt lgkmcnt(0)
	s_barrier
	s_setprio 1
	s_waitcnt lgkmcnt(0)
	v_mfma_f32_16x16x32_bf16 v[126:129], v[130:133], v[174:177], v[126:129]
	v_mfma_f32_16x16x32_bf16 v[122:125], v[138:141], v[174:177], v[122:125]
	v_mfma_f32_16x16x32_bf16 v[110:113], v[130:133], v[182:185], v[110:113]
	v_mfma_f32_16x16x32_bf16 v[106:109], v[138:141], v[182:185], v[106:109]
	v_mfma_f32_16x16x32_bf16 v[94:97], v[130:133], v[190:193], v[94:97]
	v_mfma_f32_16x16x32_bf16 v[90:93], v[138:141], v[190:193], v[90:93]
	v_mfma_f32_16x16x32_bf16 v[78:81], v[130:133], v[200:203], v[78:81]
	v_mfma_f32_16x16x32_bf16 v[74:77], v[138:141], v[200:203], v[74:77]
	v_mfma_f32_16x16x32_bf16 v[126:129], v[134:137], v[178:181], v[126:129]
	v_mfma_f32_16x16x32_bf16 v[122:125], v[142:145], v[178:181], v[122:125]
	v_mfma_f32_16x16x32_bf16 v[110:113], v[134:137], v[186:189], v[110:113]
	v_mfma_f32_16x16x32_bf16 v[106:109], v[142:145], v[186:189], v[106:109]
	v_mfma_f32_16x16x32_bf16 v[94:97], v[134:137], v[196:199], v[94:97]
	v_mfma_f32_16x16x32_bf16 v[90:93], v[142:145], v[196:199], v[90:93]
	v_mfma_f32_16x16x32_bf16 v[78:81], v[134:137], v[216:219], v[78:81]
	v_mfma_f32_16x16x32_bf16 v[74:77], v[142:145], v[216:219], v[74:77]
	s_setprio 0
	s_setprio 1
	v_mfma_f32_16x16x32_bf16 v[118:121], v[146:149], v[174:177], v[118:121]
	v_mfma_f32_16x16x32_bf16 v[114:117], v[154:157], v[174:177], v[114:117]
	v_mfma_f32_16x16x32_bf16 v[102:105], v[146:149], v[182:185], v[102:105]
	v_mfma_f32_16x16x32_bf16 v[98:101], v[154:157], v[182:185], v[98:101]
	v_mfma_f32_16x16x32_bf16 v[86:89], v[146:149], v[190:193], v[86:89]
	v_mfma_f32_16x16x32_bf16 v[82:85], v[154:157], v[190:193], v[82:85]
	v_mfma_f32_16x16x32_bf16 v[70:73], v[146:149], v[200:203], v[70:73]
	v_mfma_f32_16x16x32_bf16 v[66:69], v[154:157], v[200:203], v[66:69]
	v_mfma_f32_16x16x32_bf16 v[118:121], v[150:153], v[178:181], v[118:121]
	v_mfma_f32_16x16x32_bf16 v[114:117], v[158:161], v[178:181], v[114:117]
	v_mfma_f32_16x16x32_bf16 v[102:105], v[150:153], v[186:189], v[102:105]
	v_mfma_f32_16x16x32_bf16 v[98:101], v[158:161], v[186:189], v[98:101]
	v_mfma_f32_16x16x32_bf16 v[86:89], v[150:153], v[196:199], v[86:89]
	v_mfma_f32_16x16x32_bf16 v[82:85], v[158:161], v[196:199], v[82:85]
	v_mfma_f32_16x16x32_bf16 v[70:73], v[150:153], v[216:219], v[70:73]
	v_mfma_f32_16x16x32_bf16 v[66:69], v[158:161], v[216:219], v[66:69]
	s_setprio 0
	s_barrier
	s_add_u32 s57, s26, 0x80
	s_addc_u32 s58, s27, 0
	s_add_u32 s26, s18, s57
	s_mov_b32 m0, s46
	s_addc_u32 s27, s19, s58
	ds_read_b128 v[174:177], v167 offset:49152
	ds_read_b128 v[178:181], v167 offset:50176
	ds_read_b128 v[182:185], v167 offset:51200
	ds_read_b128 v[186:189], v167 offset:52224
	ds_read_b128 v[190:193], v167 offset:53248
	ds_read_b128 v[196:199], v167 offset:54272
	ds_read_b128 v[200:203], v167 offset:55296
	ds_read_b128 v[216:219], v167 offset:56320
	global_load_lds_dwordx4 v164, s[26:27]
	s_mov_b32 m0, s47
	s_nop 0
	global_load_lds_dwordx4 v168, s[26:27]
	s_mov_b32 m0, s50
	s_nop 0
	global_load_lds_dwordx4 v166, s[26:27]
	s_mov_b32 m0, s51
	s_nop 0
	global_load_lds_dwordx4 v170, s[26:27]
	s_add_u32 s26, s10, s57
	s_addc_u32 s27, s11, s58
	v_lshl_add_u64 v[204:205], s[26:27], 0, v[194:195]
	s_mov_b32 m0, s48
	s_nop 0
	global_load_lds_dwordx4 v[204:205], off
	v_lshl_add_u64 v[204:205], s[26:27], 0, v[162:163]
	s_mov_b32 m0, s49
	s_nop 0
	global_load_lds_dwordx4 v[204:205], off
	s_waitcnt vmcnt(8)
	s_waitcnt lgkmcnt(0)
	s_barrier
	s_setprio 1
	s_waitcnt lgkmcnt(0)
	v_mfma_f32_16x16x32_bf16 v[62:65], v[130:133], v[174:177], v[62:65]
	v_mfma_f32_16x16x32_bf16 v[58:61], v[138:141], v[174:177], v[58:61]
	v_mfma_f32_16x16x32_bf16 v[46:49], v[130:133], v[182:185], v[46:49]
	v_mfma_f32_16x16x32_bf16 v[42:45], v[138:141], v[182:185], v[42:45]
	v_mfma_f32_16x16x32_bf16 v[30:33], v[130:133], v[190:193], v[30:33]
	v_mfma_f32_16x16x32_bf16 v[26:29], v[138:141], v[190:193], v[26:29]
	v_mfma_f32_16x16x32_bf16 v[14:17], v[130:133], v[200:203], v[14:17]
	v_mfma_f32_16x16x32_bf16 v[10:13], v[138:141], v[200:203], v[10:13]
	v_mfma_f32_16x16x32_bf16 v[62:65], v[134:137], v[178:181], v[62:65]
	v_mfma_f32_16x16x32_bf16 v[58:61], v[142:145], v[178:181], v[58:61]
	v_mfma_f32_16x16x32_bf16 v[46:49], v[134:137], v[186:189], v[46:49]
	v_mfma_f32_16x16x32_bf16 v[42:45], v[142:145], v[186:189], v[42:45]
	v_mfma_f32_16x16x32_bf16 v[30:33], v[134:137], v[196:199], v[30:33]
	v_mfma_f32_16x16x32_bf16 v[26:29], v[142:145], v[196:199], v[26:29]
	v_mfma_f32_16x16x32_bf16 v[14:17], v[134:137], v[216:219], v[14:17]
	v_mfma_f32_16x16x32_bf16 v[10:13], v[142:145], v[216:219], v[10:13]
	s_setprio 0
	s_setprio 1
	v_mfma_f32_16x16x32_bf16 v[54:57], v[146:149], v[174:177], v[54:57]
	v_mfma_f32_16x16x32_bf16 v[50:53], v[154:157], v[174:177], v[50:53]
	v_mfma_f32_16x16x32_bf16 v[38:41], v[146:149], v[182:185], v[38:41]
	v_mfma_f32_16x16x32_bf16 v[34:37], v[154:157], v[182:185], v[34:37]
	v_mfma_f32_16x16x32_bf16 v[22:25], v[146:149], v[190:193], v[22:25]
	v_mfma_f32_16x16x32_bf16 v[18:21], v[154:157], v[190:193], v[18:21]
	v_mfma_f32_16x16x32_bf16 v[6:9], v[146:149], v[200:203], v[6:9]
	v_mfma_f32_16x16x32_bf16 v[2:5], v[154:157], v[200:203], v[2:5]
	v_mfma_f32_16x16x32_bf16 v[54:57], v[150:153], v[178:181], v[54:57]
	v_mfma_f32_16x16x32_bf16 v[50:53], v[158:161], v[178:181], v[50:53]
	v_mfma_f32_16x16x32_bf16 v[38:41], v[150:153], v[186:189], v[38:41]
	v_mfma_f32_16x16x32_bf16 v[34:37], v[158:161], v[186:189], v[34:37]
	v_mfma_f32_16x16x32_bf16 v[22:25], v[150:153], v[196:199], v[22:25]
	v_mfma_f32_16x16x32_bf16 v[18:21], v[158:161], v[196:199], v[18:21]
	v_mfma_f32_16x16x32_bf16 v[6:9], v[150:153], v[216:219], v[6:9]
	v_mfma_f32_16x16x32_bf16 v[2:5], v[158:161], v[216:219], v[2:5]
	s_setprio 0
	s_barrier
	s_add_i32 s26, s56, 2
	s_add_u32 s24, s24, 0x100
	s_addc_u32 s25, s25, 0
	s_cmp_ge_i32 s56, s55
	s_cbranch_scc1 .LBB0_292
	s_mov_b32 s56, s26
	s_branch .LBB0_287
.Lcz1_287:
	v_mfma_f32_16x16x32_bf16 v[126:129], v[146:149], v[174:177], 0
	v_mfma_f32_16x16x32_bf16 v[122:125], v[154:157], v[174:177], 0
	v_mfma_f32_16x16x32_bf16 v[110:113], v[146:149], v[182:185], 0
	v_mfma_f32_16x16x32_bf16 v[106:109], v[154:157], v[182:185], 0
	v_mfma_f32_16x16x32_bf16 v[94:97], v[146:149], v[190:193], 0
	v_mfma_f32_16x16x32_bf16 v[90:93], v[154:157], v[190:193], 0
	v_mfma_f32_16x16x32_bf16 v[78:81], v[146:149], v[200:203], 0
	v_mfma_f32_16x16x32_bf16 v[74:77], v[154:157], v[200:203], 0
	v_mfma_f32_16x16x32_bf16 v[126:129], v[150:153], v[178:181], v[126:129]
	v_mfma_f32_16x16x32_bf16 v[122:125], v[158:161], v[178:181], v[122:125]
	v_mfma_f32_16x16x32_bf16 v[110:113], v[150:153], v[186:189], v[110:113]
	v_mfma_f32_16x16x32_bf16 v[106:109], v[158:161], v[186:189], v[106:109]
	v_mfma_f32_16x16x32_bf16 v[94:97], v[150:153], v[196:199], v[94:97]
	v_mfma_f32_16x16x32_bf16 v[90:93], v[158:161], v[196:199], v[90:93]
	v_mfma_f32_16x16x32_bf16 v[78:81], v[150:153], v[216:219], v[78:81]
	v_mfma_f32_16x16x32_bf16 v[74:77], v[158:161], v[216:219], v[74:77]
	s_setprio 0
	s_setprio 1
	v_mfma_f32_16x16x32_bf16 v[118:121], v[130:133], v[174:177], 0
	v_mfma_f32_16x16x32_bf16 v[114:117], v[138:141], v[174:177], 0
	v_mfma_f32_16x16x32_bf16 v[102:105], v[130:133], v[182:185], 0
	v_mfma_f32_16x16x32_bf16 v[98:101], v[138:141], v[182:185], 0
	v_mfma_f32_16x16x32_bf16 v[86:89], v[130:133], v[190:193], 0
	v_mfma_f32_16x16x32_bf16 v[82:85], v[138:141], v[190:193], 0
	v_mfma_f32_16x16x32_bf16 v[70:73], v[130:133], v[200:203], 0
	v_mfma_f32_16x16x32_bf16 v[66:69], v[138:141], v[200:203], 0
	v_mfma_f32_16x16x32_bf16 v[118:121], v[134:137], v[178:181], v[118:121]
	v_mfma_f32_16x16x32_bf16 v[114:117], v[142:145], v[178:181], v[114:117]
	v_mfma_f32_16x16x32_bf16 v[102:105], v[134:137], v[186:189], v[102:105]
	v_mfma_f32_16x16x32_bf16 v[98:101], v[142:145], v[186:189], v[98:101]
	v_mfma_f32_16x16x32_bf16 v[86:89], v[134:137], v[196:199], v[86:89]
	v_mfma_f32_16x16x32_bf16 v[82:85], v[142:145], v[196:199], v[82:85]
	v_mfma_f32_16x16x32_bf16 v[70:73], v[134:137], v[216:219], v[70:73]
	v_mfma_f32_16x16x32_bf16 v[66:69], v[142:145], v[216:219], v[66:69]
	s_branch .Lcj1_287
.Lcz2_287:
	v_mfma_f32_16x16x32_bf16 v[62:65], v[146:149], v[174:177], 0
	v_mfma_f32_16x16x32_bf16 v[58:61], v[154:157], v[174:177], 0
	v_mfma_f32_16x16x32_bf16 v[46:49], v[146:149], v[182:185], 0
	v_mfma_f32_16x16x32_bf16 v[42:45], v[154:157], v[182:185], 0
	v_mfma_f32_16x16x32_bf16 v[30:33], v[146:149], v[190:193], 0
	v_mfma_f32_16x16x32_bf16 v[26:29], v[154:157], v[190:193], 0
	v_mfma_f32_16x16x32_bf16 v[14:17], v[146:149], v[200:203], 0
	v_mfma_f32_16x16x32_bf16 v[10:13], v[154:157], v[200:203], 0
	v_mfma_f32_16x16x32_bf16 v[62:65], v[150:153], v[178:181], v[62:65]
	v_mfma_f32_16x16x32_bf16 v[58:61], v[158:161], v[178:181], v[58:61]
	v_mfma_f32_16x16x32_bf16 v[46:49], v[150:153], v[186:189], v[46:49]
	v_mfma_f32_16x16x32_bf16 v[42:45], v[158:161], v[186:189], v[42:45]
	v_mfma_f32_16x16x32_bf16 v[30:33], v[150:153], v[196:199], v[30:33]
	v_mfma_f32_16x16x32_bf16 v[26:29], v[158:161], v[196:199], v[26:29]
	v_mfma_f32_16x16x32_bf16 v[14:17], v[150:153], v[216:219], v[14:17]
	v_mfma_f32_16x16x32_bf16 v[10:13], v[158:161], v[216:219], v[10:13]
	s_setprio 0
	s_setprio 1
	v_mfma_f32_16x16x32_bf16 v[54:57], v[130:133], v[174:177], 0
	v_mfma_f32_16x16x32_bf16 v[50:53], v[138:141], v[174:177], 0
	v_mfma_f32_16x16x32_bf16 v[38:41], v[130:133], v[182:185], 0
	v_mfma_f32_16x16x32_bf16 v[34:37], v[138:141], v[182:185], 0
	v_mfma_f32_16x16x32_bf16 v[22:25], v[130:133], v[190:193], 0
	v_mfma_f32_16x16x32_bf16 v[18:21], v[138:141], v[190:193], 0
	v_mfma_f32_16x16x32_bf16 v[6:9], v[130:133], v[200:203], 0
	v_mfma_f32_16x16x32_bf16 v[2:5], v[138:141], v[200:203], 0
	v_mfma_f32_16x16x32_bf16 v[54:57], v[134:137], v[178:181], v[54:57]
	v_mfma_f32_16x16x32_bf16 v[50:53], v[142:145], v[178:181], v[50:53]
	v_mfma_f32_16x16x32_bf16 v[38:41], v[134:137], v[186:189], v[38:41]
	v_mfma_f32_16x16x32_bf16 v[34:37], v[142:145], v[186:189], v[34:37]
	v_mfma_f32_16x16x32_bf16 v[22:25], v[134:137], v[196:199], v[22:25]
	v_mfma_f32_16x16x32_bf16 v[18:21], v[142:145], v[196:199], v[18:21]
	v_mfma_f32_16x16x32_bf16 v[6:9], v[134:137], v[216:219], v[6:9]
	v_mfma_f32_16x16x32_bf16 v[2:5], v[142:145], v[216:219], v[2:5]
	s_mov_b32 s100, 0
	s_branch .Lcj2_287

.LBB0_372:
	s_mov_b64 s[24:25], 0
	s_add_u32 s20, s20, s24
	s_addc_u32 s21, s21, s25
	s_add_u32 s8, s8, s24
	s_addc_u32 s9, s9, s25
	s_mov_b32 s54, 2
	s_cmp_lt_i32 s54, 1
	s_cbranch_scc1 .LBB0_380
	s_ashr_i32 s23, s22, 31
	s_lshl_b64 s[24:25], s[22:23], 16
	s_add_u32 s23, s30, s24
	s_addc_u32 s55, s31, s25
	s_mov_b32 s56, 2
	s_mov_b64 s[24:25], 0x8080
	s_mov_b32 s100, 1
.LBB0_374:
	v_add_u32_e32 v142, 0x10000, v217
	v_add_u32_e32 v158, 0x14000, v217
	ds_read_b128 v[130:133], v142
	ds_read_b128 v[134:137], v142 offset:1024
	ds_read_b128 v[138:141], v142 offset:2048
	ds_read_b128 v[142:145], v142 offset:3072
	ds_read_b128 v[146:149], v158
	ds_read_b128 v[150:153], v158 offset:1024
	ds_read_b128 v[154:157], v158 offset:2048
	ds_read_b128 v[158:161], v158 offset:3072
	s_add_i32 m0, s37, 0xc000
	s_add_i32 s57, s37, 0xe000
	s_cmp_eq_u32 s54, s56
	s_cselect_b64 s[58:59], -1, 0
	v_lshl_add_u64 v[196:197], s[20:21], 0, v[194:195]
	v_lshl_add_u64 v[196:197], v[196:197], 0, s[24:25]
	v_mov_b32_e32 v219, v195
	ds_read_b128 v[162:165], v221
	ds_read_b128 v[166:169], v221 offset:1024
	ds_read_b128 v[170:173], v221 offset:2048
	ds_read_b128 v[174:177], v221 offset:3072
	ds_read_b128 v[178:181], v221 offset:4096
	ds_read_b128 v[182:185], v221 offset:5120
	ds_read_b128 v[186:189], v221 offset:6144
	ds_read_b128 v[190:193], v221 offset:7168
	global_load_lds_dwordx4 v[196:197], off
	v_lshl_add_u64 v[196:197], s[20:21], 0, v[218:219]
	v_lshl_add_u64 v[196:197], v[196:197], 0, s[24:25]
	s_mov_b32 m0, s57
	s_nop 0
	global_load_lds_dwordx4 v[196:197], off
	s_cmp_lg_u32 s100, 0
	s_waitcnt vmcnt(8)
	s_waitcnt lgkmcnt(0)
	s_barrier
	s_setprio 1
	s_waitcnt lgkmcnt(0)
	s_cbranch_scc1 .Lcz1_374
	v_mfma_f32_16x16x32_bf16 v[126:129], v[130:133], v[162:165], v[126:129]
	v_mfma_f32_16x16x32_bf16 v[122:125], v[138:141], v[162:165], v[122:125]
	v_mfma_f32_16x16x32_bf16 v[94:97], v[130:133], v[170:173], v[94:97]
	v_mfma_f32_16x16x32_bf16 v[86:89], v[138:141], v[170:173], v[86:89]
	v_mfma_f32_16x16x32_bf16 v[62:65], v[130:133], v[178:181], v[62:65]
	v_mfma_f32_16x16x32_bf16 v[54:57], v[138:141], v[178:181], v[54:57]
	v_mfma_f32_16x16x32_bf16 v[30:33], v[130:133], v[186:189], v[30:33]
	v_mfma_f32_16x16x32_bf16 v[22:25], v[138:141], v[186:189], v[22:25]
	v_mfma_f32_16x16x32_bf16 v[126:129], v[134:137], v[166:169], v[126:129]
	v_mfma_f32_16x16x32_bf16 v[122:125], v[142:145], v[166:169], v[122:125]
	v_mfma_f32_16x16x32_bf16 v[94:97], v[134:137], v[174:177], v[94:97]
	v_mfma_f32_16x16x32_bf16 v[86:89], v[142:145], v[174:177], v[86:89]
	v_mfma_f32_16x16x32_bf16 v[62:65], v[134:137], v[182:185], v[62:65]
	v_mfma_f32_16x16x32_bf16 v[54:57], v[142:145], v[182:185], v[54:57]
	v_mfma_f32_16x16x32_bf16 v[30:33], v[134:137], v[190:193], v[30:33]
	v_mfma_f32_16x16x32_bf16 v[22:25], v[142:145], v[190:193], v[22:25]
	s_setprio 0
	s_setprio 1
	v_mfma_f32_16x16x32_bf16 v[110:113], v[146:149], v[162:165], v[110:113]
	v_mfma_f32_16x16x32_bf16 v[102:105], v[154:157], v[162:165], v[102:105]
	v_mfma_f32_16x16x32_bf16 v[78:81], v[146:149], v[170:173], v[78:81]
	v_mfma_f32_16x16x32_bf16 v[70:73], v[154:157], v[170:173], v[70:73]
	v_mfma_f32_16x16x32_bf16 v[46:49], v[146:149], v[178:181], v[46:49]
	v_mfma_f32_16x16x32_bf16 v[38:41], v[154:157], v[178:181], v[38:41]
	v_mfma_f32_16x16x32_bf16 v[14:17], v[146:149], v[186:189], v[14:17]
	v_mfma_f32_16x16x32_bf16 v[6:9], v[154:157], v[186:189], v[6:9]
	v_mfma_f32_16x16x32_bf16 v[110:113], v[150:153], v[166:169], v[110:113]
	v_mfma_f32_16x16x32_bf16 v[102:105], v[158:161], v[166:169], v[102:105]
	v_mfma_f32_16x16x32_bf16 v[78:81], v[150:153], v[174:177], v[78:81]
	v_mfma_f32_16x16x32_bf16 v[70:73], v[158:161], v[174:177], v[70:73]
	v_mfma_f32_16x16x32_bf16 v[46:49], v[150:153], v[182:185], v[46:49]
	v_mfma_f32_16x16x32_bf16 v[38:41], v[158:161], v[182:185], v[38:41]
	v_mfma_f32_16x16x32_bf16 v[14:17], v[150:153], v[190:193], v[14:17]
	v_mfma_f32_16x16x32_bf16 v[6:9], v[158:161], v[190:193], v[6:9]
.Lcj1_374:
	s_setprio 0
	s_barrier
	s_and_b64 s[60:61], s[58:59], exec
	s_cselect_b32 s62, 0, s56
	s_and_b64 s[58:59], s[2:3], s[58:59]
	s_and_b64 s[58:59], s[58:59], exec
	s_cselect_b32 s9, s55, s9
	s_cselect_b32 s8, s23, s8
	s_cselect_b32 s21, s7, s21
	s_cselect_b32 s20, s6, s20
	s_lshl_b64 s[58:59], s[62:63], 7
	s_add_u32 s60, s8, s58
	s_addc_u32 s61, s9, s59
	s_mov_b32 m0, s38
	s_add_u32 s57, s8, 0x8000
	ds_read_b128 v[162:165], v221 offset:16384
	ds_read_b128 v[166:169], v221 offset:17408
	ds_read_b128 v[170:173], v221 offset:18432
	ds_read_b128 v[174:177], v221 offset:19456
	ds_read_b128 v[178:181], v221 offset:20480
	ds_read_b128 v[182:185], v221 offset:21504
	ds_read_b128 v[186:189], v221 offset:22528
	ds_read_b128 v[190:193], v221 offset:23552
	global_load_lds_dwordx4 v216, s[60:61]
	s_mov_b32 m0, s39
	s_addc_u32 s66, s9, 0
	global_load_lds_dwordx4 v220, s[60:61]
	s_add_u32 s60, s57, s58
	s_addc_u32 s61, s66, s59
	s_mov_b32 m0, s40
	s_add_u32 s58, s20, s58
	global_load_lds_dwordx4 v216, s[60:61]
	s_mov_b32 m0, s41
	s_addc_u32 s59, s21, s59
	global_load_lds_dwordx4 v220, s[60:61]
	s_mov_b32 m0, s37
	s_nop 0
	global_load_lds_dwordx4 v194, s[58:59]
	s_mov_b32 m0, s42
	s_nop 0
	global_load_lds_dwordx4 v218, s[58:59]
	s_cmp_lg_u32 s100, 0
	s_waitcnt vmcnt(8)
	s_waitcnt lgkmcnt(0)
	s_barrier
	s_setprio 1
	s_waitcnt lgkmcnt(0)
	s_cbranch_scc1 .Lcz2_374
	v_mfma_f32_16x16x32_bf16 v[118:121], v[130:133], v[162:165], v[118:121]
	v_mfma_f32_16x16x32_bf16 v[114:117], v[138:141], v[162:165], v[114:117]
	v_mfma_f32_16x16x32_bf16 v[90:93], v[130:133], v[170:173], v[90:93]
	v_mfma_f32_16x16x32_bf16 v[82:85], v[138:141], v[170:173], v[82:85]
	v_mfma_f32_16x16x32_bf16 v[58:61], v[130:133], v[178:181], v[58:61]
	v_mfma_f32_16x16x32_bf16 v[50:53], v[138:141], v[178:181], v[50:53]
	v_mfma_f32_16x16x32_bf16 v[26:29], v[130:133], v[186:189], v[26:29]
	v_mfma_f32_16x16x32_bf16 v[18:21], v[138:141], v[186:189], v[18:21]
	v_mfma_f32_16x16x32_bf16 v[118:121], v[134:137], v[166:169], v[118:121]
	v_mfma_f32_16x16x32_bf16 v[114:117], v[142:145], v[166:169], v[114:117]
	v_mfma_f32_16x16x32_bf16 v[90:93], v[134:137], v[174:177], v[90:93]
	v_mfma_f32_16x16x32_bf16 v[82:85], v[142:145], v[174:177], v[82:85]
	v_mfma_f32_16x16x32_bf16 v[58:61], v[134:137], v[182:185], v[58:61]
	v_mfma_f32_16x16x32_bf16 v[50:53], v[142:145], v[182:185], v[50:53]
	v_mfma_f32_16x16x32_bf16 v[26:29], v[134:137], v[190:193], v[26:29]
	v_mfma_f32_16x16x32_bf16 v[18:21], v[142:145], v[190:193], v[18:21]
	s_setprio 0
	s_setprio 1
	v_mfma_f32_16x16x32_bf16 v[106:109], v[146:149], v[162:165], v[106:109]
	v_mfma_f32_16x16x32_bf16 v[98:101], v[154:157], v[162:165], v[98:101]
	v_mfma_f32_16x16x32_bf16 v[74:77], v[146:149], v[170:173], v[74:77]
	v_mfma_f32_16x16x32_bf16 v[66:69], v[154:157], v[170:173], v[66:69]
	v_mfma_f32_16x16x32_bf16 v[42:45], v[146:149], v[178:181], v[42:45]
	v_mfma_f32_16x16x32_bf16 v[34:37], v[154:157], v[178:181], v[34:37]
	v_mfma_f32_16x16x32_bf16 v[10:13], v[146:149], v[186:189], v[10:13]
	v_mfma_f32_16x16x32_bf16 v[2:5], v[154:157], v[186:189], v[2:5]
	v_mfma_f32_16x16x32_bf16 v[106:109], v[150:153], v[166:169], v[106:109]
	v_mfma_f32_16x16x32_bf16 v[98:101], v[158:161], v[166:169], v[98:101]
	v_mfma_f32_16x16x32_bf16 v[74:77], v[150:153], v[174:177], v[74:77]
	v_mfma_f32_16x16x32_bf16 v[66:69], v[158:161], v[174:177], v[66:69]
	v_mfma_f32_16x16x32_bf16 v[42:45], v[150:153], v[182:185], v[42:45]
	v_mfma_f32_16x16x32_bf16 v[34:37], v[158:161], v[182:185], v[34:37]
	v_mfma_f32_16x16x32_bf16 v[10:13], v[150:153], v[190:193], v[10:13]
	v_mfma_f32_16x16x32_bf16 v[2:5], v[158:161], v[190:193], v[2:5]
.Lcj2_374:
	s_setprio 0
	s_barrier
	v_add_u32_e32 v142, 0x18000, v217
	v_add_u32_e32 v158, 0x1c000, v217
	ds_read_b128 v[130:133], v142
	ds_read_b128 v[134:137], v142 offset:1024
	ds_read_b128 v[138:141], v142 offset:2048
	ds_read_b128 v[142:145], v142 offset:3072
	ds_read_b128 v[146:149], v158
	ds_read_b128 v[150:153], v158 offset:1024
	ds_read_b128 v[154:157], v158 offset:2048
	ds_read_b128 v[158:161], v158 offset:3072
	s_add_u32 s58, s58, 0x8000
	s_addc_u32 s59, s59, 0
	s_mov_b32 m0, s43
	ds_read_b128 v[162:165], v221 offset:32768
	ds_read_b128 v[166:169], v221 offset:33792
	ds_read_b128 v[170:173], v221 offset:34816
	ds_read_b128 v[174:177], v221 offset:35840
	ds_read_b128 v[178:181], v221 offset:36864
	ds_read_b128 v[182:185], v221 offset:37888
	ds_read_b128 v[186:189], v221 offset:38912
	ds_read_b128 v[190:193], v221 offset:39936
	global_load_lds_dwordx4 v194, s[58:59]
	s_mov_b32 m0, s44
	s_nop 0
	global_load_lds_dwordx4 v218, s[58:59]
	s_waitcnt vmcnt(8)
	s_waitcnt lgkmcnt(0)
	s_barrier
	s_setprio 1
	s_waitcnt lgkmcnt(0)
	v_mfma_f32_16x16x32_bf16 v[126:129], v[130:133], v[162:165], v[126:129]
	v_mfma_f32_16x16x32_bf16 v[122:125], v[138:141], v[162:165], v[122:125]
	v_mfma_f32_16x16x32_bf16 v[94:97], v[130:133], v[170:173], v[94:97]
	v_mfma_f32_16x16x32_bf16 v[86:89], v[138:141], v[170:173], v[86:89]
	v_mfma_f32_16x16x32_bf16 v[62:65], v[130:133], v[178:181], v[62:65]
	v_mfma_f32_16x16x32_bf16 v[54:57], v[138:141], v[178:181], v[54:57]
	v_mfma_f32_16x16x32_bf16 v[30:33], v[130:133], v[186:189], v[30:33]
	v_mfma_f32_16x16x32_bf16 v[22:25], v[138:141], v[186:189], v[22:25]
	v_mfma_f32_16x16x32_bf16 v[126:129], v[134:137], v[166:169], v[126:129]
	v_mfma_f32_16x16x32_bf16 v[122:125], v[142:145], v[166:169], v[122:125]
	v_mfma_f32_16x16x32_bf16 v[94:97], v[134:137], v[174:177], v[94:97]
	v_mfma_f32_16x16x32_bf16 v[86:89], v[142:145], v[174:177], v[86:89]
	v_mfma_f32_16x16x32_bf16 v[62:65], v[134:137], v[182:185], v[62:65]
	v_mfma_f32_16x16x32_bf16 v[54:57], v[142:145], v[182:185], v[54:57]
	v_mfma_f32_16x16x32_bf16 v[30:33], v[134:137], v[190:193], v[30:33]
	v_mfma_f32_16x16x32_bf16 v[22:25], v[142:145], v[190:193], v[22:25]
	s_setprio 0
	s_setprio 1
	v_mfma_f32_16x16x32_bf16 v[110:113], v[146:149], v[162:165], v[110:113]
	v_mfma_f32_16x16x32_bf16 v[102:105], v[154:157], v[162:165], v[102:105]
	v_mfma_f32_16x16x32_bf16 v[78:81], v[146:149], v[170:173], v[78:81]
	v_mfma_f32_16x16x32_bf16 v[70:73], v[154:157], v[170:173], v[70:73]
	v_mfma_f32_16x16x32_bf16 v[46:49], v[146:149], v[178:181], v[46:49]
	v_mfma_f32_16x16x32_bf16 v[38:41], v[154:157], v[178:181], v[38:41]
	v_mfma_f32_16x16x32_bf16 v[14:17], v[146:149], v[186:189], v[14:17]
	v_mfma_f32_16x16x32_bf16 v[6:9], v[154:157], v[186:189], v[6:9]
	v_mfma_f32_16x16x32_bf16 v[110:113], v[150:153], v[166:169], v[110:113]
	v_mfma_f32_16x16x32_bf16 v[102:105], v[158:161], v[166:169], v[102:105]
	v_mfma_f32_16x16x32_bf16 v[78:81], v[150:153], v[174:177], v[78:81]
	v_mfma_f32_16x16x32_bf16 v[70:73], v[158:161], v[174:177], v[70:73]
	v_mfma_f32_16x16x32_bf16 v[46:49], v[150:153], v[182:185], v[46:49]
	v_mfma_f32_16x16x32_bf16 v[38:41], v[158:161], v[182:185], v[38:41]
	v_mfma_f32_16x16x32_bf16 v[14:17], v[150:153], v[190:193], v[14:17]
	v_mfma_f32_16x16x32_bf16 v[6:9], v[158:161], v[190:193], v[6:9]
	s_setprio 0
	s_barrier
	s_or_b32 s62, s62, 1
	s_lshl_b64 s[58:59], s[62:63], 7
	s_add_u32 s60, s8, s58
	s_mov_b32 m0, s45
	s_addc_u32 s61, s9, s59
	ds_read_b128 v[162:165], v221 offset:49152
	ds_read_b128 v[166:169], v221 offset:50176
	ds_read_b128 v[170:173], v221 offset:51200
	ds_read_b128 v[174:177], v221 offset:52224
	ds_read_b128 v[178:181], v221 offset:53248
	ds_read_b128 v[182:185], v221 offset:54272
	ds_read_b128 v[186:189], v221 offset:55296
	ds_read_b128 v[190:193], v221 offset:56320
	global_load_lds_dwordx4 v216, s[60:61]
	s_mov_b32 m0, s46
	s_nop 0
	global_load_lds_dwordx4 v220, s[60:61]
	s_add_u32 s60, s57, s58
	s_addc_u32 s61, s66, s59
	s_mov_b32 m0, s49
	s_add_u32 s58, s20, s58
	global_load_lds_dwordx4 v216, s[60:61]
	s_mov_b32 m0, s50
	s_addc_u32 s59, s21, s59
	global_load_lds_dwordx4 v220, s[60:61]
	s_mov_b32 m0, s47
	s_nop 0
	global_load_lds_dwordx4 v194, s[58:59]
	s_mov_b32 m0, s48
	s_nop 0
	global_load_lds_dwordx4 v218, s[58:59]
	s_waitcnt vmcnt(8)
	s_waitcnt lgkmcnt(0)
	s_barrier
	s_setprio 1
	s_waitcnt lgkmcnt(0)
	v_mfma_f32_16x16x32_bf16 v[118:121], v[130:133], v[162:165], v[118:121]
	v_mfma_f32_16x16x32_bf16 v[114:117], v[138:141], v[162:165], v[114:117]
	v_mfma_f32_16x16x32_bf16 v[90:93], v[130:133], v[170:173], v[90:93]
	v_mfma_f32_16x16x32_bf16 v[82:85], v[138:141], v[170:173], v[82:85]
	v_mfma_f32_16x16x32_bf16 v[58:61], v[130:133], v[178:181], v[58:61]
	v_mfma_f32_16x16x32_bf16 v[50:53], v[138:141], v[178:181], v[50:53]
	v_mfma_f32_16x16x32_bf16 v[26:29], v[130:133], v[186:189], v[26:29]
	v_mfma_f32_16x16x32_bf16 v[18:21], v[138:141], v[186:189], v[18:21]
	v_mfma_f32_16x16x32_bf16 v[118:121], v[134:137], v[166:169], v[118:121]
	v_mfma_f32_16x16x32_bf16 v[114:117], v[142:145], v[166:169], v[114:117]
	v_mfma_f32_16x16x32_bf16 v[90:93], v[134:137], v[174:177], v[90:93]
	v_mfma_f32_16x16x32_bf16 v[82:85], v[142:145], v[174:177], v[82:85]
	v_mfma_f32_16x16x32_bf16 v[58:61], v[134:137], v[182:185], v[58:61]
	v_mfma_f32_16x16x32_bf16 v[50:53], v[142:145], v[182:185], v[50:53]
	v_mfma_f32_16x16x32_bf16 v[26:29], v[134:137], v[190:193], v[26:29]
	v_mfma_f32_16x16x32_bf16 v[18:21], v[142:145], v[190:193], v[18:21]
	s_setprio 0
	s_setprio 1
	v_mfma_f32_16x16x32_bf16 v[106:109], v[146:149], v[162:165], v[106:109]
	v_mfma_f32_16x16x32_bf16 v[98:101], v[154:157], v[162:165], v[98:101]
	v_mfma_f32_16x16x32_bf16 v[74:77], v[146:149], v[170:173], v[74:77]
	v_mfma_f32_16x16x32_bf16 v[66:69], v[154:157], v[170:173], v[66:69]
	v_mfma_f32_16x16x32_bf16 v[42:45], v[146:149], v[178:181], v[42:45]
	v_mfma_f32_16x16x32_bf16 v[34:37], v[154:157], v[178:181], v[34:37]
	v_mfma_f32_16x16x32_bf16 v[10:13], v[146:149], v[186:189], v[10:13]
	v_mfma_f32_16x16x32_bf16 v[2:5], v[154:157], v[186:189], v[2:5]
	v_mfma_f32_16x16x32_bf16 v[106:109], v[150:153], v[166:169], v[106:109]
	v_mfma_f32_16x16x32_bf16 v[98:101], v[158:161], v[166:169], v[98:101]
	v_mfma_f32_16x16x32_bf16 v[74:77], v[150:153], v[174:177], v[74:77]
	v_mfma_f32_16x16x32_bf16 v[66:69], v[158:161], v[174:177], v[66:69]
	v_mfma_f32_16x16x32_bf16 v[42:45], v[150:153], v[182:185], v[42:45]
	v_mfma_f32_16x16x32_bf16 v[34:37], v[158:161], v[182:185], v[34:37]
	v_mfma_f32_16x16x32_bf16 v[10:13], v[150:153], v[190:193], v[10:13]
	v_mfma_f32_16x16x32_bf16 v[2:5], v[158:161], v[190:193], v[2:5]
	s_setprio 0
	s_barrier
	s_add_i32 s57, s56, 2
	s_add_u32 s24, s24, 0x100
	s_addc_u32 s25, s25, 0
	s_cmp_ge_i32 s56, s54
	s_mov_b32 s56, s57
	s_cbranch_scc0 .LBB0_374
	s_branch .Lcsk_374
.Lcz1_374:
	v_mfma_f32_16x16x32_bf16 v[126:129], v[130:133], v[162:165], 0
	v_mfma_f32_16x16x32_bf16 v[122:125], v[138:141], v[162:165], 0
	v_mfma_f32_16x16x32_bf16 v[94:97], v[130:133], v[170:173], 0
	v_mfma_f32_16x16x32_bf16 v[86:89], v[138:141], v[170:173], 0
	v_mfma_f32_16x16x32_bf16 v[62:65], v[130:133], v[178:181], 0
	v_mfma_f32_16x16x32_bf16 v[54:57], v[138:141], v[178:181], 0
	v_mfma_f32_16x16x32_bf16 v[30:33], v[130:133], v[186:189], 0
	v_mfma_f32_16x16x32_bf16 v[22:25], v[138:141], v[186:189], 0
	v_mfma_f32_16x16x32_bf16 v[126:129], v[134:137], v[166:169], v[126:129]
	v_mfma_f32_16x16x32_bf16 v[122:125], v[142:145], v[166:169], v[122:125]
	v_mfma_f32_16x16x32_bf16 v[94:97], v[134:137], v[174:177], v[94:97]
	v_mfma_f32_16x16x32_bf16 v[86:89], v[142:145], v[174:177], v[86:89]
	v_mfma_f32_16x16x32_bf16 v[62:65], v[134:137], v[182:185], v[62:65]
	v_mfma_f32_16x16x32_bf16 v[54:57], v[142:145], v[182:185], v[54:57]
	v_mfma_f32_16x16x32_bf16 v[30:33], v[134:137], v[190:193], v[30:33]
	v_mfma_f32_16x16x32_bf16 v[22:25], v[142:145], v[190:193], v[22:25]
	s_setprio 0
	s_setprio 1
	v_mfma_f32_16x16x32_bf16 v[110:113], v[146:149], v[162:165], 0
	v_mfma_f32_16x16x32_bf16 v[102:105], v[154:157], v[162:165], 0
	v_mfma_f32_16x16x32_bf16 v[78:81], v[146:149], v[170:173], 0
	v_mfma_f32_16x16x32_bf16 v[70:73], v[154:157], v[170:173], 0
	v_mfma_f32_16x16x32_bf16 v[46:49], v[146:149], v[178:181], 0
	v_mfma_f32_16x16x32_bf16 v[38:41], v[154:157], v[178:181], 0
	v_mfma_f32_16x16x32_bf16 v[14:17], v[146:149], v[186:189], 0
	v_mfma_f32_16x16x32_bf16 v[6:9], v[154:157], v[186:189], 0
	v_mfma_f32_16x16x32_bf16 v[110:113], v[150:153], v[166:169], v[110:113]
	v_mfma_f32_16x16x32_bf16 v[102:105], v[158:161], v[166:169], v[102:105]
	v_mfma_f32_16x16x32_bf16 v[78:81], v[150:153], v[174:177], v[78:81]
	v_mfma_f32_16x16x32_bf16 v[70:73], v[158:161], v[174:177], v[70:73]
	v_mfma_f32_16x16x32_bf16 v[46:49], v[150:153], v[182:185], v[46:49]
	v_mfma_f32_16x16x32_bf16 v[38:41], v[158:161], v[182:185], v[38:41]
	v_mfma_f32_16x16x32_bf16 v[14:17], v[150:153], v[190:193], v[14:17]
	v_mfma_f32_16x16x32_bf16 v[6:9], v[158:161], v[190:193], v[6:9]
	s_branch .Lcj1_374
.Lcz2_374:
	v_mfma_f32_16x16x32_bf16 v[118:121], v[130:133], v[162:165], 0
	v_mfma_f32_16x16x32_bf16 v[114:117], v[138:141], v[162:165], 0
	v_mfma_f32_16x16x32_bf16 v[90:93], v[130:133], v[170:173], 0
	v_mfma_f32_16x16x32_bf16 v[82:85], v[138:141], v[170:173], 0
	v_mfma_f32_16x16x32_bf16 v[58:61], v[130:133], v[178:181], 0
	v_mfma_f32_16x16x32_bf16 v[50:53], v[138:141], v[178:181], 0
	v_mfma_f32_16x16x32_bf16 v[26:29], v[130:133], v[186:189], 0
	v_mfma_f32_16x16x32_bf16 v[18:21], v[138:141], v[186:189], 0
	v_mfma_f32_16x16x32_bf16 v[118:121], v[134:137], v[166:169], v[118:121]
	v_mfma_f32_16x16x32_bf16 v[114:117], v[142:145], v[166:169], v[114:117]
	v_mfma_f32_16x16x32_bf16 v[90:93], v[134:137], v[174:177], v[90:93]
	v_mfma_f32_16x16x32_bf16 v[82:85], v[142:145], v[174:177], v[82:85]
	v_mfma_f32_16x16x32_bf16 v[58:61], v[134:137], v[182:185], v[58:61]
	v_mfma_f32_16x16x32_bf16 v[50:53], v[142:145], v[182:185], v[50:53]
	v_mfma_f32_16x16x32_bf16 v[26:29], v[134:137], v[190:193], v[26:29]
	v_mfma_f32_16x16x32_bf16 v[18:21], v[142:145], v[190:193], v[18:21]
	s_setprio 0
	s_setprio 1
	v_mfma_f32_16x16x32_bf16 v[106:109], v[146:149], v[162:165], 0
	v_mfma_f32_16x16x32_bf16 v[98:101], v[154:157], v[162:165], 0
	v_mfma_f32_16x16x32_bf16 v[74:77], v[146:149], v[170:173], 0
	v_mfma_f32_16x16x32_bf16 v[66:69], v[154:157], v[170:173], 0
	v_mfma_f32_16x16x32_bf16 v[42:45], v[146:149], v[178:181], 0
	v_mfma_f32_16x16x32_bf16 v[34:37], v[154:157], v[178:181], 0
	v_mfma_f32_16x16x32_bf16 v[10:13], v[146:149], v[186:189], 0
	v_mfma_f32_16x16x32_bf16 v[2:5], v[154:157], v[186:189], 0
	v_mfma_f32_16x16x32_bf16 v[106:109], v[150:153], v[166:169], v[106:109]
	v_mfma_f32_16x16x32_bf16 v[98:101], v[158:161], v[166:169], v[98:101]
	v_mfma_f32_16x16x32_bf16 v[74:77], v[150:153], v[174:177], v[74:77]
	v_mfma_f32_16x16x32_bf16 v[66:69], v[158:161], v[174:177], v[66:69]
	v_mfma_f32_16x16x32_bf16 v[42:45], v[150:153], v[182:185], v[42:45]
	v_mfma_f32_16x16x32_bf16 v[34:37], v[158:161], v[182:185], v[34:37]
	v_mfma_f32_16x16x32_bf16 v[10:13], v[150:153], v[190:193], v[10:13]
	v_mfma_f32_16x16x32_bf16 v[2:5], v[158:161], v[190:193], v[2:5]
	s_mov_b32 s100, 0
	s_branch .Lcj2_374
.Lcsk_374:
	s_and_b64 vcc, exec, s[18:19]
	s_cbranch_vccz .LBB0_377

.LBB0_490:
	s_mov_b64 s[18:19], 0
	s_add_u32 s16, s16, s18
	s_addc_u32 s17, s17, s19
	s_add_u32 s14, s14, s18
	s_addc_u32 s15, s15, s19
	s_mov_b32 s52, 4
	s_cmp_lt_i32 s52, 1
	s_cbranch_scc1 .LBB0_496
	s_and_b64 s[18:19], exec, s[4:5]
	s_cselect_b32 s19, s17, s1
	s_cselect_b32 s18, s16, s0
	s_cselect_b32 s21, s15, s7
	s_cselect_b32 s20, s14, s6
	s_lshl_b32 s22, s51, 1
	s_and_b32 s53, s22, 0x7e
	s_and_b32 s54, s22, 0xff80
	s_mov_b32 s55, 2
	s_mov_b64 s[22:23], 0x10080
	s_mov_b32 s100, 1
.LBB0_492:
	v_add_u32_e32 v130, 0x10000, v165
	v_add_u32_e32 v142, 0x14000, v165
	ds_read_b128 v[146:149], v130
	ds_read_b128 v[150:153], v130 offset:1024
	ds_read_b128 v[154:157], v130 offset:2048
	ds_read_b128 v[158:161], v130 offset:3072
	ds_read_b128 v[130:133], v142
	ds_read_b128 v[134:137], v142 offset:1024
	ds_read_b128 v[138:141], v142 offset:2048
	ds_read_b128 v[142:145], v142 offset:3072
	s_add_i32 m0, s29, 0xc000
	s_add_i32 s24, s29, 0xe000
	s_cmp_lg_u32 s52, s55
	s_cselect_b64 s[56:57], -1, 0
	v_lshl_add_u64 v[204:205], s[16:17], 0, v[194:195]
	v_lshl_add_u64 v[204:205], v[204:205], 0, s[22:23]
	v_mov_b32_e32 v163, v195
	ds_read_b128 v[174:177], v167
	ds_read_b128 v[178:181], v167 offset:1024
	ds_read_b128 v[182:185], v167 offset:2048
	ds_read_b128 v[186:189], v167 offset:3072
	ds_read_b128 v[190:193], v167 offset:4096
	ds_read_b128 v[196:199], v167 offset:5120
	ds_read_b128 v[200:203], v167 offset:6144
	ds_read_b128 v[216:219], v167 offset:7168
	global_load_lds_dwordx4 v[204:205], off
	v_lshl_add_u64 v[204:205], s[16:17], 0, v[162:163]
	v_lshl_add_u64 v[204:205], v[204:205], 0, s[22:23]
	s_mov_b32 m0, s24
	s_nop 0
	global_load_lds_dwordx4 v[204:205], off
	s_cmp_lg_u32 s100, 0
	s_waitcnt vmcnt(8)
	s_waitcnt lgkmcnt(0)
	s_barrier
	s_setprio 1
	s_waitcnt lgkmcnt(0)
	s_cbranch_scc1 .Lcz1_492
	v_mfma_f32_16x16x32_bf16 v[126:129], v[146:149], v[174:177], v[126:129]
	v_mfma_f32_16x16x32_bf16 v[122:125], v[154:157], v[174:177], v[122:125]
	v_mfma_f32_16x16x32_bf16 v[110:113], v[146:149], v[182:185], v[110:113]
	v_mfma_f32_16x16x32_bf16 v[106:109], v[154:157], v[182:185], v[106:109]
	v_mfma_f32_16x16x32_bf16 v[94:97], v[146:149], v[190:193], v[94:97]
	v_mfma_f32_16x16x32_bf16 v[90:93], v[154:157], v[190:193], v[90:93]
	v_mfma_f32_16x16x32_bf16 v[78:81], v[146:149], v[200:203], v[78:81]
	v_mfma_f32_16x16x32_bf16 v[74:77], v[154:157], v[200:203], v[74:77]
	v_mfma_f32_16x16x32_bf16 v[126:129], v[150:153], v[178:181], v[126:129]
	v_mfma_f32_16x16x32_bf16 v[122:125], v[158:161], v[178:181], v[122:125]
	v_mfma_f32_16x16x32_bf16 v[110:113], v[150:153], v[186:189], v[110:113]
	v_mfma_f32_16x16x32_bf16 v[106:109], v[158:161], v[186:189], v[106:109]
	v_mfma_f32_16x16x32_bf16 v[94:97], v[150:153], v[196:199], v[94:97]
	v_mfma_f32_16x16x32_bf16 v[90:93], v[158:161], v[196:199], v[90:93]
	v_mfma_f32_16x16x32_bf16 v[78:81], v[150:153], v[216:219], v[78:81]
	v_mfma_f32_16x16x32_bf16 v[74:77], v[158:161], v[216:219], v[74:77]
	s_setprio 0
	s_setprio 1
	v_mfma_f32_16x16x32_bf16 v[118:121], v[130:133], v[174:177], v[118:121]
	v_mfma_f32_16x16x32_bf16 v[114:117], v[138:141], v[174:177], v[114:117]
	v_mfma_f32_16x16x32_bf16 v[102:105], v[130:133], v[182:185], v[102:105]
	v_mfma_f32_16x16x32_bf16 v[98:101], v[138:141], v[182:185], v[98:101]
	v_mfma_f32_16x16x32_bf16 v[86:89], v[130:133], v[190:193], v[86:89]
	v_mfma_f32_16x16x32_bf16 v[82:85], v[138:141], v[190:193], v[82:85]
	v_mfma_f32_16x16x32_bf16 v[70:73], v[130:133], v[200:203], v[70:73]
	v_mfma_f32_16x16x32_bf16 v[66:69], v[138:141], v[200:203], v[66:69]
	v_mfma_f32_16x16x32_bf16 v[118:121], v[134:137], v[178:181], v[118:121]
	v_mfma_f32_16x16x32_bf16 v[114:117], v[142:145], v[178:181], v[114:117]
	v_mfma_f32_16x16x32_bf16 v[102:105], v[134:137], v[186:189], v[102:105]
	v_mfma_f32_16x16x32_bf16 v[98:101], v[142:145], v[186:189], v[98:101]
	v_mfma_f32_16x16x32_bf16 v[86:89], v[134:137], v[196:199], v[86:89]
	v_mfma_f32_16x16x32_bf16 v[82:85], v[142:145], v[196:199], v[82:85]
	v_mfma_f32_16x16x32_bf16 v[70:73], v[134:137], v[216:219], v[70:73]
	v_mfma_f32_16x16x32_bf16 v[66:69], v[142:145], v[216:219], v[66:69]
.Lcj1_492:
	s_setprio 0
	s_barrier
	s_and_b64 s[24:25], s[56:57], exec
	s_cselect_b32 s24, s55, 0
	s_or_b64 s[56:57], s[4:5], s[56:57]
	s_and_b64 vcc, exec, s[56:57]
	s_cbranch_vccnz .LBB0_494
	v_mov_b32_e32 v164, v0
	s_mov_b32 s24, 0
	v_ashrrev_i32_e32 v166, 31, v164
	v_lshrrev_b32_e32 v166, 26, v166
	v_lshlrev_b32_e32 v168, 4, v164
	v_add_u32_e32 v166, v164, v166
	v_bfe_i32 v164, v164, 27, 1
	v_lshrrev_b32_e32 v164, 22, v164
	v_add_u32_e32 v164, v168, v164
	v_and_b32_e32 v164, 0xfffffc00, v164
	v_sub_u32_e32 v164, v168, v164
	v_lshrrev_b32_e32 v169, 4, v164
	v_bitop3_b32 v164, v169, v164, 32 bitop3:0x6c
	v_ashrrev_i32_e32 v170, 31, v164
	v_ashrrev_i32_e32 v166, 6, v166
	v_lshrrev_b32_e32 v170, 26, v170
	v_lshlrev_b32_e32 v169, 3, v166
	v_add_u32_e32 v170, v164, v170
	v_and_b32_e32 v169, -16, v169
	v_ashrrev_i32_e32 v171, 6, v170
	v_add_u32_e32 v169, v171, v169
	v_and_b32_e32 v170, 0xc0, v170
	v_lshrrev_b32_e32 v174, 2, v169
	v_sub_u32_e32 v164, v164, v170
	v_lshlrev_b32_e32 v170, 1, v169
	v_and_b32_e32 v174, 4, v174
	v_and_b32_e32 v171, 3, v171
	v_lshrrev_b32_e32 v175, 7, v169
	v_and_b32_e32 v169, 0x60, v169
	v_lshlrev_b32_e32 v166, 5, v166
	v_ashrrev_i16_sdwa v164, v237, sext(v164) dst_sel:DWORD dst_unused:UNUSED_PAD src0_sel:DWORD src1_sel:BYTE_0
	v_and_b32_e32 v170, 24, v170
	v_or3_b32 v169, v171, v169, v174
	v_and_b32_e32 v166, 32, v166
	v_bfe_i32 v164, v164, 0, 16
	v_or3_b32 v169, v169, v170, s54
	v_lshlrev_b32_e32 v169, 16, v169
	v_add_lshl_u32 v164, v166, v164, 1
	v_add_lshl_u32 v166, v175, s53, 9
	v_add_u32_e32 v168, 0x2000, v168
	v_add3_u32 v164, v169, v164, v166
	v_ashrrev_i32_e32 v169, 31, v168
	v_lshrrev_b32_e32 v169, 22, v169
	v_add_u32_e32 v169, v168, v169
	v_ashrrev_i32_e32 v169, 10, v169
	v_mul_i32_i24_e32 v170, 0x400, v169
	v_sub_u32_e32 v168, v168, v170
	v_lshrrev_b32_e32 v170, 4, v168
	v_bitop3_b32 v168, v170, v168, 32 bitop3:0x6c
	v_ashrrev_i32_e32 v171, 31, v168
	v_lshrrev_b32_e32 v171, 26, v171
	v_lshlrev_b32_e32 v170, 3, v169
	v_add_u32_e32 v171, v168, v171
	v_and_b32_e32 v170, -16, v170
	v_ashrrev_i32_e32 v174, 6, v171
	v_add_u32_e32 v170, v174, v170
	v_and_b32_e32 v171, 0xc0, v171
	v_lshrrev_b32_e32 v175, 2, v170
	v_sub_u32_e32 v168, v168, v171
	v_lshlrev_b32_e32 v171, 1, v170
	v_and_b32_e32 v175, 4, v175
	v_and_b32_e32 v174, 3, v174
	v_lshrrev_b32_e32 v176, 7, v170
	v_and_b32_e32 v170, 0x60, v170
	v_lshlrev_b32_e32 v169, 5, v169
	v_ashrrev_i16_sdwa v168, v237, sext(v168) dst_sel:DWORD dst_unused:UNUSED_PAD src0_sel:DWORD src1_sel:BYTE_0
	v_and_b32_e32 v171, 24, v171
	v_or3_b32 v170, v174, v170, v175
	v_and_b32_e32 v169, 32, v169
	v_bfe_i32 v168, v168, 0, 16
	v_or3_b32 v170, v170, v171, s54
	v_lshlrev_b32_e32 v170, 16, v170
	v_add_lshl_u32 v168, v169, v168, 1
	v_add_lshl_u32 v169, v176, s53, 9
	v_add3_u32 v168, v170, v168, v169
	v_add_u32_e32 v166, 0x200, v164
	v_add_u32_e32 v170, 0x200, v168
	s_mov_b64 s[14:15], s[20:21]
	s_mov_b64 s[16:17], s[18:19]
.LBB0_494:
	s_ashr_i32 s25, s24, 31
	s_lshl_b64 s[24:25], s[24:25], 7
	s_add_u32 s56, s14, s24
	s_mov_b32 m0, s30
	s_addc_u32 s57, s15, s25
	ds_read_b128 v[174:177], v167 offset:16384
	ds_read_b128 v[178:181], v167 offset:17408
	ds_read_b128 v[182:185], v167 offset:18432
	ds_read_b128 v[186:189], v167 offset:19456
	ds_read_b128 v[190:193], v167 offset:20480
	ds_read_b128 v[196:199], v167 offset:21504
	ds_read_b128 v[200:203], v167 offset:22528
	ds_read_b128 v[216:219], v167 offset:23552
	global_load_lds_dwordx4 v164, s[56:57]
	s_mov_b32 m0, s31
	s_nop 0
	global_load_lds_dwordx4 v168, s[56:57]
	s_mov_b32 m0, s37
	s_nop 0
	global_load_lds_dwordx4 v166, s[56:57]
	s_mov_b32 m0, s38
	s_nop 0
	global_load_lds_dwordx4 v170, s[56:57]
	s_add_u32 s56, s16, s24
	s_addc_u32 s57, s17, s25
	v_lshl_add_u64 v[204:205], s[56:57], 0, v[194:195]
	s_mov_b32 m0, s29
	s_nop 0
	global_load_lds_dwordx4 v[204:205], off
	v_lshl_add_u64 v[204:205], s[56:57], 0, v[162:163]
	s_mov_b32 m0, s39
	s_nop 0
	global_load_lds_dwordx4 v[204:205], off
	s_cmp_lg_u32 s100, 0
	s_waitcnt vmcnt(8)
	s_waitcnt lgkmcnt(0)
	s_barrier
	s_setprio 1
	s_waitcnt lgkmcnt(0)
	s_cbranch_scc1 .Lcz2_492
	v_mfma_f32_16x16x32_bf16 v[62:65], v[146:149], v[174:177], v[62:65]
	v_mfma_f32_16x16x32_bf16 v[58:61], v[154:157], v[174:177], v[58:61]
	v_mfma_f32_16x16x32_bf16 v[46:49], v[146:149], v[182:185], v[46:49]
	v_mfma_f32_16x16x32_bf16 v[42:45], v[154:157], v[182:185], v[42:45]
	v_mfma_f32_16x16x32_bf16 v[30:33], v[146:149], v[190:193], v[30:33]
	v_mfma_f32_16x16x32_bf16 v[26:29], v[154:157], v[190:193], v[26:29]
	v_mfma_f32_16x16x32_bf16 v[14:17], v[146:149], v[200:203], v[14:17]
	v_mfma_f32_16x16x32_bf16 v[10:13], v[154:157], v[200:203], v[10:13]
	v_mfma_f32_16x16x32_bf16 v[62:65], v[150:153], v[178:181], v[62:65]
	v_mfma_f32_16x16x32_bf16 v[58:61], v[158:161], v[178:181], v[58:61]
	v_mfma_f32_16x16x32_bf16 v[46:49], v[150:153], v[186:189], v[46:49]
	v_mfma_f32_16x16x32_bf16 v[42:45], v[158:161], v[186:189], v[42:45]
	v_mfma_f32_16x16x32_bf16 v[30:33], v[150:153], v[196:199], v[30:33]
	v_mfma_f32_16x16x32_bf16 v[26:29], v[158:161], v[196:199], v[26:29]
	v_mfma_f32_16x16x32_bf16 v[14:17], v[150:153], v[216:219], v[14:17]
	v_mfma_f32_16x16x32_bf16 v[10:13], v[158:161], v[216:219], v[10:13]
	s_setprio 0
	s_setprio 1
	v_mfma_f32_16x16x32_bf16 v[54:57], v[130:133], v[174:177], v[54:57]
	v_mfma_f32_16x16x32_bf16 v[50:53], v[138:141], v[174:177], v[50:53]
	v_mfma_f32_16x16x32_bf16 v[38:41], v[130:133], v[182:185], v[38:41]
	v_mfma_f32_16x16x32_bf16 v[34:37], v[138:141], v[182:185], v[34:37]
	v_mfma_f32_16x16x32_bf16 v[22:25], v[130:133], v[190:193], v[22:25]
	v_mfma_f32_16x16x32_bf16 v[18:21], v[138:141], v[190:193], v[18:21]
	v_mfma_f32_16x16x32_bf16 v[6:9], v[130:133], v[200:203], v[6:9]
	v_mfma_f32_16x16x32_bf16 v[2:5], v[138:141], v[200:203], v[2:5]
	v_mfma_f32_16x16x32_bf16 v[54:57], v[134:137], v[178:181], v[54:57]
	v_mfma_f32_16x16x32_bf16 v[50:53], v[142:145], v[178:181], v[50:53]
	v_mfma_f32_16x16x32_bf16 v[38:41], v[134:137], v[186:189], v[38:41]
	v_mfma_f32_16x16x32_bf16 v[34:37], v[142:145], v[186:189], v[34:37]
	v_mfma_f32_16x16x32_bf16 v[22:25], v[134:137], v[196:199], v[22:25]
	v_mfma_f32_16x16x32_bf16 v[18:21], v[142:145], v[196:199], v[18:21]
	v_mfma_f32_16x16x32_bf16 v[6:9], v[134:137], v[216:219], v[6:9]
	v_mfma_f32_16x16x32_bf16 v[2:5], v[142:145], v[216:219], v[2:5]
.Lcj2_492:
	s_setprio 0
	s_barrier
	v_add_u32_e32 v142, 0x18000, v165
	v_add_u32_e32 v158, 0x1c000, v165
	ds_read_b128 v[130:133], v142
	ds_read_b128 v[134:137], v142 offset:1024
	ds_read_b128 v[138:141], v142 offset:2048
	ds_read_b128 v[142:145], v142 offset:3072
	ds_read_b128 v[146:149], v158
	ds_read_b128 v[150:153], v158 offset:1024
	ds_read_b128 v[154:157], v158 offset:2048
	ds_read_b128 v[158:161], v158 offset:3072
	s_add_u32 s56, s56, 0x10000
	s_addc_u32 s57, s57, 0
	s_mov_b32 m0, s40
	v_lshl_add_u64 v[204:205], s[56:57], 0, v[194:195]
	ds_read_b128 v[174:177], v167 offset:32768
	ds_read_b128 v[178:181], v167 offset:33792
	ds_read_b128 v[182:185], v167 offset:34816
	ds_read_b128 v[186:189], v167 offset:35840
	ds_read_b128 v[190:193], v167 offset:36864
	ds_read_b128 v[196:199], v167 offset:37888
	ds_read_b128 v[200:203], v167 offset:38912
	ds_read_b128 v[216:219], v167 offset:39936
	global_load_lds_dwordx4 v[204:205], off
	v_lshl_add_u64 v[204:205], s[56:57], 0, v[162:163]
	s_mov_b32 m0, s41
	s_nop 0
	global_load_lds_dwordx4 v[204:205], off
	s_waitcnt vmcnt(8)
	s_waitcnt lgkmcnt(0)
	s_barrier
	s_setprio 1
	s_waitcnt lgkmcnt(0)
	v_mfma_f32_16x16x32_bf16 v[126:129], v[130:133], v[174:177], v[126:129]
	v_mfma_f32_16x16x32_bf16 v[122:125], v[138:141], v[174:177], v[122:125]
	v_mfma_f32_16x16x32_bf16 v[110:113], v[130:133], v[182:185], v[110:113]
	v_mfma_f32_16x16x32_bf16 v[106:109], v[138:141], v[182:185], v[106:109]
	v_mfma_f32_16x16x32_bf16 v[94:97], v[130:133], v[190:193], v[94:97]
	v_mfma_f32_16x16x32_bf16 v[90:93], v[138:141], v[190:193], v[90:93]
	v_mfma_f32_16x16x32_bf16 v[78:81], v[130:133], v[200:203], v[78:81]
	v_mfma_f32_16x16x32_bf16 v[74:77], v[138:141], v[200:203], v[74:77]
	v_mfma_f32_16x16x32_bf16 v[126:129], v[134:137], v[178:181], v[126:129]
	v_mfma_f32_16x16x32_bf16 v[122:125], v[142:145], v[178:181], v[122:125]
	v_mfma_f32_16x16x32_bf16 v[110:113], v[134:137], v[186:189], v[110:113]
	v_mfma_f32_16x16x32_bf16 v[106:109], v[142:145], v[186:189], v[106:109]
	v_mfma_f32_16x16x32_bf16 v[94:97], v[134:137], v[196:199], v[94:97]
	v_mfma_f32_16x16x32_bf16 v[90:93], v[142:145], v[196:199], v[90:93]
	v_mfma_f32_16x16x32_bf16 v[78:81], v[134:137], v[216:219], v[78:81]
	v_mfma_f32_16x16x32_bf16 v[74:77], v[142:145], v[216:219], v[74:77]
	s_setprio 0
	s_setprio 1
	v_mfma_f32_16x16x32_bf16 v[118:121], v[146:149], v[174:177], v[118:121]
	v_mfma_f32_16x16x32_bf16 v[114:117], v[154:157], v[174:177], v[114:117]
	v_mfma_f32_16x16x32_bf16 v[102:105], v[146:149], v[182:185], v[102:105]
	v_mfma_f32_16x16x32_bf16 v[98:101], v[154:157], v[182:185], v[98:101]
	v_mfma_f32_16x16x32_bf16 v[86:89], v[146:149], v[190:193], v[86:89]
	v_mfma_f32_16x16x32_bf16 v[82:85], v[154:157], v[190:193], v[82:85]
	v_mfma_f32_16x16x32_bf16 v[70:73], v[146:149], v[200:203], v[70:73]
	v_mfma_f32_16x16x32_bf16 v[66:69], v[154:157], v[200:203], v[66:69]
	v_mfma_f32_16x16x32_bf16 v[118:121], v[150:153], v[178:181], v[118:121]
	v_mfma_f32_16x16x32_bf16 v[114:117], v[158:161], v[178:181], v[114:117]
	v_mfma_f32_16x16x32_bf16 v[102:105], v[150:153], v[186:189], v[102:105]
	v_mfma_f32_16x16x32_bf16 v[98:101], v[158:161], v[186:189], v[98:101]
	v_mfma_f32_16x16x32_bf16 v[86:89], v[150:153], v[196:199], v[86:89]
	v_mfma_f32_16x16x32_bf16 v[82:85], v[158:161], v[196:199], v[82:85]
	v_mfma_f32_16x16x32_bf16 v[70:73], v[150:153], v[216:219], v[70:73]
	v_mfma_f32_16x16x32_bf16 v[66:69], v[158:161], v[216:219], v[66:69]
	s_setprio 0
	s_barrier
	s_add_u32 s56, s24, 0x80
	s_addc_u32 s57, s25, 0
	s_add_u32 s24, s14, s56
	s_mov_b32 m0, s43
	s_addc_u32 s25, s15, s57
	ds_read_b128 v[174:177], v167 offset:49152
	ds_read_b128 v[178:181], v167 offset:50176
	ds_read_b128 v[182:185], v167 offset:51200
	ds_read_b128 v[186:189], v167 offset:52224
	ds_read_b128 v[190:193], v167 offset:53248
	ds_read_b128 v[196:199], v167 offset:54272
	ds_read_b128 v[200:203], v167 offset:55296
	ds_read_b128 v[216:219], v167 offset:56320
	global_load_lds_dwordx4 v164, s[24:25]
	s_mov_b32 m0, s44
	s_nop 0
	global_load_lds_dwordx4 v168, s[24:25]
	s_mov_b32 m0, s47
	s_nop 0
	global_load_lds_dwordx4 v166, s[24:25]
	s_mov_b32 m0, s48
	s_nop 0
	global_load_lds_dwordx4 v170, s[24:25]
	s_add_u32 s24, s16, s56
	s_addc_u32 s25, s17, s57
	v_lshl_add_u64 v[204:205], s[24:25], 0, v[194:195]
	s_mov_b32 m0, s45
	s_nop 0
	global_load_lds_dwordx4 v[204:205], off
	v_lshl_add_u64 v[204:205], s[24:25], 0, v[162:163]
	s_mov_b32 m0, s46
	s_nop 0
	global_load_lds_dwordx4 v[204:205], off
	s_waitcnt vmcnt(8)
	s_waitcnt lgkmcnt(0)
	s_barrier
	s_setprio 1
	s_waitcnt lgkmcnt(0)
	v_mfma_f32_16x16x32_bf16 v[62:65], v[130:133], v[174:177], v[62:65]
	v_mfma_f32_16x16x32_bf16 v[58:61], v[138:141], v[174:177], v[58:61]
	v_mfma_f32_16x16x32_bf16 v[46:49], v[130:133], v[182:185], v[46:49]
	v_mfma_f32_16x16x32_bf16 v[42:45], v[138:141], v[182:185], v[42:45]
	v_mfma_f32_16x16x32_bf16 v[30:33], v[130:133], v[190:193], v[30:33]
	v_mfma_f32_16x16x32_bf16 v[26:29], v[138:141], v[190:193], v[26:29]
	v_mfma_f32_16x16x32_bf16 v[14:17], v[130:133], v[200:203], v[14:17]
	v_mfma_f32_16x16x32_bf16 v[10:13], v[138:141], v[200:203], v[10:13]
	v_mfma_f32_16x16x32_bf16 v[62:65], v[134:137], v[178:181], v[62:65]
	v_mfma_f32_16x16x32_bf16 v[58:61], v[142:145], v[178:181], v[58:61]
	v_mfma_f32_16x16x32_bf16 v[46:49], v[134:137], v[186:189], v[46:49]
	v_mfma_f32_16x16x32_bf16 v[42:45], v[142:145], v[186:189], v[42:45]
	v_mfma_f32_16x16x32_bf16 v[30:33], v[134:137], v[196:199], v[30:33]
	v_mfma_f32_16x16x32_bf16 v[26:29], v[142:145], v[196:199], v[26:29]
	v_mfma_f32_16x16x32_bf16 v[14:17], v[134:137], v[216:219], v[14:17]
	v_mfma_f32_16x16x32_bf16 v[10:13], v[142:145], v[216:219], v[10:13]
	s_setprio 0
	s_setprio 1
	v_mfma_f32_16x16x32_bf16 v[54:57], v[146:149], v[174:177], v[54:57]
	v_mfma_f32_16x16x32_bf16 v[50:53], v[154:157], v[174:177], v[50:53]
	v_mfma_f32_16x16x32_bf16 v[38:41], v[146:149], v[182:185], v[38:41]
	v_mfma_f32_16x16x32_bf16 v[34:37], v[154:157], v[182:185], v[34:37]
	v_mfma_f32_16x16x32_bf16 v[22:25], v[146:149], v[190:193], v[22:25]
	v_mfma_f32_16x16x32_bf16 v[18:21], v[154:157], v[190:193], v[18:21]
	v_mfma_f32_16x16x32_bf16 v[6:9], v[146:149], v[200:203], v[6:9]
	v_mfma_f32_16x16x32_bf16 v[2:5], v[154:157], v[200:203], v[2:5]
	v_mfma_f32_16x16x32_bf16 v[54:57], v[150:153], v[178:181], v[54:57]
	v_mfma_f32_16x16x32_bf16 v[50:53], v[158:161], v[178:181], v[50:53]
	v_mfma_f32_16x16x32_bf16 v[38:41], v[150:153], v[186:189], v[38:41]
	v_mfma_f32_16x16x32_bf16 v[34:37], v[158:161], v[186:189], v[34:37]
	v_mfma_f32_16x16x32_bf16 v[22:25], v[150:153], v[196:199], v[22:25]
	v_mfma_f32_16x16x32_bf16 v[18:21], v[158:161], v[196:199], v[18:21]
	v_mfma_f32_16x16x32_bf16 v[6:9], v[150:153], v[216:219], v[6:9]
	v_mfma_f32_16x16x32_bf16 v[2:5], v[158:161], v[216:219], v[2:5]
	s_setprio 0
	s_barrier
	s_add_i32 s24, s55, 2
	s_add_u32 s22, s22, 0x100
	s_addc_u32 s23, s23, 0
	s_cmp_ge_i32 s55, s52
	s_cbranch_scc1 .LBB0_497
	s_mov_b32 s55, s24
	s_branch .LBB0_492

.LBB0_577:
	s_mov_b32 s58, 24
	s_cmp_lt_i32 s58, 1
	s_cbranch_scc1 .LBB0_588
	s_lshl_b32 s20, s57, 8
	s_ashr_i32 s21, s20, 31
	s_add_i32 s59, s58, -2
	s_lshl_b32 s60, s56, 8
	s_lshl_b64 s[20:21], s[20:21], 1
	s_add_u32 s20, s44, s20
	s_addc_u32 s21, s45, s21
	s_mov_b32 s61, 0
	s_mov_b64 s[22:23], 0x60080
	s_mov_b32 s100, 1

.LBB0_581:
	v_add_u32_e32 v142, 0x10000, v191
	v_add_u32_e32 v158, 0x14000, v191
	ds_read_b128 v[130:133], v142
	ds_read_b128 v[134:137], v142 offset:1024
	ds_read_b128 v[138:141], v142 offset:2048
	ds_read_b128 v[142:145], v142 offset:3072
	ds_read_b128 v[146:149], v158
	ds_read_b128 v[150:153], v158 offset:1024
	ds_read_b128 v[154:157], v158 offset:2048
	ds_read_b128 v[158:161], v158 offset:3072
	s_add_i32 m0, s31, 0xc000
	s_add_i32 s62, s31, 0xe000
	s_add_i32 s66, s61, 2
	s_cmp_eq_u32 s59, s61
	s_cselect_b64 s[68:69], -1, 0
	v_lshl_add_u64 v[200:201], s[0:1], 0, v[194:195]
	v_lshl_add_u64 v[200:201], v[200:201], 0, s[22:23]
	v_mov_b32_e32 v193, v195
	ds_read_b128 v[162:165], v217
	ds_read_b128 v[166:169], v217 offset:1024
	ds_read_b128 v[170:173], v217 offset:2048
	ds_read_b128 v[174:177], v217 offset:3072
	ds_read_b128 v[178:181], v217 offset:4096
	ds_read_b128 v[182:185], v217 offset:5120
	ds_read_b128 v[186:189], v217 offset:6144
	ds_read_b128 v[196:199], v217 offset:7168
	global_load_lds_dwordx4 v[200:201], off
	v_lshl_add_u64 v[200:201], s[0:1], 0, v[192:193]
	v_lshl_add_u64 v[200:201], v[200:201], 0, s[22:23]
	s_mov_b32 m0, s62
	s_nop 0
	global_load_lds_dwordx4 v[200:201], off
	s_cmp_lg_u32 s100, 0
	s_waitcnt vmcnt(8)
	s_waitcnt lgkmcnt(0)
	s_barrier
	s_setprio 1
	s_waitcnt lgkmcnt(0)
	s_cbranch_scc1 .Lcz1_579
	v_mfma_f32_16x16x32_bf16 v[122:125], v[130:133], v[162:165], v[122:125]
	v_mfma_f32_16x16x32_bf16 v[126:129], v[138:141], v[162:165], v[126:129]
	v_mfma_f32_16x16x32_bf16 v[110:113], v[130:133], v[170:173], v[110:113]
	v_mfma_f32_16x16x32_bf16 v[106:109], v[138:141], v[170:173], v[106:109]
	v_mfma_f32_16x16x32_bf16 v[94:97], v[130:133], v[178:181], v[94:97]
	v_mfma_f32_16x16x32_bf16 v[90:93], v[138:141], v[178:181], v[90:93]
	v_mfma_f32_16x16x32_bf16 v[78:81], v[130:133], v[186:189], v[78:81]
	v_mfma_f32_16x16x32_bf16 v[74:77], v[138:141], v[186:189], v[74:77]
	v_mfma_f32_16x16x32_bf16 v[122:125], v[134:137], v[166:169], v[122:125]
	v_mfma_f32_16x16x32_bf16 v[126:129], v[142:145], v[166:169], v[126:129]
	v_mfma_f32_16x16x32_bf16 v[110:113], v[134:137], v[174:177], v[110:113]
	v_mfma_f32_16x16x32_bf16 v[106:109], v[142:145], v[174:177], v[106:109]
	v_mfma_f32_16x16x32_bf16 v[94:97], v[134:137], v[182:185], v[94:97]
	v_mfma_f32_16x16x32_bf16 v[90:93], v[142:145], v[182:185], v[90:93]
	v_mfma_f32_16x16x32_bf16 v[78:81], v[134:137], v[196:199], v[78:81]
	v_mfma_f32_16x16x32_bf16 v[74:77], v[142:145], v[196:199], v[74:77]
	s_setprio 0
	s_setprio 1
	v_mfma_f32_16x16x32_bf16 v[118:121], v[146:149], v[162:165], v[118:121]
	v_mfma_f32_16x16x32_bf16 v[114:117], v[154:157], v[162:165], v[114:117]
	v_mfma_f32_16x16x32_bf16 v[102:105], v[146:149], v[170:173], v[102:105]
	v_mfma_f32_16x16x32_bf16 v[98:101], v[154:157], v[170:173], v[98:101]
	v_mfma_f32_16x16x32_bf16 v[86:89], v[146:149], v[178:181], v[86:89]
	v_mfma_f32_16x16x32_bf16 v[82:85], v[154:157], v[178:181], v[82:85]
	v_mfma_f32_16x16x32_bf16 v[70:73], v[146:149], v[186:189], v[70:73]
	v_mfma_f32_16x16x32_bf16 v[66:69], v[154:157], v[186:189], v[66:69]
	v_mfma_f32_16x16x32_bf16 v[118:121], v[150:153], v[166:169], v[118:121]
	v_mfma_f32_16x16x32_bf16 v[114:117], v[158:161], v[166:169], v[114:117]
	v_mfma_f32_16x16x32_bf16 v[102:105], v[150:153], v[174:177], v[102:105]
	v_mfma_f32_16x16x32_bf16 v[98:101], v[158:161], v[174:177], v[98:101]
	v_mfma_f32_16x16x32_bf16 v[86:89], v[150:153], v[182:185], v[86:89]
	v_mfma_f32_16x16x32_bf16 v[82:85], v[158:161], v[182:185], v[82:85]
	v_mfma_f32_16x16x32_bf16 v[70:73], v[150:153], v[196:199], v[70:73]
	v_mfma_f32_16x16x32_bf16 v[66:69], v[158:161], v[196:199], v[66:69]
.Lcj1_579:
	s_setprio 0
	s_barrier
	s_and_b64 s[72:73], s[68:69], exec
	s_cselect_b32 s62, 0, s66
	s_and_b64 s[68:69], s[4:5], s[68:69]
	s_and_b64 s[68:69], s[68:69], exec
	s_cselect_b32 s7, s19, s7
	s_cselect_b32 s6, s18, s6
	s_cselect_b32 s1, s17, s1
	s_cselect_b32 s0, s16, s0
	s_lshl_b64 s[68:69], s[62:63], 7
	s_add_u32 s72, s6, s68
	s_addc_u32 s73, s7, s69
	s_mov_b32 m0, s37
	s_add_u32 s61, s6, 0x60000
	ds_read_b128 v[162:165], v217 offset:16384
	ds_read_b128 v[166:169], v217 offset:17408
	ds_read_b128 v[170:173], v217 offset:18432
	ds_read_b128 v[174:177], v217 offset:19456
	ds_read_b128 v[178:181], v217 offset:20480
	ds_read_b128 v[182:185], v217 offset:21504
	ds_read_b128 v[186:189], v217 offset:22528
	ds_read_b128 v[196:199], v217 offset:23552
	global_load_lds_dwordx4 v190, s[72:73]
	s_mov_b32 m0, s38
	s_addc_u32 s67, s7, 0
	global_load_lds_dwordx4 v216, s[72:73]
	s_add_u32 s72, s61, s68
	s_addc_u32 s73, s67, s69
	s_mov_b32 m0, s39
	s_add_u32 s68, s0, s68
	global_load_lds_dwordx4 v190, s[72:73]
	s_mov_b32 m0, s40
	s_addc_u32 s69, s1, s69
	global_load_lds_dwordx4 v216, s[72:73]
	s_mov_b32 m0, s31
	s_nop 0
	global_load_lds_dwordx4 v194, s[68:69]
	s_mov_b32 m0, s41
	s_nop 0
	global_load_lds_dwordx4 v192, s[68:69]
	s_cmp_lg_u32 s100, 0
	s_waitcnt vmcnt(8)
	s_waitcnt lgkmcnt(0)
	s_barrier
	s_setprio 1
	s_waitcnt lgkmcnt(0)
	s_cbranch_scc1 .Lcz2_579
	v_mfma_f32_16x16x32_bf16 v[62:65], v[130:133], v[162:165], v[62:65]
	v_mfma_f32_16x16x32_bf16 v[58:61], v[138:141], v[162:165], v[58:61]
	v_mfma_f32_16x16x32_bf16 v[46:49], v[130:133], v[170:173], v[46:49]
	v_mfma_f32_16x16x32_bf16 v[42:45], v[138:141], v[170:173], v[42:45]
	v_mfma_f32_16x16x32_bf16 v[30:33], v[130:133], v[178:181], v[30:33]
	v_mfma_f32_16x16x32_bf16 v[26:29], v[138:141], v[178:181], v[26:29]
	v_mfma_f32_16x16x32_bf16 v[14:17], v[130:133], v[186:189], v[14:17]
	v_mfma_f32_16x16x32_bf16 v[10:13], v[138:141], v[186:189], v[10:13]
	v_mfma_f32_16x16x32_bf16 v[62:65], v[134:137], v[166:169], v[62:65]
	v_mfma_f32_16x16x32_bf16 v[58:61], v[142:145], v[166:169], v[58:61]
	v_mfma_f32_16x16x32_bf16 v[46:49], v[134:137], v[174:177], v[46:49]
	v_mfma_f32_16x16x32_bf16 v[42:45], v[142:145], v[174:177], v[42:45]
	v_mfma_f32_16x16x32_bf16 v[30:33], v[134:137], v[182:185], v[30:33]
	v_mfma_f32_16x16x32_bf16 v[26:29], v[142:145], v[182:185], v[26:29]
	v_mfma_f32_16x16x32_bf16 v[14:17], v[134:137], v[196:199], v[14:17]
	v_mfma_f32_16x16x32_bf16 v[10:13], v[142:145], v[196:199], v[10:13]
	s_setprio 0
	s_setprio 1
	v_mfma_f32_16x16x32_bf16 v[54:57], v[146:149], v[162:165], v[54:57]
	v_mfma_f32_16x16x32_bf16 v[50:53], v[154:157], v[162:165], v[50:53]
	v_mfma_f32_16x16x32_bf16 v[38:41], v[146:149], v[170:173], v[38:41]
	v_mfma_f32_16x16x32_bf16 v[34:37], v[154:157], v[170:173], v[34:37]
	v_mfma_f32_16x16x32_bf16 v[22:25], v[146:149], v[178:181], v[22:25]
	v_mfma_f32_16x16x32_bf16 v[18:21], v[154:157], v[178:181], v[18:21]
	v_mfma_f32_16x16x32_bf16 v[6:9], v[146:149], v[186:189], v[6:9]
	v_mfma_f32_16x16x32_bf16 v[2:5], v[154:157], v[186:189], v[2:5]
	v_mfma_f32_16x16x32_bf16 v[54:57], v[150:153], v[166:169], v[54:57]
	v_mfma_f32_16x16x32_bf16 v[50:53], v[158:161], v[166:169], v[50:53]
	v_mfma_f32_16x16x32_bf16 v[38:41], v[150:153], v[174:177], v[38:41]
	v_mfma_f32_16x16x32_bf16 v[34:37], v[158:161], v[174:177], v[34:37]
	v_mfma_f32_16x16x32_bf16 v[22:25], v[150:153], v[182:185], v[22:25]
	v_mfma_f32_16x16x32_bf16 v[18:21], v[158:161], v[182:185], v[18:21]
	v_mfma_f32_16x16x32_bf16 v[6:9], v[150:153], v[196:199], v[6:9]
	v_mfma_f32_16x16x32_bf16 v[2:5], v[158:161], v[196:199], v[2:5]
.Lcj2_579:
	s_setprio 0
	s_barrier
	v_add_u32_e32 v142, 0x18000, v191
	v_add_u32_e32 v158, 0x1c000, v191
	ds_read_b128 v[130:133], v142
	ds_read_b128 v[134:137], v142 offset:1024
	ds_read_b128 v[138:141], v142 offset:2048
	ds_read_b128 v[142:145], v142 offset:3072
	ds_read_b128 v[146:149], v158
	ds_read_b128 v[150:153], v158 offset:1024
	ds_read_b128 v[154:157], v158 offset:2048
	ds_read_b128 v[158:161], v158 offset:3072
	s_add_u32 s68, s68, 0x60000
	s_addc_u32 s69, s69, 0
	s_mov_b32 m0, s42
	ds_read_b128 v[162:165], v217 offset:32768
	ds_read_b128 v[166:169], v217 offset:33792
	ds_read_b128 v[170:173], v217 offset:34816
	ds_read_b128 v[174:177], v217 offset:35840
	ds_read_b128 v[178:181], v217 offset:36864
	ds_read_b128 v[182:185], v217 offset:37888
	ds_read_b128 v[186:189], v217 offset:38912
	ds_read_b128 v[196:199], v217 offset:39936
	global_load_lds_dwordx4 v194, s[68:69]
	s_mov_b32 m0, s43
	s_nop 0
	global_load_lds_dwordx4 v192, s[68:69]
	s_waitcnt vmcnt(8)
	s_waitcnt lgkmcnt(0)
	s_barrier
	s_setprio 1
	s_waitcnt lgkmcnt(0)
	v_mfma_f32_16x16x32_bf16 v[122:125], v[130:133], v[162:165], v[122:125]
	v_mfma_f32_16x16x32_bf16 v[126:129], v[138:141], v[162:165], v[126:129]
	v_mfma_f32_16x16x32_bf16 v[110:113], v[130:133], v[170:173], v[110:113]
	v_mfma_f32_16x16x32_bf16 v[106:109], v[138:141], v[170:173], v[106:109]
	v_mfma_f32_16x16x32_bf16 v[94:97], v[130:133], v[178:181], v[94:97]
	v_mfma_f32_16x16x32_bf16 v[90:93], v[138:141], v[178:181], v[90:93]
	v_mfma_f32_16x16x32_bf16 v[78:81], v[130:133], v[186:189], v[78:81]
	v_mfma_f32_16x16x32_bf16 v[74:77], v[138:141], v[186:189], v[74:77]
	v_mfma_f32_16x16x32_bf16 v[122:125], v[134:137], v[166:169], v[122:125]
	v_mfma_f32_16x16x32_bf16 v[126:129], v[142:145], v[166:169], v[126:129]
	v_mfma_f32_16x16x32_bf16 v[110:113], v[134:137], v[174:177], v[110:113]
	v_mfma_f32_16x16x32_bf16 v[106:109], v[142:145], v[174:177], v[106:109]
	v_mfma_f32_16x16x32_bf16 v[94:97], v[134:137], v[182:185], v[94:97]
	v_mfma_f32_16x16x32_bf16 v[90:93], v[142:145], v[182:185], v[90:93]
	v_mfma_f32_16x16x32_bf16 v[78:81], v[134:137], v[196:199], v[78:81]
	v_mfma_f32_16x16x32_bf16 v[74:77], v[142:145], v[196:199], v[74:77]
	s_setprio 0
	s_setprio 1
	v_mfma_f32_16x16x32_bf16 v[118:121], v[146:149], v[162:165], v[118:121]
	v_mfma_f32_16x16x32_bf16 v[114:117], v[154:157], v[162:165], v[114:117]
	v_mfma_f32_16x16x32_bf16 v[102:105], v[146:149], v[170:173], v[102:105]
	v_mfma_f32_16x16x32_bf16 v[98:101], v[154:157], v[170:173], v[98:101]
	v_mfma_f32_16x16x32_bf16 v[86:89], v[146:149], v[178:181], v[86:89]
	v_mfma_f32_16x16x32_bf16 v[82:85], v[154:157], v[178:181], v[82:85]
	v_mfma_f32_16x16x32_bf16 v[70:73], v[146:149], v[186:189], v[70:73]
	v_mfma_f32_16x16x32_bf16 v[66:69], v[154:157], v[186:189], v[66:69]
	v_mfma_f32_16x16x32_bf16 v[118:121], v[150:153], v[166:169], v[118:121]
	v_mfma_f32_16x16x32_bf16 v[114:117], v[158:161], v[166:169], v[114:117]
	v_mfma_f32_16x16x32_bf16 v[102:105], v[150:153], v[174:177], v[102:105]
	v_mfma_f32_16x16x32_bf16 v[98:101], v[158:161], v[174:177], v[98:101]
	v_mfma_f32_16x16x32_bf16 v[86:89], v[150:153], v[182:185], v[86:89]
	v_mfma_f32_16x16x32_bf16 v[82:85], v[158:161], v[182:185], v[82:85]
	v_mfma_f32_16x16x32_bf16 v[70:73], v[150:153], v[196:199], v[70:73]
	v_mfma_f32_16x16x32_bf16 v[66:69], v[158:161], v[196:199], v[66:69]
	s_setprio 0
	s_barrier
	s_or_b32 s62, s62, 1
	s_lshl_b64 s[68:69], s[62:63], 7
	s_add_u32 s72, s6, s68
	s_mov_b32 m0, s46
	s_addc_u32 s73, s7, s69
	ds_read_b128 v[162:165], v217 offset:49152
	ds_read_b128 v[166:169], v217 offset:50176
	ds_read_b128 v[170:173], v217 offset:51200
	ds_read_b128 v[174:177], v217 offset:52224
	ds_read_b128 v[178:181], v217 offset:53248
	ds_read_b128 v[182:185], v217 offset:54272
	ds_read_b128 v[186:189], v217 offset:55296
	ds_read_b128 v[196:199], v217 offset:56320
	global_load_lds_dwordx4 v190, s[72:73]
	s_mov_b32 m0, s47
	s_nop 0
	global_load_lds_dwordx4 v216, s[72:73]
	s_add_u32 s72, s61, s68
	s_addc_u32 s73, s67, s69
	s_mov_b32 m0, s50
	s_add_u32 s68, s0, s68
	global_load_lds_dwordx4 v190, s[72:73]
	s_mov_b32 m0, s51
	s_addc_u32 s69, s1, s69
	global_load_lds_dwordx4 v216, s[72:73]
	s_mov_b32 m0, s48
	s_nop 0
	global_load_lds_dwordx4 v194, s[68:69]
	s_mov_b32 m0, s49
	s_nop 0
	global_load_lds_dwordx4 v192, s[68:69]
	s_waitcnt vmcnt(8)
	s_waitcnt lgkmcnt(0)
	s_barrier
	s_setprio 1
	s_waitcnt lgkmcnt(0)
	v_mfma_f32_16x16x32_bf16 v[62:65], v[130:133], v[162:165], v[62:65]
	v_mfma_f32_16x16x32_bf16 v[58:61], v[138:141], v[162:165], v[58:61]
	v_mfma_f32_16x16x32_bf16 v[46:49], v[130:133], v[170:173], v[46:49]
	v_mfma_f32_16x16x32_bf16 v[42:45], v[138:141], v[170:173], v[42:45]
	v_mfma_f32_16x16x32_bf16 v[30:33], v[130:133], v[178:181], v[30:33]
	v_mfma_f32_16x16x32_bf16 v[26:29], v[138:141], v[178:181], v[26:29]
	v_mfma_f32_16x16x32_bf16 v[14:17], v[130:133], v[186:189], v[14:17]
	v_mfma_f32_16x16x32_bf16 v[10:13], v[138:141], v[186:189], v[10:13]
	v_mfma_f32_16x16x32_bf16 v[62:65], v[134:137], v[166:169], v[62:65]
	v_mfma_f32_16x16x32_bf16 v[58:61], v[142:145], v[166:169], v[58:61]
	v_mfma_f32_16x16x32_bf16 v[46:49], v[134:137], v[174:177], v[46:49]
	v_mfma_f32_16x16x32_bf16 v[42:45], v[142:145], v[174:177], v[42:45]
	v_mfma_f32_16x16x32_bf16 v[30:33], v[134:137], v[182:185], v[30:33]
	v_mfma_f32_16x16x32_bf16 v[26:29], v[142:145], v[182:185], v[26:29]
	v_mfma_f32_16x16x32_bf16 v[14:17], v[134:137], v[196:199], v[14:17]
	v_mfma_f32_16x16x32_bf16 v[10:13], v[142:145], v[196:199], v[10:13]
	s_setprio 0
	s_setprio 1
	v_mfma_f32_16x16x32_bf16 v[54:57], v[146:149], v[162:165], v[54:57]
	v_mfma_f32_16x16x32_bf16 v[50:53], v[154:157], v[162:165], v[50:53]
	v_mfma_f32_16x16x32_bf16 v[38:41], v[146:149], v[170:173], v[38:41]
	v_mfma_f32_16x16x32_bf16 v[34:37], v[154:157], v[170:173], v[34:37]
	v_mfma_f32_16x16x32_bf16 v[22:25], v[146:149], v[178:181], v[22:25]
	v_mfma_f32_16x16x32_bf16 v[18:21], v[154:157], v[178:181], v[18:21]
	v_mfma_f32_16x16x32_bf16 v[6:9], v[146:149], v[186:189], v[6:9]
	v_mfma_f32_16x16x32_bf16 v[2:5], v[154:157], v[186:189], v[2:5]
	v_mfma_f32_16x16x32_bf16 v[54:57], v[150:153], v[166:169], v[54:57]
	v_mfma_f32_16x16x32_bf16 v[50:53], v[158:161], v[166:169], v[50:53]
	v_mfma_f32_16x16x32_bf16 v[38:41], v[150:153], v[174:177], v[38:41]
	v_mfma_f32_16x16x32_bf16 v[34:37], v[158:161], v[174:177], v[34:37]
	v_mfma_f32_16x16x32_bf16 v[22:25], v[150:153], v[182:185], v[22:25]
	v_mfma_f32_16x16x32_bf16 v[18:21], v[158:161], v[182:185], v[18:21]
	v_mfma_f32_16x16x32_bf16 v[6:9], v[150:153], v[196:199], v[6:9]
	v_mfma_f32_16x16x32_bf16 v[2:5], v[158:161], v[196:199], v[2:5]
	s_setprio 0
	s_barrier
	s_add_u32 s22, s22, 0x100
	s_addc_u32 s23, s23, 0
	s_cmp_ge_i32 s66, s58
	s_cbranch_scc1 .LBB0_583
	s_mov_b32 s61, s66
	s_mov_b32 s73, 0x10000
	s_branch .LBB0_579
.Lcz1_579:
	v_mfma_f32_16x16x32_bf16 v[122:125], v[130:133], v[162:165], 0
	v_mfma_f32_16x16x32_bf16 v[126:129], v[138:141], v[162:165], 0
	v_mfma_f32_16x16x32_bf16 v[110:113], v[130:133], v[170:173], 0
	v_mfma_f32_16x16x32_bf16 v[106:109], v[138:141], v[170:173], 0
	v_mfma_f32_16x16x32_bf16 v[94:97], v[130:133], v[178:181], 0
	v_mfma_f32_16x16x32_bf16 v[90:93], v[138:141], v[178:181], 0
	v_mfma_f32_16x16x32_bf16 v[78:81], v[130:133], v[186:189], 0
	v_mfma_f32_16x16x32_bf16 v[74:77], v[138:141], v[186:189], 0
	v_mfma_f32_16x16x32_bf16 v[122:125], v[134:137], v[166:169], v[122:125]
	v_mfma_f32_16x16x32_bf16 v[126:129], v[142:145], v[166:169], v[126:129]
	v_mfma_f32_16x16x32_bf16 v[110:113], v[134:137], v[174:177], v[110:113]
	v_mfma_f32_16x16x32_bf16 v[106:109], v[142:145], v[174:177], v[106:109]
	v_mfma_f32_16x16x32_bf16 v[94:97], v[134:137], v[182:185], v[94:97]
	v_mfma_f32_16x16x32_bf16 v[90:93], v[142:145], v[182:185], v[90:93]
	v_mfma_f32_16x16x32_bf16 v[78:81], v[134:137], v[196:199], v[78:81]
	v_mfma_f32_16x16x32_bf16 v[74:77], v[142:145], v[196:199], v[74:77]
	s_setprio 0
	s_setprio 1
	v_mfma_f32_16x16x32_bf16 v[118:121], v[146:149], v[162:165], 0
	v_mfma_f32_16x16x32_bf16 v[114:117], v[154:157], v[162:165], 0
	v_mfma_f32_16x16x32_bf16 v[102:105], v[146:149], v[170:173], 0
	v_mfma_f32_16x16x32_bf16 v[98:101], v[154:157], v[170:173], 0
	v_mfma_f32_16x16x32_bf16 v[86:89], v[146:149], v[178:181], 0
	v_mfma_f32_16x16x32_bf16 v[82:85], v[154:157], v[178:181], 0
	v_mfma_f32_16x16x32_bf16 v[70:73], v[146:149], v[186:189], 0
	v_mfma_f32_16x16x32_bf16 v[66:69], v[154:157], v[186:189], 0
	v_mfma_f32_16x16x32_bf16 v[118:121], v[150:153], v[166:169], v[118:121]
	v_mfma_f32_16x16x32_bf16 v[114:117], v[158:161], v[166:169], v[114:117]
	v_mfma_f32_16x16x32_bf16 v[102:105], v[150:153], v[174:177], v[102:105]
	v_mfma_f32_16x16x32_bf16 v[98:101], v[158:161], v[174:177], v[98:101]
	v_mfma_f32_16x16x32_bf16 v[86:89], v[150:153], v[182:185], v[86:89]
	v_mfma_f32_16x16x32_bf16 v[82:85], v[158:161], v[182:185], v[82:85]
	v_mfma_f32_16x16x32_bf16 v[70:73], v[150:153], v[196:199], v[70:73]
	v_mfma_f32_16x16x32_bf16 v[66:69], v[158:161], v[196:199], v[66:69]
	s_branch .Lcj1_579
.Lcz2_579:
	v_mfma_f32_16x16x32_bf16 v[62:65], v[130:133], v[162:165], 0
	v_mfma_f32_16x16x32_bf16 v[58:61], v[138:141], v[162:165], 0
	v_mfma_f32_16x16x32_bf16 v[46:49], v[130:133], v[170:173], 0
	v_mfma_f32_16x16x32_bf16 v[42:45], v[138:141], v[170:173], 0
	v_mfma_f32_16x16x32_bf16 v[30:33], v[130:133], v[178:181], 0
	v_mfma_f32_16x16x32_bf16 v[26:29], v[138:141], v[178:181], 0
	v_mfma_f32_16x16x32_bf16 v[14:17], v[130:133], v[186:189], 0
	v_mfma_f32_16x16x32_bf16 v[10:13], v[138:141], v[186:189], 0
	v_mfma_f32_16x16x32_bf16 v[62:65], v[134:137], v[166:169], v[62:65]
	v_mfma_f32_16x16x32_bf16 v[58:61], v[142:145], v[166:169], v[58:61]
	v_mfma_f32_16x16x32_bf16 v[46:49], v[134:137], v[174:177], v[46:49]
	v_mfma_f32_16x16x32_bf16 v[42:45], v[142:145], v[174:177], v[42:45]
	v_mfma_f32_16x16x32_bf16 v[30:33], v[134:137], v[182:185], v[30:33]
	v_mfma_f32_16x16x32_bf16 v[26:29], v[142:145], v[182:185], v[26:29]
	v_mfma_f32_16x16x32_bf16 v[14:17], v[134:137], v[196:199], v[14:17]
	v_mfma_f32_16x16x32_bf16 v[10:13], v[142:145], v[196:199], v[10:13]
	s_setprio 0
	s_setprio 1
	v_mfma_f32_16x16x32_bf16 v[54:57], v[146:149], v[162:165], 0
	v_mfma_f32_16x16x32_bf16 v[50:53], v[154:157], v[162:165], 0
	v_mfma_f32_16x16x32_bf16 v[38:41], v[146:149], v[170:173], 0
	v_mfma_f32_16x16x32_bf16 v[34:37], v[154:157], v[170:173], 0
	v_mfma_f32_16x16x32_bf16 v[22:25], v[146:149], v[178:181], 0
	v_mfma_f32_16x16x32_bf16 v[18:21], v[154:157], v[178:181], 0
	v_mfma_f32_16x16x32_bf16 v[6:9], v[146:149], v[186:189], 0
	v_mfma_f32_16x16x32_bf16 v[2:5], v[154:157], v[186:189], 0
	v_mfma_f32_16x16x32_bf16 v[54:57], v[150:153], v[166:169], v[54:57]
	v_mfma_f32_16x16x32_bf16 v[50:53], v[158:161], v[166:169], v[50:53]
	v_mfma_f32_16x16x32_bf16 v[38:41], v[150:153], v[174:177], v[38:41]
	v_mfma_f32_16x16x32_bf16 v[34:37], v[158:161], v[174:177], v[34:37]
	v_mfma_f32_16x16x32_bf16 v[22:25], v[150:153], v[182:185], v[22:25]
	v_mfma_f32_16x16x32_bf16 v[18:21], v[158:161], v[182:185], v[18:21]
	v_mfma_f32_16x16x32_bf16 v[6:9], v[150:153], v[196:199], v[6:9]
	v_mfma_f32_16x16x32_bf16 v[2:5], v[158:161], v[196:199], v[2:5]
	s_mov_b32 s100, 0
	s_branch .Lcj2_579

.LBB0_660:
	s_mov_b64 s[22:23], 0
	s_add_u32 s0, s0, s22
	s_addc_u32 s1, s1, s23
	s_add_u32 s4, s4, s22
	s_addc_u32 s5, s5, s23
	s_mov_b32 s52, 16
	s_cmp_lt_i32 s52, 1
	s_cbranch_scc1 .LBB0_671
	s_ashr_i32 s19, s18, 31
	s_lshl_b64 s[22:23], s[18:19], 19
	s_add_u32 s19, s27, s22
	s_addc_u32 s53, s28, s23
	s_ashr_i32 s17, s16, 31
	s_lshl_b64 s[22:23], s[16:17], 19
	s_add_u32 s17, s29, s22
	s_addc_u32 s54, s30, s23
	s_mov_b32 s55, 2
	s_mov_b64 s[22:23], 0x40080
	s_mov_b32 s100, 1
.LBB0_662:
	v_add_u32_e32 v142, 0x10000, v191
	v_add_u32_e32 v158, 0x14000, v191
	ds_read_b128 v[130:133], v142
	ds_read_b128 v[134:137], v142 offset:1024
	ds_read_b128 v[138:141], v142 offset:2048
	ds_read_b128 v[142:145], v142 offset:3072
	ds_read_b128 v[146:149], v158
	ds_read_b128 v[150:153], v158 offset:1024
	ds_read_b128 v[154:157], v158 offset:2048
	ds_read_b128 v[158:161], v158 offset:3072
	s_add_i32 m0, s31, 0xc000
	s_add_i32 s58, s31, 0xe000
	s_cmp_eq_u32 s52, s55
	s_cselect_b64 s[56:57], -1, 0
	v_lshl_add_u64 v[200:201], s[0:1], 0, v[194:195]
	v_lshl_add_u64 v[200:201], v[200:201], 0, s[22:23]
	v_mov_b32_e32 v193, v195
	ds_read_b128 v[162:165], v217
	ds_read_b128 v[166:169], v217 offset:1024
	ds_read_b128 v[170:173], v217 offset:2048
	ds_read_b128 v[174:177], v217 offset:3072
	ds_read_b128 v[178:181], v217 offset:4096
	ds_read_b128 v[182:185], v217 offset:5120
	ds_read_b128 v[186:189], v217 offset:6144
	ds_read_b128 v[196:199], v217 offset:7168
	global_load_lds_dwordx4 v[200:201], off
	v_lshl_add_u64 v[200:201], s[0:1], 0, v[192:193]
	v_lshl_add_u64 v[200:201], v[200:201], 0, s[22:23]
	s_mov_b32 m0, s58
	s_nop 0
	global_load_lds_dwordx4 v[200:201], off
	s_cmp_lg_u32 s100, 0
	s_waitcnt vmcnt(8)
	s_waitcnt lgkmcnt(0)
	s_barrier
	s_setprio 1
	s_waitcnt lgkmcnt(0)
	s_cbranch_scc1 .Lcz1_662
	v_mfma_f32_16x16x32_bf16 v[126:129], v[130:133], v[162:165], v[126:129]
	v_mfma_f32_16x16x32_bf16 v[122:125], v[138:141], v[162:165], v[122:125]
	v_mfma_f32_16x16x32_bf16 v[110:113], v[130:133], v[170:173], v[110:113]
	v_mfma_f32_16x16x32_bf16 v[106:109], v[138:141], v[170:173], v[106:109]
	v_mfma_f32_16x16x32_bf16 v[94:97], v[130:133], v[178:181], v[94:97]
	v_mfma_f32_16x16x32_bf16 v[90:93], v[138:141], v[178:181], v[90:93]
	v_mfma_f32_16x16x32_bf16 v[78:81], v[130:133], v[186:189], v[78:81]
	v_mfma_f32_16x16x32_bf16 v[74:77], v[138:141], v[186:189], v[74:77]
	v_mfma_f32_16x16x32_bf16 v[126:129], v[134:137], v[166:169], v[126:129]
	v_mfma_f32_16x16x32_bf16 v[122:125], v[142:145], v[166:169], v[122:125]
	v_mfma_f32_16x16x32_bf16 v[110:113], v[134:137], v[174:177], v[110:113]
	v_mfma_f32_16x16x32_bf16 v[106:109], v[142:145], v[174:177], v[106:109]
	v_mfma_f32_16x16x32_bf16 v[94:97], v[134:137], v[182:185], v[94:97]
	v_mfma_f32_16x16x32_bf16 v[90:93], v[142:145], v[182:185], v[90:93]
	v_mfma_f32_16x16x32_bf16 v[78:81], v[134:137], v[196:199], v[78:81]
	v_mfma_f32_16x16x32_bf16 v[74:77], v[142:145], v[196:199], v[74:77]
	s_setprio 0
	s_setprio 1
	v_mfma_f32_16x16x32_bf16 v[118:121], v[146:149], v[162:165], v[118:121]
	v_mfma_f32_16x16x32_bf16 v[114:117], v[154:157], v[162:165], v[114:117]
	v_mfma_f32_16x16x32_bf16 v[102:105], v[146:149], v[170:173], v[102:105]
	v_mfma_f32_16x16x32_bf16 v[98:101], v[154:157], v[170:173], v[98:101]
	v_mfma_f32_16x16x32_bf16 v[86:89], v[146:149], v[178:181], v[86:89]
	v_mfma_f32_16x16x32_bf16 v[82:85], v[154:157], v[178:181], v[82:85]
	v_mfma_f32_16x16x32_bf16 v[70:73], v[146:149], v[186:189], v[70:73]
	v_mfma_f32_16x16x32_bf16 v[66:69], v[154:157], v[186:189], v[66:69]
	v_mfma_f32_16x16x32_bf16 v[118:121], v[150:153], v[166:169], v[118:121]
	v_mfma_f32_16x16x32_bf16 v[114:117], v[158:161], v[166:169], v[114:117]
	v_mfma_f32_16x16x32_bf16 v[102:105], v[150:153], v[174:177], v[102:105]
	v_mfma_f32_16x16x32_bf16 v[98:101], v[158:161], v[174:177], v[98:101]
	v_mfma_f32_16x16x32_bf16 v[86:89], v[150:153], v[182:185], v[86:89]
	v_mfma_f32_16x16x32_bf16 v[82:85], v[158:161], v[182:185], v[82:85]
	v_mfma_f32_16x16x32_bf16 v[70:73], v[150:153], v[196:199], v[70:73]
	v_mfma_f32_16x16x32_bf16 v[66:69], v[158:161], v[196:199], v[66:69]
.Lcj1_662:
	s_setprio 0
	s_barrier
	s_and_b64 s[58:59], s[56:57], exec
	s_cselect_b32 s62, 0, s55
	s_and_b64 s[56:57], s[2:3], s[56:57]
	s_and_b64 s[56:57], s[56:57], exec
	s_cselect_b32 s5, s54, s5
	s_cselect_b32 s4, s17, s4
	s_cselect_b32 s1, s53, s1
	s_cselect_b32 s0, s19, s0
	s_lshl_b64 s[56:57], s[62:63], 7
	s_add_u32 s58, s4, s56
	s_addc_u32 s59, s5, s57
	s_mov_b32 m0, s37
	s_add_u32 s60, s4, 0x40000
	ds_read_b128 v[162:165], v217 offset:16384
	ds_read_b128 v[166:169], v217 offset:17408
	ds_read_b128 v[170:173], v217 offset:18432
	ds_read_b128 v[174:177], v217 offset:19456
	ds_read_b128 v[178:181], v217 offset:20480
	ds_read_b128 v[182:185], v217 offset:21504
	ds_read_b128 v[186:189], v217 offset:22528
	ds_read_b128 v[196:199], v217 offset:23552
	global_load_lds_dwordx4 v190, s[58:59]
	s_mov_b32 m0, s38
	s_addc_u32 s61, s5, 0
	global_load_lds_dwordx4 v216, s[58:59]
	s_add_u32 s58, s60, s56
	s_addc_u32 s59, s61, s57
	s_mov_b32 m0, s39
	s_add_u32 s56, s0, s56
	global_load_lds_dwordx4 v190, s[58:59]
	s_mov_b32 m0, s40
	s_addc_u32 s57, s1, s57
	global_load_lds_dwordx4 v216, s[58:59]
	s_mov_b32 m0, s31
	s_nop 0
	global_load_lds_dwordx4 v194, s[56:57]
	s_mov_b32 m0, s41
	s_nop 0
	global_load_lds_dwordx4 v192, s[56:57]
	s_cmp_lg_u32 s100, 0
	s_waitcnt vmcnt(8)
	s_waitcnt lgkmcnt(0)
	s_barrier
	s_setprio 1
	s_waitcnt lgkmcnt(0)
	s_cbranch_scc1 .Lcz2_662
	v_mfma_f32_16x16x32_bf16 v[62:65], v[130:133], v[162:165], v[62:65]
	v_mfma_f32_16x16x32_bf16 v[58:61], v[138:141], v[162:165], v[58:61]
	v_mfma_f32_16x16x32_bf16 v[46:49], v[130:133], v[170:173], v[46:49]
	v_mfma_f32_16x16x32_bf16 v[42:45], v[138:141], v[170:173], v[42:45]
	v_mfma_f32_16x16x32_bf16 v[30:33], v[130:133], v[178:181], v[30:33]
	v_mfma_f32_16x16x32_bf16 v[26:29], v[138:141], v[178:181], v[26:29]
	v_mfma_f32_16x16x32_bf16 v[14:17], v[130:133], v[186:189], v[14:17]
	v_mfma_f32_16x16x32_bf16 v[10:13], v[138:141], v[186:189], v[10:13]
	v_mfma_f32_16x16x32_bf16 v[62:65], v[134:137], v[166:169], v[62:65]
	v_mfma_f32_16x16x32_bf16 v[58:61], v[142:145], v[166:169], v[58:61]
	v_mfma_f32_16x16x32_bf16 v[46:49], v[134:137], v[174:177], v[46:49]
	v_mfma_f32_16x16x32_bf16 v[42:45], v[142:145], v[174:177], v[42:45]
	v_mfma_f32_16x16x32_bf16 v[30:33], v[134:137], v[182:185], v[30:33]
	v_mfma_f32_16x16x32_bf16 v[26:29], v[142:145], v[182:185], v[26:29]
	v_mfma_f32_16x16x32_bf16 v[14:17], v[134:137], v[196:199], v[14:17]
	v_mfma_f32_16x16x32_bf16 v[10:13], v[142:145], v[196:199], v[10:13]
	s_setprio 0
	s_setprio 1
	v_mfma_f32_16x16x32_bf16 v[54:57], v[146:149], v[162:165], v[54:57]
	v_mfma_f32_16x16x32_bf16 v[50:53], v[154:157], v[162:165], v[50:53]
	v_mfma_f32_16x16x32_bf16 v[38:41], v[146:149], v[170:173], v[38:41]
	v_mfma_f32_16x16x32_bf16 v[34:37], v[154:157], v[170:173], v[34:37]
	v_mfma_f32_16x16x32_bf16 v[22:25], v[146:149], v[178:181], v[22:25]
	v_mfma_f32_16x16x32_bf16 v[18:21], v[154:157], v[178:181], v[18:21]
	v_mfma_f32_16x16x32_bf16 v[6:9], v[146:149], v[186:189], v[6:9]
	v_mfma_f32_16x16x32_bf16 v[2:5], v[154:157], v[186:189], v[2:5]
	v_mfma_f32_16x16x32_bf16 v[54:57], v[150:153], v[166:169], v[54:57]
	v_mfma_f32_16x16x32_bf16 v[50:53], v[158:161], v[166:169], v[50:53]
	v_mfma_f32_16x16x32_bf16 v[38:41], v[150:153], v[174:177], v[38:41]
	v_mfma_f32_16x16x32_bf16 v[34:37], v[158:161], v[174:177], v[34:37]
	v_mfma_f32_16x16x32_bf16 v[22:25], v[150:153], v[182:185], v[22:25]
	v_mfma_f32_16x16x32_bf16 v[18:21], v[158:161], v[182:185], v[18:21]
	v_mfma_f32_16x16x32_bf16 v[6:9], v[150:153], v[196:199], v[6:9]
	v_mfma_f32_16x16x32_bf16 v[2:5], v[158:161], v[196:199], v[2:5]
.Lcj2_662:
	s_setprio 0
	s_barrier
	v_add_u32_e32 v142, 0x18000, v191
	v_add_u32_e32 v158, 0x1c000, v191
	ds_read_b128 v[130:133], v142
	ds_read_b128 v[134:137], v142 offset:1024
	ds_read_b128 v[138:141], v142 offset:2048
	ds_read_b128 v[142:145], v142 offset:3072
	ds_read_b128 v[146:149], v158
	ds_read_b128 v[150:153], v158 offset:1024
	ds_read_b128 v[154:157], v158 offset:2048
	ds_read_b128 v[158:161], v158 offset:3072
	s_add_u32 s56, s56, 0x40000
	s_addc_u32 s57, s57, 0
	s_mov_b32 m0, s42
	ds_read_b128 v[162:165], v217 offset:32768
	ds_read_b128 v[166:169], v217 offset:33792
	ds_read_b128 v[170:173], v217 offset:34816
	ds_read_b128 v[174:177], v217 offset:35840
	ds_read_b128 v[178:181], v217 offset:36864
	ds_read_b128 v[182:185], v217 offset:37888
	ds_read_b128 v[186:189], v217 offset:38912
	ds_read_b128 v[196:199], v217 offset:39936
	global_load_lds_dwordx4 v194, s[56:57]
	s_mov_b32 m0, s43
	s_nop 0
	global_load_lds_dwordx4 v192, s[56:57]
	s_waitcnt vmcnt(8)
	s_waitcnt lgkmcnt(0)
	s_barrier
	s_setprio 1
	s_waitcnt lgkmcnt(0)
	v_mfma_f32_16x16x32_bf16 v[126:129], v[130:133], v[162:165], v[126:129]
	v_mfma_f32_16x16x32_bf16 v[122:125], v[138:141], v[162:165], v[122:125]
	v_mfma_f32_16x16x32_bf16 v[110:113], v[130:133], v[170:173], v[110:113]
	v_mfma_f32_16x16x32_bf16 v[106:109], v[138:141], v[170:173], v[106:109]
	v_mfma_f32_16x16x32_bf16 v[94:97], v[130:133], v[178:181], v[94:97]
	v_mfma_f32_16x16x32_bf16 v[90:93], v[138:141], v[178:181], v[90:93]
	v_mfma_f32_16x16x32_bf16 v[78:81], v[130:133], v[186:189], v[78:81]
	v_mfma_f32_16x16x32_bf16 v[74:77], v[138:141], v[186:189], v[74:77]
	v_mfma_f32_16x16x32_bf16 v[126:129], v[134:137], v[166:169], v[126:129]
	v_mfma_f32_16x16x32_bf16 v[122:125], v[142:145], v[166:169], v[122:125]
	v_mfma_f32_16x16x32_bf16 v[110:113], v[134:137], v[174:177], v[110:113]
	v_mfma_f32_16x16x32_bf16 v[106:109], v[142:145], v[174:177], v[106:109]
	v_mfma_f32_16x16x32_bf16 v[94:97], v[134:137], v[182:185], v[94:97]
	v_mfma_f32_16x16x32_bf16 v[90:93], v[142:145], v[182:185], v[90:93]
	v_mfma_f32_16x16x32_bf16 v[78:81], v[134:137], v[196:199], v[78:81]
	v_mfma_f32_16x16x32_bf16 v[74:77], v[142:145], v[196:199], v[74:77]
	s_setprio 0
	s_setprio 1
	v_mfma_f32_16x16x32_bf16 v[118:121], v[146:149], v[162:165], v[118:121]
	v_mfma_f32_16x16x32_bf16 v[114:117], v[154:157], v[162:165], v[114:117]
	v_mfma_f32_16x16x32_bf16 v[102:105], v[146:149], v[170:173], v[102:105]
	v_mfma_f32_16x16x32_bf16 v[98:101], v[154:157], v[170:173], v[98:101]
	v_mfma_f32_16x16x32_bf16 v[86:89], v[146:149], v[178:181], v[86:89]
	v_mfma_f32_16x16x32_bf16 v[82:85], v[154:157], v[178:181], v[82:85]
	v_mfma_f32_16x16x32_bf16 v[70:73], v[146:149], v[186:189], v[70:73]
	v_mfma_f32_16x16x32_bf16 v[66:69], v[154:157], v[186:189], v[66:69]
	v_mfma_f32_16x16x32_bf16 v[118:121], v[150:153], v[166:169], v[118:121]
	v_mfma_f32_16x16x32_bf16 v[114:117], v[158:161], v[166:169], v[114:117]
	v_mfma_f32_16x16x32_bf16 v[102:105], v[150:153], v[174:177], v[102:105]
	v_mfma_f32_16x16x32_bf16 v[98:101], v[158:161], v[174:177], v[98:101]
	v_mfma_f32_16x16x32_bf16 v[86:89], v[150:153], v[182:185], v[86:89]
	v_mfma_f32_16x16x32_bf16 v[82:85], v[158:161], v[182:185], v[82:85]
	v_mfma_f32_16x16x32_bf16 v[70:73], v[150:153], v[196:199], v[70:73]
	v_mfma_f32_16x16x32_bf16 v[66:69], v[158:161], v[196:199], v[66:69]
	s_setprio 0
	s_barrier
	s_or_b32 s62, s62, 1
	s_lshl_b64 s[56:57], s[62:63], 7
	s_add_u32 s58, s4, s56
	s_mov_b32 m0, s45
	s_addc_u32 s59, s5, s57
	ds_read_b128 v[162:165], v217 offset:49152
	ds_read_b128 v[166:169], v217 offset:50176
	ds_read_b128 v[170:173], v217 offset:51200
	ds_read_b128 v[174:177], v217 offset:52224
	ds_read_b128 v[178:181], v217 offset:53248
	ds_read_b128 v[182:185], v217 offset:54272
	ds_read_b128 v[186:189], v217 offset:55296
	ds_read_b128 v[196:199], v217 offset:56320
	global_load_lds_dwordx4 v190, s[58:59]
	s_mov_b32 m0, s46
	s_nop 0
	global_load_lds_dwordx4 v216, s[58:59]
	s_add_u32 s58, s60, s56
	s_addc_u32 s59, s61, s57
	s_mov_b32 m0, s49
	s_add_u32 s56, s0, s56
	global_load_lds_dwordx4 v190, s[58:59]
	s_mov_b32 m0, s50
	s_addc_u32 s57, s1, s57
	global_load_lds_dwordx4 v216, s[58:59]
	s_mov_b32 m0, s47
	s_nop 0
	global_load_lds_dwordx4 v194, s[56:57]
	s_mov_b32 m0, s48
	s_nop 0
	global_load_lds_dwordx4 v192, s[56:57]
	s_waitcnt vmcnt(8)
	s_waitcnt lgkmcnt(0)
	s_barrier
	s_setprio 1
	s_waitcnt lgkmcnt(0)
	v_mfma_f32_16x16x32_bf16 v[62:65], v[130:133], v[162:165], v[62:65]
	v_mfma_f32_16x16x32_bf16 v[58:61], v[138:141], v[162:165], v[58:61]
	v_mfma_f32_16x16x32_bf16 v[46:49], v[130:133], v[170:173], v[46:49]
	v_mfma_f32_16x16x32_bf16 v[42:45], v[138:141], v[170:173], v[42:45]
	v_mfma_f32_16x16x32_bf16 v[30:33], v[130:133], v[178:181], v[30:33]
	v_mfma_f32_16x16x32_bf16 v[26:29], v[138:141], v[178:181], v[26:29]
	v_mfma_f32_16x16x32_bf16 v[14:17], v[130:133], v[186:189], v[14:17]
	v_mfma_f32_16x16x32_bf16 v[10:13], v[138:141], v[186:189], v[10:13]
	v_mfma_f32_16x16x32_bf16 v[62:65], v[134:137], v[166:169], v[62:65]
	v_mfma_f32_16x16x32_bf16 v[58:61], v[142:145], v[166:169], v[58:61]
	v_mfma_f32_16x16x32_bf16 v[46:49], v[134:137], v[174:177], v[46:49]
	v_mfma_f32_16x16x32_bf16 v[42:45], v[142:145], v[174:177], v[42:45]
	v_mfma_f32_16x16x32_bf16 v[30:33], v[134:137], v[182:185], v[30:33]
	v_mfma_f32_16x16x32_bf16 v[26:29], v[142:145], v[182:185], v[26:29]
	v_mfma_f32_16x16x32_bf16 v[14:17], v[134:137], v[196:199], v[14:17]
	v_mfma_f32_16x16x32_bf16 v[10:13], v[142:145], v[196:199], v[10:13]
	s_setprio 0
	s_setprio 1
	v_mfma_f32_16x16x32_bf16 v[54:57], v[146:149], v[162:165], v[54:57]
	v_mfma_f32_16x16x32_bf16 v[50:53], v[154:157], v[162:165], v[50:53]
	v_mfma_f32_16x16x32_bf16 v[38:41], v[146:149], v[170:173], v[38:41]
	v_mfma_f32_16x16x32_bf16 v[34:37], v[154:157], v[170:173], v[34:37]
	v_mfma_f32_16x16x32_bf16 v[22:25], v[146:149], v[178:181], v[22:25]
	v_mfma_f32_16x16x32_bf16 v[18:21], v[154:157], v[178:181], v[18:21]
	v_mfma_f32_16x16x32_bf16 v[6:9], v[146:149], v[186:189], v[6:9]
	v_mfma_f32_16x16x32_bf16 v[2:5], v[154:157], v[186:189], v[2:5]
	v_mfma_f32_16x16x32_bf16 v[54:57], v[150:153], v[166:169], v[54:57]
	v_mfma_f32_16x16x32_bf16 v[50:53], v[158:161], v[166:169], v[50:53]
	v_mfma_f32_16x16x32_bf16 v[38:41], v[150:153], v[174:177], v[38:41]
	v_mfma_f32_16x16x32_bf16 v[34:37], v[158:161], v[174:177], v[34:37]
	v_mfma_f32_16x16x32_bf16 v[22:25], v[150:153], v[182:185], v[22:25]
	v_mfma_f32_16x16x32_bf16 v[18:21], v[158:161], v[182:185], v[18:21]
	v_mfma_f32_16x16x32_bf16 v[6:9], v[150:153], v[196:199], v[6:9]
	v_mfma_f32_16x16x32_bf16 v[2:5], v[158:161], v[196:199], v[2:5]
	s_setprio 0
	s_barrier
	s_add_i32 s56, s55, 2
	s_add_u32 s22, s22, 0x100
	s_addc_u32 s23, s23, 0
	s_cmp_ge_i32 s55, s52
	s_mov_b32 s55, s56
	s_cbranch_scc0 .LBB0_662
	s_branch .Lcsk_662
.Lcz1_662:
	v_mfma_f32_16x16x32_bf16 v[126:129], v[130:133], v[162:165], 0
	v_mfma_f32_16x16x32_bf16 v[122:125], v[138:141], v[162:165], 0
	v_mfma_f32_16x16x32_bf16 v[110:113], v[130:133], v[170:173], 0
	v_mfma_f32_16x16x32_bf16 v[106:109], v[138:141], v[170:173], 0
	v_mfma_f32_16x16x32_bf16 v[94:97], v[130:133], v[178:181], 0
	v_mfma_f32_16x16x32_bf16 v[90:93], v[138:141], v[178:181], 0
	v_mfma_f32_16x16x32_bf16 v[78:81], v[130:133], v[186:189], 0
	v_mfma_f32_16x16x32_bf16 v[74:77], v[138:141], v[186:189], 0
	v_mfma_f32_16x16x32_bf16 v[126:129], v[134:137], v[166:169], v[126:129]
	v_mfma_f32_16x16x32_bf16 v[122:125], v[142:145], v[166:169], v[122:125]
	v_mfma_f32_16x16x32_bf16 v[110:113], v[134:137], v[174:177], v[110:113]
	v_mfma_f32_16x16x32_bf16 v[106:109], v[142:145], v[174:177], v[106:109]
	v_mfma_f32_16x16x32_bf16 v[94:97], v[134:137], v[182:185], v[94:97]
	v_mfma_f32_16x16x32_bf16 v[90:93], v[142:145], v[182:185], v[90:93]
	v_mfma_f32_16x16x32_bf16 v[78:81], v[134:137], v[196:199], v[78:81]
	v_mfma_f32_16x16x32_bf16 v[74:77], v[142:145], v[196:199], v[74:77]
	s_setprio 0
	s_setprio 1
	v_mfma_f32_16x16x32_bf16 v[118:121], v[146:149], v[162:165], 0
	v_mfma_f32_16x16x32_bf16 v[114:117], v[154:157], v[162:165], 0
	v_mfma_f32_16x16x32_bf16 v[102:105], v[146:149], v[170:173], 0
	v_mfma_f32_16x16x32_bf16 v[98:101], v[154:157], v[170:173], 0
	v_mfma_f32_16x16x32_bf16 v[86:89], v[146:149], v[178:181], 0
	v_mfma_f32_16x16x32_bf16 v[82:85], v[154:157], v[178:181], 0
	v_mfma_f32_16x16x32_bf16 v[70:73], v[146:149], v[186:189], 0
	v_mfma_f32_16x16x32_bf16 v[66:69], v[154:157], v[186:189], 0
	v_mfma_f32_16x16x32_bf16 v[118:121], v[150:153], v[166:169], v[118:121]
	v_mfma_f32_16x16x32_bf16 v[114:117], v[158:161], v[166:169], v[114:117]
	v_mfma_f32_16x16x32_bf16 v[102:105], v[150:153], v[174:177], v[102:105]
	v_mfma_f32_16x16x32_bf16 v[98:101], v[158:161], v[174:177], v[98:101]
	v_mfma_f32_16x16x32_bf16 v[86:89], v[150:153], v[182:185], v[86:89]
	v_mfma_f32_16x16x32_bf16 v[82:85], v[158:161], v[182:185], v[82:85]
	v_mfma_f32_16x16x32_bf16 v[70:73], v[150:153], v[196:199], v[70:73]
	v_mfma_f32_16x16x32_bf16 v[66:69], v[158:161], v[196:199], v[66:69]
	s_branch .Lcj1_662

.Lcsk_662:
	s_and_b64 vcc, exec, s[14:15]
	s_cbranch_vccz .LBB0_665
.LBB0_664:
	s_barrier

.LBB0_959:
	s_add_u32 s20, s20, s24
	s_addc_u32 s21, s21, s25
	s_mov_b32 s19, 8
	s_cmp_lt_i32 s19, 1
	s_cbranch_scc1 .LBB0_965
	s_and_b64 s[24:25], exec, s[4:5]
	s_cselect_b32 s25, s21, s7
	s_cselect_b32 s24, s20, s6
	s_mov_b32 s60, 2
	s_mov_b64 s[26:27], 0x80
	s_mov_b32 s100, 1
.LBB0_961:
	v_add_u32_e32 v2, 0x10000, v167
	v_add_u32_e32 v14, 0x14000, v167
	ds_read_b128 v[18:21], v2
	ds_read_b128 v[22:25], v2 offset:1024
	ds_read_b128 v[26:29], v2 offset:2048
	ds_read_b128 v[30:33], v2 offset:3072
	ds_read_b128 v[2:5], v14
	ds_read_b128 v[6:9], v14 offset:1024
	ds_read_b128 v[10:13], v14 offset:2048
	ds_read_b128 v[14:17], v14 offset:3072
	s_add_i32 m0, s41, 0xc000
	s_add_i32 s28, s41, 0xe000
	s_cmp_lg_u32 s19, s60
	s_cselect_b64 s[30:31], -1, 0
	v_lshl_add_u64 v[188:189], s[20:21], 0, v[194:195]
	v_lshl_add_u64 v[188:189], v[188:189], 0, s[26:27]
	v_mov_b32_e32 v169, v195
	ds_read_b128 v[180:183], v170
	ds_read_b128 v[184:187], v170 offset:1024
	ds_read_b128 v[216:219], v170 offset:2048
	ds_read_b128 v[220:223], v170 offset:3072
	ds_read_b128 v[224:227], v170 offset:4096
	ds_read_b128 v[228:231], v170 offset:5120
	ds_read_b128 v[196:199], v170 offset:6144
	ds_read_b128 v[200:203], v170 offset:7168
	global_load_lds_dwordx4 v[188:189], off
	v_lshl_add_u64 v[188:189], s[20:21], 0, v[168:169]
	v_lshl_add_u64 v[188:189], v[188:189], 0, s[26:27]
	s_mov_b32 m0, s28
	s_nop 0
	global_load_lds_dwordx4 v[188:189], off
	s_cmp_lg_u32 s100, 0
	s_waitcnt vmcnt(8)
	s_waitcnt lgkmcnt(0)
	s_barrier
	s_setprio 1
	s_waitcnt lgkmcnt(0)
	s_cbranch_scc1 .Lcz1_961
	v_mfma_f32_16x16x128_f8f6f4 v[146:149], v[18:25], v[180:187], v[146:149]
	v_mfma_f32_16x16x128_f8f6f4 v[158:161], v[26:33], v[180:187], v[158:161]
	v_mfma_f32_16x16x128_f8f6f4 v[142:145], v[18:25], v[216:223], v[142:145]
	v_mfma_f32_16x16x128_f8f6f4 v[138:141], v[26:33], v[216:223], v[138:141]
	v_mfma_f32_16x16x128_f8f6f4 v[126:129], v[18:25], v[224:231], v[126:129]
	v_mfma_f32_16x16x128_f8f6f4 v[122:125], v[26:33], v[224:231], v[122:125]
	v_mfma_f32_16x16x128_f8f6f4 v[110:113], v[18:25], v[196:203], v[110:113]
	v_mfma_f32_16x16x128_f8f6f4 v[106:109], v[26:33], v[196:203], v[106:109]
	s_setprio 0
	s_setprio 1
	v_mfma_f32_16x16x128_f8f6f4 v[154:157], v[2:9], v[180:187], v[154:157]
	v_mfma_f32_16x16x128_f8f6f4 v[150:153], v[10:17], v[180:187], v[150:153]
	v_mfma_f32_16x16x128_f8f6f4 v[134:137], v[2:9], v[216:223], v[134:137]
	v_mfma_f32_16x16x128_f8f6f4 v[130:133], v[10:17], v[216:223], v[130:133]
	v_mfma_f32_16x16x128_f8f6f4 v[118:121], v[2:9], v[224:231], v[118:121]
	v_mfma_f32_16x16x128_f8f6f4 v[114:117], v[10:17], v[224:231], v[114:117]
	v_mfma_f32_16x16x128_f8f6f4 v[102:105], v[2:9], v[196:203], v[102:105]
	v_mfma_f32_16x16x128_f8f6f4 v[98:101], v[10:17], v[196:203], v[98:101]
.Lcj1_961:
	s_setprio 0
	s_barrier
	s_and_b64 s[28:29], s[30:31], exec
	s_cselect_b32 s28, s60, 0
	s_or_b64 s[30:31], s[4:5], s[30:31]
	s_or_b64 s[66:67], s[30:31], s[22:23]
	s_and_b64 s[30:31], s[30:31], exec
	s_cselect_b32 s13, s13, s1
	s_cselect_b32 s12, s12, s0
	s_cselect_b32 s21, s21, s7
	s_cselect_b32 s20, s20, s6
	s_and_b64 vcc, exec, s[66:67]
	s_cbranch_vccnz .LBB0_963
	v_mov_b32_e32 v164, v0
	s_mov_b32 s28, 0
	v_ashrrev_i32_e32 v168, 31, v164
	v_lshrrev_b32_e32 v168, 26, v168
	v_lshlrev_b32_e32 v166, 4, v164
	v_add_u32_e32 v168, v164, v168
	v_bfe_i32 v164, v164, 27, 1
	v_lshrrev_b32_e32 v164, 22, v164
	v_add_u32_e32 v164, v166, v164
	v_and_b32_e32 v164, 0xfffffc00, v164
	v_sub_u32_e32 v164, v166, v164
	v_lshrrev_b32_e32 v169, 4, v164
	v_bitop3_b32 v169, v169, v164, 32 bitop3:0x6c
	v_ashrrev_i32_e32 v164, 31, v164
	v_lshrrev_b32_e32 v164, 26, v164
	v_add_u32_e32 v164, v169, v164
	v_and_b32_e32 v164, 0xc0, v164
	v_sub_u32_e32 v164, v169, v164
	v_lshrrev_b32_e32 v168, 1, v168
	v_ashrrev_i16_sdwa v164, v237, sext(v164) dst_sel:DWORD dst_unused:UNUSED_PAD src0_sel:DWORD src1_sel:BYTE_0
	v_and_b32_e32 v168, 32, v168
	v_bfe_i32 v164, v164, 0, 16
	v_add_lshl_u32 v168, v168, v164, 1
	v_add_u32_e32 v166, 0x2000, v166
	v_lshl_add_u32 v164, v172, 10, v168
	v_lshl_add_u32 v194, v173, 10, v168
	v_ashrrev_i32_e32 v168, 31, v166
	v_lshrrev_b32_e32 v168, 22, v168
	v_add_u32_e32 v168, v166, v168
	v_ashrrev_i32_e32 v168, 10, v168
	v_mul_i32_i24_e32 v169, 0x400, v168
	v_sub_u32_e32 v166, v166, v169
	v_lshrrev_b32_e32 v169, 4, v166
	v_bitop3_b32 v169, v169, v166, 32 bitop3:0x6c
	v_ashrrev_i32_e32 v166, 31, v166
	v_lshrrev_b32_e32 v166, 26, v166
	v_add_u32_e32 v166, v169, v166
	v_and_b32_e32 v166, 0xc0, v166
	v_sub_u32_e32 v166, v169, v166
	v_lshlrev_b32_e32 v168, 5, v168
	v_ashrrev_i16_sdwa v166, v237, sext(v166) dst_sel:DWORD dst_unused:UNUSED_PAD src0_sel:DWORD src1_sel:BYTE_0
	v_and_b32_e32 v168, 32, v168
	v_bfe_i32 v166, v166, 0, 16
	v_add_lshl_u32 v168, v168, v166, 1
	v_lshl_add_u32 v166, v174, 10, v168
	v_lshl_add_u32 v168, v175, 10, v168
	v_mov_b32_e32 v169, v195
	s_mov_b64 s[12:13], s[0:1]
	s_mov_b64 s[20:21], s[24:25]
.LBB0_963:
	s_ashr_i32 s29, s28, 31
	s_lshl_b64 s[28:29], s[28:29], 7
	s_add_u32 s30, s12, s28
	s_mov_b32 m0, s42
	s_addc_u32 s31, s13, s29
	ds_read_b128 v[180:183], v170 offset:16384
	ds_read_b128 v[184:187], v170 offset:17408
	ds_read_b128 v[196:199], v170 offset:18432
	ds_read_b128 v[200:203], v170 offset:19456
	ds_read_b128 v[216:219], v170 offset:20480
	ds_read_b128 v[220:223], v170 offset:21504
	ds_read_b128 v[224:227], v170 offset:22528
	ds_read_b128 v[228:231], v170 offset:23552
	global_load_lds_dwordx4 v171, s[30:31]
	s_mov_b32 m0, s43
	s_nop 0
	global_load_lds_dwordx4 v162, s[30:31]
	s_add_u32 s30, s12, 0x20000
	s_addc_u32 s31, s13, 0
	s_add_u32 s66, s30, s28
	s_addc_u32 s67, s31, s29
	s_mov_b32 m0, s44
	s_nop 0
	global_load_lds_dwordx4 v171, s[66:67]
	s_mov_b32 m0, s45
	s_nop 0
	global_load_lds_dwordx4 v162, s[66:67]
	s_add_u32 s66, s20, s28
	s_addc_u32 s67, s21, s29
	s_mov_b32 m0, s41
	s_nop 0
	global_load_lds_dwordx4 v164, s[66:67]
	s_mov_b32 m0, s46
	s_nop 0
	global_load_lds_dwordx4 v166, s[66:67]
	s_cmp_lg_u32 s100, 0
	s_waitcnt vmcnt(8)
	s_waitcnt lgkmcnt(0)
	s_barrier
	s_setprio 1
	s_waitcnt lgkmcnt(0)
	s_cbranch_scc1 .Lcz2_961
	v_mfma_f32_16x16x128_f8f6f4 v[94:97], v[18:25], v[180:187], v[94:97]
	v_mfma_f32_16x16x128_f8f6f4 v[90:93], v[26:33], v[180:187], v[90:93]
	v_mfma_f32_16x16x128_f8f6f4 v[78:81], v[18:25], v[196:203], v[78:81]
	v_mfma_f32_16x16x128_f8f6f4 v[74:77], v[26:33], v[196:203], v[74:77]
	v_mfma_f32_16x16x128_f8f6f4 v[188:191], v[18:25], v[216:223], v[62:65]
	v_mfma_f32_16x16x128_f8f6f4 v[248:251], v[26:33], v[216:223], v[58:61]
	v_mfma_f32_16x16x128_f8f6f4 v[242:245], v[18:25], v[224:231], v[46:49]
	v_mfma_f32_16x16x128_f8f6f4 v[208:211], v[26:33], v[224:231], v[42:45]
	s_setprio 0
	s_setprio 1
	v_mfma_f32_16x16x128_f8f6f4 v[86:89], v[2:9], v[180:187], v[86:89]
	v_mfma_f32_16x16x128_f8f6f4 v[82:85], v[10:17], v[180:187], v[82:85]
	v_mfma_f32_16x16x128_f8f6f4 v[70:73], v[2:9], v[196:203], v[70:73]
	v_mfma_f32_16x16x128_f8f6f4 v[66:69], v[10:17], v[196:203], v[66:69]
	v_mfma_f32_16x16x128_f8f6f4 v[212:215], v[2:9], v[216:223], v[54:57]
	v_mfma_f32_16x16x128_f8f6f4 v[216:219], v[10:17], v[216:223], v[50:53]
	v_mfma_f32_16x16x128_f8f6f4 v[220:223], v[2:9], v[224:231], v[38:41]
	v_mfma_f32_16x16x128_f8f6f4 v[224:227], v[10:17], v[224:231], v[34:37]
.Lcj2_961:
	s_setprio 0
	s_barrier
	v_add_u32_e32 v14, 0x18000, v167
	v_add_u32_e32 v30, 0x1c000, v167
	ds_read_b128 v[2:5], v14
	ds_read_b128 v[6:9], v14 offset:1024
	ds_read_b128 v[10:13], v14 offset:2048
	ds_read_b128 v[14:17], v14 offset:3072
	ds_read_b128 v[18:21], v30
	ds_read_b128 v[22:25], v30 offset:1024
	ds_read_b128 v[26:29], v30 offset:2048
	ds_read_b128 v[30:33], v30 offset:3072
	s_mov_b32 m0, s47
	v_lshl_add_u64 v[180:181], s[66:67], 0, v[194:195]
	ds_read_b128 v[34:37], v170 offset:32768
	ds_read_b128 v[38:41], v170 offset:33792
	ds_read_b128 v[42:45], v170 offset:34816
	ds_read_b128 v[46:49], v170 offset:35840
	ds_read_b128 v[50:53], v170 offset:36864
	ds_read_b128 v[54:57], v170 offset:37888
	ds_read_b128 v[58:61], v170 offset:38912
	ds_read_b128 v[62:65], v170 offset:39936
	global_load_lds_dwordx4 v[180:181], off
	v_lshl_add_u64 v[180:181], s[66:67], 0, v[168:169]
	s_mov_b32 m0, s48
	s_nop 0
	global_load_lds_dwordx4 v[180:181], off
	s_waitcnt vmcnt(8)
	s_waitcnt lgkmcnt(0)
	s_barrier
	s_setprio 1
	s_waitcnt lgkmcnt(0)
	v_mfma_f32_16x16x128_f8f6f4 v[146:149], v[2:9], v[34:41], v[146:149]
	v_mfma_f32_16x16x128_f8f6f4 v[158:161], v[10:17], v[34:41], v[158:161]
	v_mfma_f32_16x16x128_f8f6f4 v[142:145], v[2:9], v[42:49], v[142:145]
	v_mfma_f32_16x16x128_f8f6f4 v[138:141], v[10:17], v[42:49], v[138:141]
	v_mfma_f32_16x16x128_f8f6f4 v[126:129], v[2:9], v[50:57], v[126:129]
	v_mfma_f32_16x16x128_f8f6f4 v[122:125], v[10:17], v[50:57], v[122:125]
	v_mfma_f32_16x16x128_f8f6f4 v[110:113], v[2:9], v[58:65], v[110:113]
	v_mfma_f32_16x16x128_f8f6f4 v[106:109], v[10:17], v[58:65], v[106:109]
	s_setprio 0
	s_setprio 1
	v_mfma_f32_16x16x128_f8f6f4 v[154:157], v[18:25], v[34:41], v[154:157]
	v_mfma_f32_16x16x128_f8f6f4 v[150:153], v[26:33], v[34:41], v[150:153]
	v_mfma_f32_16x16x128_f8f6f4 v[134:137], v[18:25], v[42:49], v[134:137]
	v_mfma_f32_16x16x128_f8f6f4 v[130:133], v[26:33], v[42:49], v[130:133]
	v_mfma_f32_16x16x128_f8f6f4 v[118:121], v[18:25], v[50:57], v[118:121]
	v_mfma_f32_16x16x128_f8f6f4 v[114:117], v[26:33], v[50:57], v[114:117]
	v_mfma_f32_16x16x128_f8f6f4 v[102:105], v[18:25], v[58:65], v[102:105]
	v_mfma_f32_16x16x128_f8f6f4 v[98:101], v[26:33], v[58:65], v[98:101]
	s_setprio 0
	s_barrier
	s_add_u32 s61, s28, 0x80
	s_addc_u32 s62, s29, 0
	s_add_u32 s28, s12, s61
	s_mov_b32 m0, s49
	s_addc_u32 s29, s13, s62
	ds_read_b128 v[34:37], v170 offset:49152
	ds_read_b128 v[38:41], v170 offset:50176
	ds_read_b128 v[50:53], v170 offset:51200
	ds_read_b128 v[54:57], v170 offset:52224
	ds_read_b128 v[180:183], v170 offset:53248
	ds_read_b128 v[184:187], v170 offset:54272
	ds_read_b128 v[196:199], v170 offset:55296
	ds_read_b128 v[200:203], v170 offset:56320
	global_load_lds_dwordx4 v171, s[28:29]
	s_mov_b32 m0, s50
	s_nop 0
	global_load_lds_dwordx4 v162, s[28:29]
	s_add_u32 s28, s30, s61
	s_addc_u32 s29, s31, s62
	s_mov_b32 m0, s53
	s_nop 0
	global_load_lds_dwordx4 v171, s[28:29]
	s_mov_b32 m0, s54
	s_nop 0
	global_load_lds_dwordx4 v162, s[28:29]
	s_add_u32 s28, s20, s61
	s_addc_u32 s29, s21, s62
	s_mov_b32 m0, s51
	s_nop 0
	global_load_lds_dwordx4 v164, s[28:29]
	s_mov_b32 m0, s52
	s_nop 0
	global_load_lds_dwordx4 v166, s[28:29]
	s_waitcnt vmcnt(8)
	s_waitcnt lgkmcnt(0)
	s_barrier
	s_setprio 1
	s_waitcnt lgkmcnt(0)
	v_mfma_f32_16x16x128_f8f6f4 v[94:97], v[2:9], v[34:41], v[94:97]
	v_mfma_f32_16x16x128_f8f6f4 v[90:93], v[10:17], v[34:41], v[90:93]
	v_mfma_f32_16x16x128_f8f6f4 v[78:81], v[2:9], v[50:57], v[78:81]
	v_mfma_f32_16x16x128_f8f6f4 v[74:77], v[10:17], v[50:57], v[74:77]
	v_mfma_f32_16x16x128_f8f6f4 v[62:65], v[2:9], v[180:187], v[188:191]
	v_mfma_f32_16x16x128_f8f6f4 v[58:61], v[10:17], v[180:187], v[248:251]
	v_mfma_f32_16x16x128_f8f6f4 v[46:49], v[2:9], v[196:203], v[242:245]
	v_mfma_f32_16x16x128_f8f6f4 v[42:45], v[10:17], v[196:203], v[208:211]
	s_setprio 0
	s_setprio 1
	v_mfma_f32_16x16x128_f8f6f4 v[86:89], v[18:25], v[34:41], v[86:89]
	v_mfma_f32_16x16x128_f8f6f4 v[82:85], v[26:33], v[34:41], v[82:85]
	v_mfma_f32_16x16x128_f8f6f4 v[70:73], v[18:25], v[50:57], v[70:73]
	v_mfma_f32_16x16x128_f8f6f4 v[66:69], v[26:33], v[50:57], v[66:69]
	v_mfma_f32_16x16x128_f8f6f4 v[54:57], v[18:25], v[180:187], v[212:215]
	v_mfma_f32_16x16x128_f8f6f4 v[50:53], v[26:33], v[180:187], v[216:219]
	v_mfma_f32_16x16x128_f8f6f4 v[38:41], v[18:25], v[196:203], v[220:223]
	v_mfma_f32_16x16x128_f8f6f4 v[34:37], v[26:33], v[196:203], v[224:227]
	s_setprio 0
	s_barrier
	s_add_i32 s28, s60, 2
	s_add_u32 s26, s26, 0x100
	s_addc_u32 s27, s27, 0
	s_cmp_ge_i32 s60, s19
	s_cbranch_scc1 .LBB0_966
	s_mov_b32 s60, s28
	s_branch .LBB0_961
.Lcz1_961:
	v_mfma_f32_16x16x128_f8f6f4 v[146:149], v[18:25], v[180:187], 0
	v_mfma_f32_16x16x128_f8f6f4 v[158:161], v[26:33], v[180:187], 0
	v_mfma_f32_16x16x128_f8f6f4 v[142:145], v[18:25], v[216:223], 0
	v_mfma_f32_16x16x128_f8f6f4 v[138:141], v[26:33], v[216:223], 0
	v_mfma_f32_16x16x128_f8f6f4 v[126:129], v[18:25], v[224:231], 0
	v_mfma_f32_16x16x128_f8f6f4 v[122:125], v[26:33], v[224:231], 0
	v_mfma_f32_16x16x128_f8f6f4 v[110:113], v[18:25], v[196:203], 0
	v_mfma_f32_16x16x128_f8f6f4 v[106:109], v[26:33], v[196:203], 0
	s_setprio 0
	s_setprio 1
	v_mfma_f32_16x16x128_f8f6f4 v[154:157], v[2:9], v[180:187], 0
	v_mfma_f32_16x16x128_f8f6f4 v[150:153], v[10:17], v[180:187], 0
	v_mfma_f32_16x16x128_f8f6f4 v[134:137], v[2:9], v[216:223], 0
	v_mfma_f32_16x16x128_f8f6f4 v[130:133], v[10:17], v[216:223], 0
	v_mfma_f32_16x16x128_f8f6f4 v[118:121], v[2:9], v[224:231], 0
	v_mfma_f32_16x16x128_f8f6f4 v[114:117], v[10:17], v[224:231], 0
	v_mfma_f32_16x16x128_f8f6f4 v[102:105], v[2:9], v[196:203], 0
	v_mfma_f32_16x16x128_f8f6f4 v[98:101], v[10:17], v[196:203], 0
	s_branch .Lcj1_961
.Lcz2_961:
	v_mfma_f32_16x16x128_f8f6f4 v[94:97], v[18:25], v[180:187], 0
	v_mfma_f32_16x16x128_f8f6f4 v[90:93], v[26:33], v[180:187], 0
	v_mfma_f32_16x16x128_f8f6f4 v[78:81], v[18:25], v[196:203], 0
	v_mfma_f32_16x16x128_f8f6f4 v[74:77], v[26:33], v[196:203], 0
	v_mfma_f32_16x16x128_f8f6f4 v[188:191], v[18:25], v[216:223], 0
	v_mfma_f32_16x16x128_f8f6f4 v[248:251], v[26:33], v[216:223], 0
	v_mfma_f32_16x16x128_f8f6f4 v[242:245], v[18:25], v[224:231], 0
	v_mfma_f32_16x16x128_f8f6f4 v[208:211], v[26:33], v[224:231], 0
	s_setprio 0
	s_setprio 1
	v_mfma_f32_16x16x128_f8f6f4 v[86:89], v[2:9], v[180:187], 0
	v_mfma_f32_16x16x128_f8f6f4 v[82:85], v[10:17], v[180:187], 0
	v_mfma_f32_16x16x128_f8f6f4 v[70:73], v[2:9], v[196:203], 0
	v_mfma_f32_16x16x128_f8f6f4 v[66:69], v[10:17], v[196:203], 0
	v_mfma_f32_16x16x128_f8f6f4 v[212:215], v[2:9], v[216:223], 0
	v_mfma_f32_16x16x128_f8f6f4 v[216:219], v[10:17], v[216:223], 0
	v_mfma_f32_16x16x128_f8f6f4 v[220:223], v[2:9], v[224:231], 0
	v_mfma_f32_16x16x128_f8f6f4 v[224:227], v[10:17], v[224:231], 0
	s_mov_b32 s100, 0
	s_branch .Lcj2_961

.LBB0_1046:
	s_mov_b32 s55, 22
	s_cmp_lt_i32 s55, 1
	s_cbranch_scc1 .LBB0_1054
	v_mov_b32_e32 v236, 0xf149f2ca
	v_mov_b32_e32 v252, 0x7f800000
	v_mov_b32_e32 v1, -1
	v_mov_b32_e32 v193, 0x260
	v_mov_b64_e32 v[246:247], 0x200
	v_mov_b32_e32 v192, 0x358637bd
	s_mov_b32 s56, 2
	s_mov_b64 s[20:21], 0x58080
	s_mov_b32 s100, 1
.LBB0_1048:
	v_add_u32_e32 v66, 0x10000, v131
	ds_read_b128 v[136:139], v66
	ds_read_b128 v[140:143], v66 offset:1024
	ds_read_b128 v[144:147], v66 offset:2048
	ds_read_b128 v[148:151], v66 offset:3072
	v_add_u32_e32 v66, 0x14000, v131
	ds_read_b128 v[152:155], v66
	ds_read_b128 v[156:159], v66 offset:1024
	ds_read_b128 v[160:163], v66 offset:2048
	ds_read_b128 v[164:167], v66 offset:3072
	s_add_i32 m0, s31, 0xc000
	s_add_i32 s57, s31, 0xe000
	s_cmp_eq_u32 s55, s56
	s_cselect_b64 s[22:23], -1, 0
	v_lshl_add_u64 v[66:67], s[0:1], 0, v[194:195]
	v_lshl_add_u64 v[66:67], v[66:67], 0, s[20:21]
	v_mov_b32_e32 v133, v195
	ds_read_b128 v[168:171], v135
	ds_read_b128 v[172:175], v135 offset:1024
	ds_read_b128 v[176:179], v135 offset:2048
	ds_read_b128 v[180:183], v135 offset:3072
	ds_read_b128 v[184:187], v135 offset:4096
	ds_read_b128 v[188:191], v135 offset:5120
	ds_read_b128 v[196:199], v135 offset:6144
	ds_read_b128 v[200:203], v135 offset:7168
	global_load_lds_dwordx4 v[66:67], off
	v_lshl_add_u64 v[66:67], s[0:1], 0, v[132:133]
	v_lshl_add_u64 v[66:67], v[66:67], 0, s[20:21]
	s_mov_b32 m0, s57
	s_nop 0
	global_load_lds_dwordx4 v[66:67], off
	s_cmp_lg_u32 s100, 0
	s_waitcnt vmcnt(8)
	s_waitcnt lgkmcnt(0)
	s_barrier
	s_setprio 1
	s_waitcnt lgkmcnt(0)
	s_cbranch_scc1 .Lcz1_1048
	v_mfma_f32_16x16x128_f8f6f4 v[126:129], v[136:143], v[168:175], v[126:129]
	v_mfma_f32_16x16x128_f8f6f4 v[122:125], v[144:151], v[168:175], v[122:125]
	v_mfma_f32_16x16x128_f8f6f4 v[110:113], v[136:143], v[176:183], v[110:113]
	v_mfma_f32_16x16x128_f8f6f4 v[106:109], v[144:151], v[176:183], v[106:109]
	v_mfma_f32_16x16x128_f8f6f4 v[208:211], v[136:143], v[184:191], v[94:97]
	v_mfma_f32_16x16x128_f8f6f4 v[212:215], v[144:151], v[184:191], v[90:93]
	v_mfma_f32_16x16x128_f8f6f4 v[216:219], v[136:143], v[196:203], v[78:81]
	v_mfma_f32_16x16x128_f8f6f4 v[220:223], v[144:151], v[196:203], v[74:77]
	s_setprio 0
	s_setprio 1
	v_mfma_f32_16x16x128_f8f6f4 v[118:121], v[152:159], v[168:175], v[118:121]
	v_mfma_f32_16x16x128_f8f6f4 v[114:117], v[160:167], v[168:175], v[114:117]
	v_mfma_f32_16x16x128_f8f6f4 v[102:105], v[152:159], v[176:183], v[102:105]
	v_mfma_f32_16x16x128_f8f6f4 v[98:101], v[160:167], v[176:183], v[98:101]
	v_mfma_f32_16x16x128_f8f6f4 v[168:171], v[152:159], v[184:191], v[86:89]
	v_mfma_f32_16x16x128_f8f6f4 v[172:175], v[160:167], v[184:191], v[82:85]
	v_mfma_f32_16x16x128_f8f6f4 v[176:179], v[152:159], v[196:203], v[70:73]
	v_mfma_f32_16x16x128_f8f6f4 v[180:183], v[160:167], v[196:203], v[10:13]
.Lcj1_1048:
	s_setprio 0
	s_barrier
	s_and_b64 s[58:59], s[22:23], exec
	s_cselect_b32 s62, 0, s56
	s_and_b64 s[22:23], s[4:5], s[22:23]
	s_and_b64 s[22:23], s[22:23], exec
	s_cselect_b32 s7, s19, s7
	s_cselect_b32 s6, s18, s6
	s_cselect_b32 s1, s17, s1
	s_cselect_b32 s0, s16, s0
	s_lshl_b64 s[58:59], s[62:63], 7
	s_add_u32 s22, s6, s58
	s_mov_b32 m0, s36
	s_addc_u32 s23, s7, s59
	ds_read_b128 v[66:69], v135 offset:16384
	ds_read_b128 v[70:73], v135 offset:17408
	ds_read_b128 v[74:77], v135 offset:18432
	ds_read_b128 v[78:81], v135 offset:19456
	ds_read_b128 v[82:85], v135 offset:20480
	ds_read_b128 v[86:89], v135 offset:21504
	ds_read_b128 v[90:93], v135 offset:22528
	ds_read_b128 v[94:97], v135 offset:23552
	global_load_lds_dwordx4 v130, s[22:23]
	s_mov_b32 m0, s37
	s_nop 0
	global_load_lds_dwordx4 v134, s[22:23]
	s_add_u32 s22, s6, 0x58000
	s_addc_u32 s23, s7, 0
	s_add_u32 s60, s22, s58
	s_addc_u32 s61, s23, s59
	s_mov_b32 m0, s38
	s_add_u32 s58, s0, s58
	global_load_lds_dwordx4 v130, s[60:61]
	s_mov_b32 m0, s39
	s_addc_u32 s59, s1, s59
	global_load_lds_dwordx4 v134, s[60:61]
	s_mov_b32 m0, s31
	s_nop 0
	global_load_lds_dwordx4 v194, s[58:59]
	s_mov_b32 m0, s40
	s_nop 0
	global_load_lds_dwordx4 v132, s[58:59]
	s_cmp_lg_u32 s100, 0
	s_waitcnt vmcnt(8)
	s_waitcnt lgkmcnt(0)
	s_barrier
	s_setprio 1
	s_waitcnt lgkmcnt(0)
	s_cbranch_scc1 .Lcz2_1048
	v_mfma_f32_16x16x128_f8f6f4 v[62:65], v[136:143], v[66:73], v[62:65]
	v_mfma_f32_16x16x128_f8f6f4 v[58:61], v[144:151], v[66:73], v[58:61]
	v_mfma_f32_16x16x128_f8f6f4 v[228:231], v[144:151], v[90:97], v[228:231]
	v_mfma_f32_16x16x128_f8f6f4 v[184:187], v[136:143], v[74:81], v[46:49]
	v_mfma_f32_16x16x128_f8f6f4 v[188:191], v[144:151], v[74:81], v[42:45]
	v_mfma_f32_16x16x128_f8f6f4 v[196:199], v[136:143], v[82:89], v[30:33]
	v_mfma_f32_16x16x128_f8f6f4 v[200:203], v[144:151], v[82:89], v[26:29]
	v_mfma_f32_16x16x128_f8f6f4 v[224:227], v[136:143], v[90:97], v[14:17]
	s_setprio 0
	s_setprio 1
	v_mfma_f32_16x16x128_f8f6f4 v[54:57], v[152:159], v[66:73], v[54:57]
	v_mfma_f32_16x16x128_f8f6f4 v[50:53], v[160:167], v[66:73], v[50:53]
	v_mfma_f32_16x16x128_f8f6f4 v[242:245], v[152:159], v[74:81], v[38:41]
	v_mfma_f32_16x16x128_f8f6f4 v[248:251], v[160:167], v[74:81], v[34:37]
	v_mfma_f32_16x16x128_f8f6f4 v[232:235], v[152:159], v[82:89], v[22:25]
	v_mfma_f32_16x16x128_f8f6f4 v[238:241], v[160:167], v[82:89], v[18:21]
	v_mfma_f32_16x16x128_f8f6f4 v[204:207], v[152:159], v[90:97], v[6:9]
	v_mfma_f32_16x16x128_f8f6f4 v[66:69], v[160:167], v[90:97], v[2:5]
.Lcj2_1048:
	s_setprio 0
	s_barrier
	v_add_u32_e32 v10, 0x18000, v131
	s_nop 3
	ds_read_b128 v[2:5], v10
	ds_read_b128 v[6:9], v10 offset:1024
	ds_read_b128 v[18:21], v10 offset:2048
	ds_read_b128 v[22:25], v10 offset:3072
	v_add_u32_e32 v10, 0x1c000, v131
	ds_read_b128 v[136:139], v10
	ds_read_b128 v[140:143], v10 offset:1024
	ds_read_b128 v[144:147], v10 offset:2048
	ds_read_b128 v[148:151], v10 offset:3072
	s_add_u32 s58, s58, 0x58000
	s_addc_u32 s59, s59, 0
	s_mov_b32 m0, s41
	ds_read_b128 v[10:13], v135 offset:32768
	ds_read_b128 v[14:17], v135 offset:33792
	ds_read_b128 v[26:29], v135 offset:34816
	ds_read_b128 v[30:33], v135 offset:35840
	ds_read_b128 v[34:37], v135 offset:36864
	ds_read_b128 v[38:41], v135 offset:37888
	ds_read_b128 v[42:45], v135 offset:38912
	ds_read_b128 v[46:49], v135 offset:39936
	global_load_lds_dwordx4 v194, s[58:59]
	s_mov_b32 m0, s42
	s_nop 0
	global_load_lds_dwordx4 v132, s[58:59]
	s_waitcnt vmcnt(8)
	s_waitcnt lgkmcnt(0)
	s_barrier
	s_setprio 1
	s_waitcnt lgkmcnt(0)
	v_mfma_f32_16x16x128_f8f6f4 v[126:129], v[2:9], v[10:17], v[126:129]
	v_mfma_f32_16x16x128_f8f6f4 v[122:125], v[18:25], v[10:17], v[122:125]
	v_mfma_f32_16x16x128_f8f6f4 v[110:113], v[2:9], v[26:33], v[110:113]
	v_mfma_f32_16x16x128_f8f6f4 v[106:109], v[18:25], v[26:33], v[106:109]
	v_mfma_f32_16x16x128_f8f6f4 v[94:97], v[2:9], v[34:41], v[208:211]
	v_mfma_f32_16x16x128_f8f6f4 v[90:93], v[18:25], v[34:41], v[212:215]
	v_mfma_f32_16x16x128_f8f6f4 v[78:81], v[2:9], v[42:49], v[216:219]
	v_mfma_f32_16x16x128_f8f6f4 v[74:77], v[18:25], v[42:49], v[220:223]
	s_setprio 0
	s_setprio 1
	v_mfma_f32_16x16x128_f8f6f4 v[118:121], v[136:143], v[10:17], v[118:121]
	v_mfma_f32_16x16x128_f8f6f4 v[114:117], v[144:151], v[10:17], v[114:117]
	v_mfma_f32_16x16x128_f8f6f4 v[102:105], v[136:143], v[26:33], v[102:105]
	v_mfma_f32_16x16x128_f8f6f4 v[98:101], v[144:151], v[26:33], v[98:101]
	v_mfma_f32_16x16x128_f8f6f4 v[86:89], v[136:143], v[34:41], v[168:171]
	v_mfma_f32_16x16x128_f8f6f4 v[82:85], v[144:151], v[34:41], v[172:175]
	v_mfma_f32_16x16x128_f8f6f4 v[70:73], v[136:143], v[42:49], v[176:179]
	v_mfma_f32_16x16x128_f8f6f4 v[10:13], v[144:151], v[42:49], v[180:183]
	s_setprio 0
	s_barrier
	s_or_b32 s62, s62, 1
	s_lshl_b64 s[58:59], s[62:63], 7
	s_add_u32 s60, s6, s58
	s_mov_b32 m0, s43
	s_addc_u32 s61, s7, s59
	ds_read_b128 v[34:37], v135 offset:49152
	ds_read_b128 v[38:41], v135 offset:50176
	ds_read_b128 v[152:155], v135 offset:51200
	ds_read_b128 v[156:159], v135 offset:52224
	ds_read_b128 v[160:163], v135 offset:53248
	ds_read_b128 v[164:167], v135 offset:54272
	ds_read_b128 v[168:171], v135 offset:55296
	ds_read_b128 v[172:175], v135 offset:56320
	global_load_lds_dwordx4 v130, s[60:61]
	s_mov_b32 m0, s44
	s_add_u32 s22, s22, s58
	global_load_lds_dwordx4 v134, s[60:61]
	s_addc_u32 s23, s23, s59
	s_mov_b32 m0, s47
	s_nop 0
	global_load_lds_dwordx4 v130, s[22:23]
	s_mov_b32 m0, s48
	s_nop 0
	global_load_lds_dwordx4 v134, s[22:23]
	s_add_u32 s22, s0, s58
	s_addc_u32 s23, s1, s59
	s_mov_b32 m0, s45
	s_nop 0
	global_load_lds_dwordx4 v194, s[22:23]
	s_mov_b32 m0, s46
	s_nop 0
	global_load_lds_dwordx4 v132, s[22:23]
	s_waitcnt vmcnt(8)
	s_waitcnt lgkmcnt(0)
	s_barrier
	s_setprio 1
	s_waitcnt lgkmcnt(0)
	v_mfma_f32_16x16x128_f8f6f4 v[62:65], v[2:9], v[34:41], v[62:65]
	v_mfma_f32_16x16x128_f8f6f4 v[58:61], v[18:25], v[34:41], v[58:61]
	v_mfma_f32_16x16x128_f8f6f4 v[46:49], v[2:9], v[152:159], v[184:187]
	v_mfma_f32_16x16x128_f8f6f4 v[42:45], v[18:25], v[152:159], v[188:191]
	v_mfma_f32_16x16x128_f8f6f4 v[30:33], v[2:9], v[160:167], v[196:199]
	v_mfma_f32_16x16x128_f8f6f4 v[26:29], v[18:25], v[160:167], v[200:203]
	v_mfma_f32_16x16x128_f8f6f4 v[14:17], v[2:9], v[168:175], v[224:227]
	v_mfma_f32_16x16x128_f8f6f4 v[228:231], v[18:25], v[168:175], v[228:231]
	s_setprio 0
	s_setprio 1
	v_mfma_f32_16x16x128_f8f6f4 v[54:57], v[136:143], v[34:41], v[54:57]
	v_mfma_f32_16x16x128_f8f6f4 v[50:53], v[144:151], v[34:41], v[50:53]
	v_mfma_f32_16x16x128_f8f6f4 v[38:41], v[136:143], v[152:159], v[242:245]
	v_mfma_f32_16x16x128_f8f6f4 v[34:37], v[144:151], v[152:159], v[248:251]
	v_mfma_f32_16x16x128_f8f6f4 v[22:25], v[136:143], v[160:167], v[232:235]
	v_mfma_f32_16x16x128_f8f6f4 v[18:21], v[144:151], v[160:167], v[238:241]
	v_mfma_f32_16x16x128_f8f6f4 v[6:9], v[136:143], v[168:175], v[204:207]
	v_mfma_f32_16x16x128_f8f6f4 v[2:5], v[144:151], v[168:175], v[66:69]
	s_setprio 0
	s_barrier
	s_add_i32 s22, s56, 2
	s_add_u32 s20, s20, 0x100
	s_addc_u32 s21, s21, 0
	s_cmp_ge_i32 s56, s55
	s_mov_b32 s56, s22
	s_cbranch_scc0 .LBB0_1048
	s_branch .Lcsk_1048
.Lcz1_1048:
	v_mfma_f32_16x16x128_f8f6f4 v[126:129], v[136:143], v[168:175], 0
	v_mfma_f32_16x16x128_f8f6f4 v[122:125], v[144:151], v[168:175], 0
	v_mfma_f32_16x16x128_f8f6f4 v[110:113], v[136:143], v[176:183], 0
	v_mfma_f32_16x16x128_f8f6f4 v[106:109], v[144:151], v[176:183], 0
	v_mfma_f32_16x16x128_f8f6f4 v[208:211], v[136:143], v[184:191], 0
	v_mfma_f32_16x16x128_f8f6f4 v[212:215], v[144:151], v[184:191], 0
	v_mfma_f32_16x16x128_f8f6f4 v[216:219], v[136:143], v[196:203], 0
	v_mfma_f32_16x16x128_f8f6f4 v[220:223], v[144:151], v[196:203], 0
	s_setprio 0
	s_setprio 1
	v_mfma_f32_16x16x128_f8f6f4 v[118:121], v[152:159], v[168:175], 0
	v_mfma_f32_16x16x128_f8f6f4 v[114:117], v[160:167], v[168:175], 0
	v_mfma_f32_16x16x128_f8f6f4 v[102:105], v[152:159], v[176:183], 0
	v_mfma_f32_16x16x128_f8f6f4 v[98:101], v[160:167], v[176:183], 0
	v_mfma_f32_16x16x128_f8f6f4 v[168:171], v[152:159], v[184:191], 0
	v_mfma_f32_16x16x128_f8f6f4 v[172:175], v[160:167], v[184:191], 0
	v_mfma_f32_16x16x128_f8f6f4 v[176:179], v[152:159], v[196:203], 0
	v_mfma_f32_16x16x128_f8f6f4 v[180:183], v[160:167], v[196:203], 0
	s_branch .Lcj1_1048
.Lcz2_1048:
	v_mfma_f32_16x16x128_f8f6f4 v[62:65], v[136:143], v[66:73], 0
	v_mfma_f32_16x16x128_f8f6f4 v[58:61], v[144:151], v[66:73], 0
	v_mfma_f32_16x16x128_f8f6f4 v[228:231], v[144:151], v[90:97], 0
	v_mfma_f32_16x16x128_f8f6f4 v[184:187], v[136:143], v[74:81], 0
	v_mfma_f32_16x16x128_f8f6f4 v[188:191], v[144:151], v[74:81], 0
	v_mfma_f32_16x16x128_f8f6f4 v[196:199], v[136:143], v[82:89], 0
	v_mfma_f32_16x16x128_f8f6f4 v[200:203], v[144:151], v[82:89], 0
	v_mfma_f32_16x16x128_f8f6f4 v[224:227], v[136:143], v[90:97], 0
	s_setprio 0
	s_setprio 1
	v_mfma_f32_16x16x128_f8f6f4 v[54:57], v[152:159], v[66:73], 0
	v_mfma_f32_16x16x128_f8f6f4 v[50:53], v[160:167], v[66:73], 0
	v_mfma_f32_16x16x128_f8f6f4 v[242:245], v[152:159], v[74:81], 0
	v_mfma_f32_16x16x128_f8f6f4 v[248:251], v[160:167], v[74:81], 0
	v_mfma_f32_16x16x128_f8f6f4 v[232:235], v[152:159], v[82:89], 0
	v_mfma_f32_16x16x128_f8f6f4 v[238:241], v[160:167], v[82:89], 0
	v_mfma_f32_16x16x128_f8f6f4 v[204:207], v[152:159], v[90:97], 0
	v_mfma_f32_16x16x128_f8f6f4 v[66:69], v[160:167], v[90:97], 0
	s_mov_b32 s100, 0
	s_branch .Lcj2_1048
.Lcsk_1048:
	v_mov_b32_e32 v206, v192
	v_mov_b32_e32 v207, v193
	v_mov_b32_e32 v238, v1
	v_mov_b64_e32 v[240:241], 0x1ff
	s_and_b64 vcc, exec, s[14:15]
	s_cbranch_vccz .LBB0_1051

	.amdhsa_kernel _Z6mk_fwd4Args
		.amdhsa_group_segment_fixed_size 0
		.amdhsa_private_segment_fixed_size 0
		.amdhsa_kernarg_size 400
		.amdhsa_user_sgpr_count 2
		.amdhsa_user_sgpr_dispatch_ptr 0
		.amdhsa_user_sgpr_queue_ptr 0
		.amdhsa_user_sgpr_kernarg_segment_ptr 1
		.amdhsa_user_sgpr_dispatch_id 0
		.amdhsa_user_sgpr_kernarg_preload_length 0
		.amdhsa_user_sgpr_kernarg_preload_offset 0
		.amdhsa_user_sgpr_private_segment_size 0
		.amdhsa_uses_dynamic_stack 0
		.amdhsa_enable_private_segment 0
		.amdhsa_system_sgpr_workgroup_id_x 1
		.amdhsa_system_sgpr_workgroup_id_y 0
		.amdhsa_system_sgpr_workgroup_id_z 0
		.amdhsa_system_sgpr_workgroup_info 0
		.amdhsa_system_vgpr_workitem_id 0
		.amdhsa_next_free_vgpr 256
		.amdhsa_next_free_sgpr 102
		.amdhsa_accum_offset 256
		.amdhsa_reserve_vcc 1
		.amdhsa_float_round_mode_32 0
		.amdhsa_float_round_mode_16_64 0
		.amdhsa_float_denorm_mode_32 3
		.amdhsa_float_denorm_mode_16_64 3
		.amdhsa_dx10_clamp 1
		.amdhsa_ieee_mode 1
		.amdhsa_fp16_overflow 0
		.amdhsa_tg_split 0
		.amdhsa_exception_fp_ieee_invalid_op 0
		.amdhsa_exception_fp_denorm_src 0
		.amdhsa_exception_fp_ieee_div_zero 0
		.amdhsa_exception_fp_ieee_overflow 0
		.amdhsa_exception_fp_ieee_underflow 0
		.amdhsa_exception_fp_ieee_inexact 0
		.amdhsa_exception_int_div_zero 0
	.end_amdhsa_kernel

.Lfunc_end0:
	.size	_Z6mk_fwd4Args, .Lfunc_end0-_Z6mk_fwd4Args
	.set _Z6mk_fwd4Args.num_vgpr, 256
	.set _Z6mk_fwd4Args.num_agpr, 0
	.set _Z6mk_fwd4Args.numbered_sgpr, 102
	.set _Z6mk_fwd4Args.num_named_barrier, 0
	.set _Z6mk_fwd4Args.private_seg_size, 0
	.set _Z6mk_fwd4Args.uses_vcc, 1
	.set _Z6mk_fwd4Args.uses_flat_scratch, 0
	.set _Z6mk_fwd4Args.has_dyn_sized_stack, 0
	.set _Z6mk_fwd4Args.has_recursion, 0
	.set _Z6mk_fwd4Args.has_indirect_call, 0

amdhsa.kernels:
  - .agpr_count:     0
    .args:
      - .offset:         0
        .size:           144
        .value_kind:     by_value
      - .offset:         144
        .size:           4
        .value_kind:     hidden_block_count_x
      - .offset:         148
        .size:           4
        .value_kind:     hidden_block_count_y
      - .offset:         152
        .size:           4
        .value_kind:     hidden_block_count_z
      - .offset:         156
        .size:           2
        .value_kind:     hidden_group_size_x
      - .offset:         158
        .size:           2
        .value_kind:     hidden_group_size_y
      - .offset:         160
        .size:           2
        .value_kind:     hidden_group_size_z
      - .offset:         162
        .size:           2
        .value_kind:     hidden_remainder_x
      - .offset:         164
        .size:           2
        .value_kind:     hidden_remainder_y
      - .offset:         166
        .size:           2
        .value_kind:     hidden_remainder_z
      - .offset:         184
        .size:           8
        .value_kind:     hidden_global_offset_x
      - .offset:         192
        .size:           8
        .value_kind:     hidden_global_offset_y
      - .offset:         200
        .size:           8
        .value_kind:     hidden_global_offset_z
      - .offset:         208
        .size:           2
        .value_kind:     hidden_grid_dims
      - .offset:         264
        .size:           4
        .value_kind:     hidden_dynamic_lds_size
    .group_segment_fixed_size: 0
    .kernarg_segment_align: 8
    .kernarg_segment_size: 400
    .language:       OpenCL C
    .language_version:
      - 2
      - 0
    .max_flat_workgroup_size: 512
    .name:           _Z6mk_fwd4Args
    .private_segment_fixed_size: 0
    .sgpr_count:     108
    .sgpr_spill_count: 179
    .symbol:         _Z6mk_fwd4Args.kd
    .uniform_work_group_size: 1
    .uses_dynamic_stack: false
    .vgpr_count:     256
    .vgpr_spill_count: 0
    .wavefront_size: 64
